# static priority: one s_setprio 1 for waves 4-7 per GEMM phase (P2,9,11,12,14,20,23,24), per-segment priority flips deleted
# speedup vs baseline: 1.0035x; 1.0020x over previous
.LBB0_284:
.LBB0_285:
	s_cmp_gt_i32 s40, 2
	s_cselect_b64 s[2:3], -1, 0
	s_cmp_lt_i32 s41, 3
	s_cselect_b64 s[4:5], -1, 0
	s_or_b64 s[2:3], s[2:3], s[4:5]
	s_and_b64 vcc, exec, s[2:3]
	s_cbranch_vccnz .LBB0_481
	s_cmp_ge_u32 s27, 4
	s_cbranch_scc0 .Lsp_2
	s_setprio 1
.Lsp_2:
	s_add_u32 s20, s38, 0x1000000
	s_addc_u32 s21, s39, 0
	v_mov_b32_e32 v7, v0
	s_movk_i32 s8, 0x800
	v_readfirstlane_b32 s3, v7
	s_movk_i32 s2, 0x800
	s_movk_i32 s6, 0x800
	s_cmpk_gt_i32 s26, 0x83f
	s_cbranch_scc1 .LBB0_303
	v_bfe_i32 v3, v7, 27, 1
	v_lshlrev_b32_e32 v1, 4, v7
	v_lshrrev_b32_e32 v3, 22, v3
	v_add_u32_e32 v3, v1, v3
	v_and_b32_e32 v3, 0xfffffc00, v3
	v_sub_u32_e32 v1, v1, v3
	v_ashrrev_i32_e32 v2, 31, v7
	v_lshrrev_b32_e32 v3, 4, v1
	v_lshrrev_b32_e32 v2, 26, v2
	v_bitop3_b32 v1, v3, v1, 32 bitop3:0x6c
	s_add_u32 s4, s38, 0x2a400000
	v_add_u32_e32 v2, v7, v2
	v_ashrrev_i32_e32 v4, 31, v1
	s_addc_u32 s5, s39, 0
	v_ashrrev_i32_e32 v2, 6, v2
	v_lshrrev_b32_e32 v4, 26, v4
	s_ashr_i32 s18, s26, 31
	v_lshlrev_b32_e32 v3, 3, v2
	v_add_u32_e32 v5, v1, v4
	s_lshr_b32 s11, s18, 29
	v_and_b32_e32 v3, -16, v3
	v_ashrrev_i32_e32 v4, 6, v5
	s_add_i32 s11, s26, s11
	s_ashr_i32 s9, s3, 6
	v_add_u32_e32 v6, v4, v3
	v_and_b32_e32 v10, 3, v4
	s_mov_b32 s7, 0x7fffffe0
	s_ashr_i32 s12, s11, 3
	s_and_b32 s11, s11, -8
	s_ashr_i32 s10, s3, 8
	v_and_or_b32 v10, v6, s7, v10
	s_lshl_b32 s16, s2, 7
	s_lshl_b32 s17, s6, 7
	s_lshl_b32 s7, s9, 10
	s_lshl_b32 s13, s2, 8
	s_sub_i32 s11, s26, s11
	s_cmp_lt_i32 s11, 0
	s_movk_i32 s19, 0x109
	s_cselect_b32 s14, s19, 0x108
	s_mul_i32 s11, s11, s14
	s_add_i32 s11, s11, s12
	s_ashr_i32 s12, s11, 31
	s_lshr_b32 s12, s12, 25
	s_add_i32 s12, s11, s12
	v_and_b32_e32 v5, 0xc0, v5
	s_ashr_i32 s14, s12, 7
	v_sub_u32_e32 v1, v1, v5
	v_mov_b32_e32 v5, 1
	s_lshl_b32 s22, s14, 3
	v_ashrrev_i16_sdwa v1, v5, sext(v1) dst_sel:DWORD dst_unused:UNUSED_PAD src0_sel:DWORD src1_sel:BYTE_0
	s_sub_i32 s14, 0x84, s22
	v_bfe_i32 v5, v1, 0, 16
	v_lshlrev_b32_e32 v1, 1, v6
	v_lshrrev_b32_e32 v9, 2, v6
	s_min_u32 s23, s14, 8
	s_and_b32 s12, s12, 0xffffff80
	v_and_b32_e32 v1, 24, v1
	v_and_b32_e32 v9, 4, v9
	s_sub_i32 s11, s11, s12
	v_cvt_f32_ubyte0_e32 v11, s23
	v_or3_b32 v9, v10, v9, v1
	v_cvt_f32_i32_e32 v10, s11
	v_rcp_iflag_f32_e32 v12, v11
	v_lshlrev_b32_e32 v3, 5, v2
	v_and_b32_e32 v3, 32, v3
	v_add_u32_e32 v8, v3, v5
	v_mul_lo_u32 v6, v6, s2
	v_mul_lo_u32 v9, v9, s6
	v_add_lshl_u32 v1, v8, v6, 1
	v_add_lshl_u32 v134, v9, v8, 1
	v_mul_f32_e32 v8, v10, v12
	v_trunc_f32_e32 v8, v8
	v_fma_f32 v9, -v8, v11, v10
	v_cvt_i32_f32_e32 v8, v8
	s_ashr_i32 s12, s11, 30
	s_or_b32 s12, s12, 1
	v_cmp_ge_f32_e64 s[14:15], |v9|, v11
	s_and_b64 s[14:15], s[14:15], exec
	s_cselect_b32 s12, s12, 0
	v_readfirstlane_b32 s14, v8
	s_add_i32 s14, s14, s12
	s_mul_i32 s12, s14, s23
	s_sub_i32 s11, s11, s12
	s_sext_i32_i8 s11, s11
	s_add_i32 s12, s22, s11
	s_sext_i32_i8 s65, s14
	s_add_i32 s22, s7, 0
	s_lshl_b32 s70, s65, 20
	s_add_i32 s23, s22, 0x10000
	v_add_u32_e32 v9, s70, v134
	s_mov_b32 m0, s23
	s_add_i32 s28, s22, 0x12000
	global_load_lds_dwordx4 v9, s[20:21]
	v_add_u32_e32 v8, s17, v9
	s_mov_b32 m0, s28
	v_lshl_add_u32 v135, s6, 8, v134
	s_add_i32 s29, s22, 0x14000
	global_load_lds_dwordx4 v8, s[20:21]
	v_add_u32_e32 v8, s70, v135
	s_mov_b32 m0, s29
	s_add_i32 s30, s22, 0x16000
	s_lshl_b32 s71, s12, 20
	global_load_lds_dwordx4 v8, s[20:21]
	v_add_u32_e32 v10, s17, v8
	s_mov_b32 m0, s30
	s_add_i32 s31, s22, 0x2000
	global_load_lds_dwordx4 v10, s[20:21]
	v_add_u32_e32 v10, s71, v1
	s_mov_b32 m0, s22
	v_add_u32_e32 v136, s13, v1
	global_load_lds_dwordx4 v10, s[4:5]
	v_add_u32_e32 v10, s16, v10
	s_mov_b32 m0, s31
	s_add_i32 s35, s22, 0x4000
	global_load_lds_dwordx4 v10, s[4:5]
	v_add_u32_e32 v10, s71, v136
	s_mov_b32 m0, s35
	s_add_i32 s44, s22, 0x6000
	global_load_lds_dwordx4 v10, s[4:5]
	v_add_u32_e32 v10, s16, v10
	s_mov_b32 m0, s44
	s_cmp_eq_u32 s10, 1
	global_load_lds_dwordx4 v10, s[4:5]
	s_cselect_b64 s[6:7], -1, 0
	s_cmp_lg_u32 s10, 1
	s_mov_b32 s45, 0
	s_cbranch_scc1 .LBB0_289
	s_barrier

.LBB0_294:
	s_andn2_b64 vcc, exec, s[8:9]
	s_waitcnt lgkmcnt(0)
	s_cbranch_vccnz .Lzs_0
	s_add_i32 s14, s71, 0x80
	s_addk_i32 s70, 0x100
	s_mov_b32 s71, 0
	ds_read_b128 v[160:163], v144
	ds_read_b128 v[164:167], v145
	ds_read_b128 v[168:171], v140
	ds_read_b128 v[172:175], v141
	ds_read_b128 v[176:179], v146
	ds_read_b128 v[180:183], v147
	ds_read_b128 v[184:187], v148
	ds_read_b128 v[188:191], v149
	s_add_i32 s72, s14, 0x80
	s_cmp_eq_u32 s54, s71
	s_cselect_b32 s73, s13, s70
	s_cselect_b32 s72, s15, s72
	v_add_u32_e32 v159, s14, v157
	s_add_i32 m0, s22, 0xc000
	ds_read_b128 v[192:195], v158
	ds_read_b128 v[196:199], v158 offset:1024
	ds_read_b128 v[200:203], v158 offset:2048
	ds_read_b128 v[204:207], v158 offset:3072
	ds_read_b128 v[214:217], v158 offset:4096
	ds_read_b128 v[218:221], v158 offset:5120
	ds_read_b128 v[222:225], v158 offset:6144
	ds_read_b128 v[226:229], v158 offset:7168
	global_load_lds_dwordx4 v159, s[4:5]
	v_add_u32_e32 v159, s14, v156
	s_add_i32 m0, s22, 0xe000
	s_nop 0
	global_load_lds_dwordx4 v159, s[4:5]
	s_waitcnt vmcnt(8)
	s_waitcnt lgkmcnt(0)
	s_barrier
	s_waitcnt lgkmcnt(0)
	v_mfma_f32_16x16x32_bf16 v[122:125], v[168:171], v[192:195], 0
	v_mfma_f32_16x16x32_bf16 v[126:129], v[164:167], v[192:195], 0
	v_mfma_f32_16x16x32_bf16 v[110:113], v[168:171], v[200:203], 0
	v_mfma_f32_16x16x32_bf16 v[106:109], v[164:167], v[200:203], 0
	v_mfma_f32_16x16x32_bf16 v[94:97], v[168:171], v[214:217], 0
	v_mfma_f32_16x16x32_bf16 v[90:93], v[164:167], v[214:217], 0
	v_mfma_f32_16x16x32_bf16 v[78:81], v[168:171], v[222:225], 0
	v_mfma_f32_16x16x32_bf16 v[74:77], v[164:167], v[222:225], 0
	v_mfma_f32_16x16x32_bf16 v[122:125], v[160:163], v[196:199], v[122:125]
	v_mfma_f32_16x16x32_bf16 v[126:129], v[176:179], v[196:199], v[126:129]
	v_mfma_f32_16x16x32_bf16 v[110:113], v[160:163], v[204:207], v[110:113]
	v_mfma_f32_16x16x32_bf16 v[106:109], v[176:179], v[204:207], v[106:109]
	v_mfma_f32_16x16x32_bf16 v[94:97], v[160:163], v[218:221], v[94:97]
	v_mfma_f32_16x16x32_bf16 v[90:93], v[176:179], v[218:221], v[90:93]
	v_mfma_f32_16x16x32_bf16 v[78:81], v[160:163], v[226:229], v[78:81]
	v_mfma_f32_16x16x32_bf16 v[74:77], v[176:179], v[226:229], v[74:77]
	v_mfma_f32_16x16x32_bf16 v[118:121], v[172:175], v[192:195], 0
	v_mfma_f32_16x16x32_bf16 v[114:117], v[184:187], v[192:195], 0
	v_mfma_f32_16x16x32_bf16 v[102:105], v[172:175], v[200:203], 0
	v_mfma_f32_16x16x32_bf16 v[98:101], v[184:187], v[200:203], 0
	v_mfma_f32_16x16x32_bf16 v[86:89], v[172:175], v[214:217], 0
	v_mfma_f32_16x16x32_bf16 v[82:85], v[184:187], v[214:217], 0
	v_mfma_f32_16x16x32_bf16 v[70:73], v[172:175], v[222:225], 0
	v_mfma_f32_16x16x32_bf16 v[66:69], v[184:187], v[222:225], 0
	v_mfma_f32_16x16x32_bf16 v[118:121], v[180:183], v[196:199], v[118:121]
	v_mfma_f32_16x16x32_bf16 v[114:117], v[188:191], v[196:199], v[114:117]
	v_mfma_f32_16x16x32_bf16 v[102:105], v[180:183], v[204:207], v[102:105]
	v_mfma_f32_16x16x32_bf16 v[98:101], v[188:191], v[204:207], v[98:101]
	v_mfma_f32_16x16x32_bf16 v[86:89], v[180:183], v[218:221], v[86:89]
	v_mfma_f32_16x16x32_bf16 v[82:85], v[188:191], v[218:221], v[82:85]
	v_mfma_f32_16x16x32_bf16 v[70:73], v[180:183], v[226:229], v[70:73]
	v_mfma_f32_16x16x32_bf16 v[66:69], v[188:191], v[226:229], v[66:69]
	s_barrier
	s_mov_b32 m0, s23
	v_add_u32_e32 v159, s73, v134
	ds_read_b128 v[192:195], v158 offset:16384
	ds_read_b128 v[196:199], v158 offset:17408
	ds_read_b128 v[200:203], v158 offset:18432
	ds_read_b128 v[204:207], v158 offset:19456
	ds_read_b128 v[214:217], v158 offset:20480
	ds_read_b128 v[218:221], v158 offset:21504
	ds_read_b128 v[222:225], v158 offset:22528
	ds_read_b128 v[226:229], v158 offset:23552
	global_load_lds_dwordx4 v159, s[20:21]
	v_add_u32_e32 v159, s17, v159
	s_mov_b32 m0, s28
	s_nop 0
	global_load_lds_dwordx4 v159, s[20:21]
	v_add_u32_e32 v159, s73, v135
	s_mov_b32 m0, s29
	s_nop 0
	global_load_lds_dwordx4 v159, s[20:21]
	v_add_u32_e32 v159, s17, v159
	s_mov_b32 m0, s30
	s_nop 0
	global_load_lds_dwordx4 v159, s[20:21]
	v_add_u32_e32 v159, s72, v1
	s_mov_b32 m0, s22
	s_nop 0
	global_load_lds_dwordx4 v159, s[4:5]
	v_add_u32_e32 v159, s16, v159
	s_mov_b32 m0, s31
	s_nop 0
	global_load_lds_dwordx4 v159, s[4:5]
	s_waitcnt vmcnt(8)
	s_waitcnt lgkmcnt(0)
	s_barrier
	s_waitcnt lgkmcnt(0)
	v_mfma_f32_16x16x32_bf16 v[62:65], v[168:171], v[192:195], 0
	v_mfma_f32_16x16x32_bf16 v[58:61], v[164:167], v[192:195], 0
	v_mfma_f32_16x16x32_bf16 v[46:49], v[168:171], v[200:203], 0
	v_mfma_f32_16x16x32_bf16 v[42:45], v[164:167], v[200:203], 0
	v_mfma_f32_16x16x32_bf16 v[30:33], v[168:171], v[214:217], 0
	v_mfma_f32_16x16x32_bf16 v[26:29], v[164:167], v[214:217], 0
	v_mfma_f32_16x16x32_bf16 v[14:17], v[168:171], v[222:225], 0
	v_mfma_f32_16x16x32_bf16 v[10:13], v[164:167], v[222:225], 0
	v_mfma_f32_16x16x32_bf16 v[62:65], v[160:163], v[196:199], v[62:65]
	v_mfma_f32_16x16x32_bf16 v[58:61], v[176:179], v[196:199], v[58:61]
	v_mfma_f32_16x16x32_bf16 v[46:49], v[160:163], v[204:207], v[46:49]
	v_mfma_f32_16x16x32_bf16 v[42:45], v[176:179], v[204:207], v[42:45]
	v_mfma_f32_16x16x32_bf16 v[30:33], v[160:163], v[218:221], v[30:33]
	v_mfma_f32_16x16x32_bf16 v[26:29], v[176:179], v[218:221], v[26:29]
	v_mfma_f32_16x16x32_bf16 v[14:17], v[160:163], v[226:229], v[14:17]
	v_mfma_f32_16x16x32_bf16 v[10:13], v[176:179], v[226:229], v[10:13]
	v_mfma_f32_16x16x32_bf16 v[54:57], v[172:175], v[192:195], 0
	v_mfma_f32_16x16x32_bf16 v[50:53], v[184:187], v[192:195], 0
	v_mfma_f32_16x16x32_bf16 v[38:41], v[172:175], v[200:203], 0
	v_mfma_f32_16x16x32_bf16 v[34:37], v[184:187], v[200:203], 0
	v_mfma_f32_16x16x32_bf16 v[22:25], v[172:175], v[214:217], 0
	v_mfma_f32_16x16x32_bf16 v[18:21], v[184:187], v[214:217], 0
	v_mfma_f32_16x16x32_bf16 v[6:9], v[172:175], v[222:225], 0
	v_mfma_f32_16x16x32_bf16 v[2:5], v[184:187], v[222:225], 0
	v_mfma_f32_16x16x32_bf16 v[54:57], v[180:183], v[196:199], v[54:57]
	v_mfma_f32_16x16x32_bf16 v[50:53], v[188:191], v[196:199], v[50:53]
	v_mfma_f32_16x16x32_bf16 v[38:41], v[180:183], v[204:207], v[38:41]
	v_mfma_f32_16x16x32_bf16 v[34:37], v[188:191], v[204:207], v[34:37]
	v_mfma_f32_16x16x32_bf16 v[22:25], v[180:183], v[218:221], v[22:25]
	v_mfma_f32_16x16x32_bf16 v[18:21], v[188:191], v[218:221], v[18:21]
	v_mfma_f32_16x16x32_bf16 v[6:9], v[180:183], v[226:229], v[6:9]
	v_mfma_f32_16x16x32_bf16 v[2:5], v[188:191], v[226:229], v[2:5]
	s_barrier
	s_branch .Lmid_0
.LBB0_296:
	ds_read_b128 v[160:163], v144
	ds_read_b128 v[164:167], v145
	ds_read_b128 v[168:171], v140
	ds_read_b128 v[172:175], v141
	ds_read_b128 v[176:179], v146
	ds_read_b128 v[180:183], v147
	ds_read_b128 v[184:187], v148
	ds_read_b128 v[188:191], v149
	s_add_i32 s72, s14, 0x80
	s_cmp_eq_u32 s54, s71
	s_cselect_b32 s73, s13, s70
	s_cselect_b32 s72, s15, s72
	v_add_u32_e32 v159, s14, v157
	s_add_i32 m0, s22, 0xc000
	ds_read_b128 v[192:195], v158
	ds_read_b128 v[196:199], v158 offset:1024
	ds_read_b128 v[200:203], v158 offset:2048
	ds_read_b128 v[204:207], v158 offset:3072
	ds_read_b128 v[214:217], v158 offset:4096
	ds_read_b128 v[218:221], v158 offset:5120
	ds_read_b128 v[222:225], v158 offset:6144
	ds_read_b128 v[226:229], v158 offset:7168
	global_load_lds_dwordx4 v159, s[4:5]
	v_add_u32_e32 v159, s14, v156
	s_add_i32 m0, s22, 0xe000
	s_nop 0
	global_load_lds_dwordx4 v159, s[4:5]
	s_waitcnt vmcnt(8)
	s_waitcnt lgkmcnt(0)
	s_barrier
	s_waitcnt lgkmcnt(0)
	v_mfma_f32_16x16x32_bf16 v[122:125], v[168:171], v[192:195], v[122:125]
	v_mfma_f32_16x16x32_bf16 v[126:129], v[164:167], v[192:195], v[126:129]
	v_mfma_f32_16x16x32_bf16 v[110:113], v[168:171], v[200:203], v[110:113]
	v_mfma_f32_16x16x32_bf16 v[106:109], v[164:167], v[200:203], v[106:109]
	v_mfma_f32_16x16x32_bf16 v[94:97], v[168:171], v[214:217], v[94:97]
	v_mfma_f32_16x16x32_bf16 v[90:93], v[164:167], v[214:217], v[90:93]
	v_mfma_f32_16x16x32_bf16 v[78:81], v[168:171], v[222:225], v[78:81]
	v_mfma_f32_16x16x32_bf16 v[74:77], v[164:167], v[222:225], v[74:77]
	v_mfma_f32_16x16x32_bf16 v[122:125], v[160:163], v[196:199], v[122:125]
	v_mfma_f32_16x16x32_bf16 v[126:129], v[176:179], v[196:199], v[126:129]
	v_mfma_f32_16x16x32_bf16 v[110:113], v[160:163], v[204:207], v[110:113]
	v_mfma_f32_16x16x32_bf16 v[106:109], v[176:179], v[204:207], v[106:109]
	v_mfma_f32_16x16x32_bf16 v[94:97], v[160:163], v[218:221], v[94:97]
	v_mfma_f32_16x16x32_bf16 v[90:93], v[176:179], v[218:221], v[90:93]
	v_mfma_f32_16x16x32_bf16 v[78:81], v[160:163], v[226:229], v[78:81]
	v_mfma_f32_16x16x32_bf16 v[74:77], v[176:179], v[226:229], v[74:77]
	v_mfma_f32_16x16x32_bf16 v[118:121], v[172:175], v[192:195], v[118:121]
	v_mfma_f32_16x16x32_bf16 v[114:117], v[184:187], v[192:195], v[114:117]
	v_mfma_f32_16x16x32_bf16 v[102:105], v[172:175], v[200:203], v[102:105]
	v_mfma_f32_16x16x32_bf16 v[98:101], v[184:187], v[200:203], v[98:101]
	v_mfma_f32_16x16x32_bf16 v[86:89], v[172:175], v[214:217], v[86:89]
	v_mfma_f32_16x16x32_bf16 v[82:85], v[184:187], v[214:217], v[82:85]
	v_mfma_f32_16x16x32_bf16 v[70:73], v[172:175], v[222:225], v[70:73]
	v_mfma_f32_16x16x32_bf16 v[66:69], v[184:187], v[222:225], v[66:69]
	v_mfma_f32_16x16x32_bf16 v[118:121], v[180:183], v[196:199], v[118:121]
	v_mfma_f32_16x16x32_bf16 v[114:117], v[188:191], v[196:199], v[114:117]
	v_mfma_f32_16x16x32_bf16 v[102:105], v[180:183], v[204:207], v[102:105]
	v_mfma_f32_16x16x32_bf16 v[98:101], v[188:191], v[204:207], v[98:101]
	v_mfma_f32_16x16x32_bf16 v[86:89], v[180:183], v[218:221], v[86:89]
	v_mfma_f32_16x16x32_bf16 v[82:85], v[188:191], v[218:221], v[82:85]
	v_mfma_f32_16x16x32_bf16 v[70:73], v[180:183], v[226:229], v[70:73]
	v_mfma_f32_16x16x32_bf16 v[66:69], v[188:191], v[226:229], v[66:69]
	s_barrier
	s_mov_b32 m0, s23
	v_add_u32_e32 v159, s73, v134
	ds_read_b128 v[192:195], v158 offset:16384
	ds_read_b128 v[196:199], v158 offset:17408
	ds_read_b128 v[200:203], v158 offset:18432
	ds_read_b128 v[204:207], v158 offset:19456
	ds_read_b128 v[214:217], v158 offset:20480
	ds_read_b128 v[218:221], v158 offset:21504
	ds_read_b128 v[222:225], v158 offset:22528
	ds_read_b128 v[226:229], v158 offset:23552
	global_load_lds_dwordx4 v159, s[20:21]
	v_add_u32_e32 v159, s17, v159
	s_mov_b32 m0, s28
	s_nop 0
	global_load_lds_dwordx4 v159, s[20:21]
	v_add_u32_e32 v159, s73, v135
	s_mov_b32 m0, s29
	s_nop 0
	global_load_lds_dwordx4 v159, s[20:21]
	v_add_u32_e32 v159, s17, v159
	s_mov_b32 m0, s30
	s_nop 0
	global_load_lds_dwordx4 v159, s[20:21]
	v_add_u32_e32 v159, s72, v1
	s_mov_b32 m0, s22
	s_nop 0
	global_load_lds_dwordx4 v159, s[4:5]
	v_add_u32_e32 v159, s16, v159
	s_mov_b32 m0, s31
	s_nop 0
	global_load_lds_dwordx4 v159, s[4:5]
	s_waitcnt vmcnt(8)
	s_waitcnt lgkmcnt(0)
	s_barrier
	s_waitcnt lgkmcnt(0)
	v_mfma_f32_16x16x32_bf16 v[62:65], v[168:171], v[192:195], v[62:65]
	v_mfma_f32_16x16x32_bf16 v[58:61], v[164:167], v[192:195], v[58:61]
	v_mfma_f32_16x16x32_bf16 v[46:49], v[168:171], v[200:203], v[46:49]
	v_mfma_f32_16x16x32_bf16 v[42:45], v[164:167], v[200:203], v[42:45]
	v_mfma_f32_16x16x32_bf16 v[30:33], v[168:171], v[214:217], v[30:33]
	v_mfma_f32_16x16x32_bf16 v[26:29], v[164:167], v[214:217], v[26:29]
	v_mfma_f32_16x16x32_bf16 v[14:17], v[168:171], v[222:225], v[14:17]
	v_mfma_f32_16x16x32_bf16 v[10:13], v[164:167], v[222:225], v[10:13]
	v_mfma_f32_16x16x32_bf16 v[62:65], v[160:163], v[196:199], v[62:65]
	v_mfma_f32_16x16x32_bf16 v[58:61], v[176:179], v[196:199], v[58:61]
	v_mfma_f32_16x16x32_bf16 v[46:49], v[160:163], v[204:207], v[46:49]
	v_mfma_f32_16x16x32_bf16 v[42:45], v[176:179], v[204:207], v[42:45]
	v_mfma_f32_16x16x32_bf16 v[30:33], v[160:163], v[218:221], v[30:33]
	v_mfma_f32_16x16x32_bf16 v[26:29], v[176:179], v[218:221], v[26:29]
	v_mfma_f32_16x16x32_bf16 v[14:17], v[160:163], v[226:229], v[14:17]
	v_mfma_f32_16x16x32_bf16 v[10:13], v[176:179], v[226:229], v[10:13]
	v_mfma_f32_16x16x32_bf16 v[54:57], v[172:175], v[192:195], v[54:57]
	v_mfma_f32_16x16x32_bf16 v[50:53], v[184:187], v[192:195], v[50:53]
	v_mfma_f32_16x16x32_bf16 v[38:41], v[172:175], v[200:203], v[38:41]
	v_mfma_f32_16x16x32_bf16 v[34:37], v[184:187], v[200:203], v[34:37]
	v_mfma_f32_16x16x32_bf16 v[22:25], v[172:175], v[214:217], v[22:25]
	v_mfma_f32_16x16x32_bf16 v[18:21], v[184:187], v[214:217], v[18:21]
	v_mfma_f32_16x16x32_bf16 v[6:9], v[172:175], v[222:225], v[6:9]
	v_mfma_f32_16x16x32_bf16 v[2:5], v[184:187], v[222:225], v[2:5]
	v_mfma_f32_16x16x32_bf16 v[54:57], v[180:183], v[196:199], v[54:57]
	v_mfma_f32_16x16x32_bf16 v[50:53], v[188:191], v[196:199], v[50:53]
	v_mfma_f32_16x16x32_bf16 v[38:41], v[180:183], v[204:207], v[38:41]
	v_mfma_f32_16x16x32_bf16 v[34:37], v[188:191], v[204:207], v[34:37]
	v_mfma_f32_16x16x32_bf16 v[22:25], v[180:183], v[218:221], v[22:25]
	v_mfma_f32_16x16x32_bf16 v[18:21], v[188:191], v[218:221], v[18:21]
	v_mfma_f32_16x16x32_bf16 v[6:9], v[180:183], v[226:229], v[6:9]
	v_mfma_f32_16x16x32_bf16 v[2:5], v[188:191], v[226:229], v[2:5]
	s_barrier
.Lmid_0:
	ds_read_b128 v[160:163], v150
	ds_read_b128 v[164:167], v151
	ds_read_b128 v[168:171], v142
	ds_read_b128 v[172:175], v143
	ds_read_b128 v[176:179], v152
	ds_read_b128 v[180:183], v153
	ds_read_b128 v[184:187], v154
	ds_read_b128 v[188:191], v155
	s_mov_b32 m0, s35
	v_add_u32_e32 v159, s72, v136
	ds_read_b128 v[192:195], v158 offset:32768
	ds_read_b128 v[196:199], v158 offset:33792
	ds_read_b128 v[200:203], v158 offset:34816
	ds_read_b128 v[204:207], v158 offset:35840
	ds_read_b128 v[214:217], v158 offset:36864
	ds_read_b128 v[218:221], v158 offset:37888
	ds_read_b128 v[222:225], v158 offset:38912
	ds_read_b128 v[226:229], v158 offset:39936
	global_load_lds_dwordx4 v159, s[4:5]
	v_add_u32_e32 v159, s16, v159
	s_mov_b32 m0, s44
	s_nop 0
	global_load_lds_dwordx4 v159, s[4:5]
	s_waitcnt vmcnt(8)
	s_waitcnt lgkmcnt(0)
	s_barrier
	s_waitcnt lgkmcnt(0)
	v_mfma_f32_16x16x32_bf16 v[122:125], v[168:171], v[192:195], v[122:125]
	v_mfma_f32_16x16x32_bf16 v[126:129], v[164:167], v[192:195], v[126:129]
	v_mfma_f32_16x16x32_bf16 v[110:113], v[168:171], v[200:203], v[110:113]
	v_mfma_f32_16x16x32_bf16 v[106:109], v[164:167], v[200:203], v[106:109]
	v_mfma_f32_16x16x32_bf16 v[94:97], v[168:171], v[214:217], v[94:97]
	v_mfma_f32_16x16x32_bf16 v[90:93], v[164:167], v[214:217], v[90:93]
	v_mfma_f32_16x16x32_bf16 v[78:81], v[168:171], v[222:225], v[78:81]
	v_mfma_f32_16x16x32_bf16 v[74:77], v[164:167], v[222:225], v[74:77]
	v_mfma_f32_16x16x32_bf16 v[122:125], v[160:163], v[196:199], v[122:125]
	v_mfma_f32_16x16x32_bf16 v[126:129], v[176:179], v[196:199], v[126:129]
	v_mfma_f32_16x16x32_bf16 v[110:113], v[160:163], v[204:207], v[110:113]
	v_mfma_f32_16x16x32_bf16 v[106:109], v[176:179], v[204:207], v[106:109]
	v_mfma_f32_16x16x32_bf16 v[94:97], v[160:163], v[218:221], v[94:97]
	v_mfma_f32_16x16x32_bf16 v[90:93], v[176:179], v[218:221], v[90:93]
	v_mfma_f32_16x16x32_bf16 v[78:81], v[160:163], v[226:229], v[78:81]
	v_mfma_f32_16x16x32_bf16 v[74:77], v[176:179], v[226:229], v[74:77]
	v_mfma_f32_16x16x32_bf16 v[118:121], v[172:175], v[192:195], v[118:121]
	v_mfma_f32_16x16x32_bf16 v[114:117], v[184:187], v[192:195], v[114:117]
	v_mfma_f32_16x16x32_bf16 v[102:105], v[172:175], v[200:203], v[102:105]
	v_mfma_f32_16x16x32_bf16 v[98:101], v[184:187], v[200:203], v[98:101]
	v_mfma_f32_16x16x32_bf16 v[86:89], v[172:175], v[214:217], v[86:89]
	v_mfma_f32_16x16x32_bf16 v[82:85], v[184:187], v[214:217], v[82:85]
	v_mfma_f32_16x16x32_bf16 v[70:73], v[172:175], v[222:225], v[70:73]
	v_mfma_f32_16x16x32_bf16 v[66:69], v[184:187], v[222:225], v[66:69]
	v_mfma_f32_16x16x32_bf16 v[118:121], v[180:183], v[196:199], v[118:121]
	v_mfma_f32_16x16x32_bf16 v[114:117], v[188:191], v[196:199], v[114:117]
	v_mfma_f32_16x16x32_bf16 v[102:105], v[180:183], v[204:207], v[102:105]
	v_mfma_f32_16x16x32_bf16 v[98:101], v[188:191], v[204:207], v[98:101]
	v_mfma_f32_16x16x32_bf16 v[86:89], v[180:183], v[218:221], v[86:89]
	v_mfma_f32_16x16x32_bf16 v[82:85], v[188:191], v[218:221], v[82:85]
	v_mfma_f32_16x16x32_bf16 v[70:73], v[180:183], v[226:229], v[70:73]
	v_mfma_f32_16x16x32_bf16 v[66:69], v[188:191], v[226:229], v[66:69]
	s_barrier
	s_addk_i32 s73, 0x80
	s_mov_b32 m0, s46
	v_add_u32_e32 v159, s73, v134
	ds_read_b128 v[192:195], v158 offset:49152
	ds_read_b128 v[196:199], v158 offset:50176
	ds_read_b128 v[200:203], v158 offset:51200
	ds_read_b128 v[204:207], v158 offset:52224
	ds_read_b128 v[214:217], v158 offset:53248
	ds_read_b128 v[218:221], v158 offset:54272
	ds_read_b128 v[222:225], v158 offset:55296
	ds_read_b128 v[226:229], v158 offset:56320
	global_load_lds_dwordx4 v159, s[20:21]
	v_add_u32_e32 v159, s17, v159
	s_mov_b32 m0, s47
	s_nop 0
	global_load_lds_dwordx4 v159, s[20:21]
	v_add_u32_e32 v159, s73, v135
	s_mov_b32 m0, s50
	s_nop 0
	global_load_lds_dwordx4 v159, s[20:21]
	v_add_u32_e32 v159, s17, v159
	s_mov_b32 m0, s51
	s_nop 0
	global_load_lds_dwordx4 v159, s[20:21]
	v_add_u32_e32 v159, s72, v137
	s_mov_b32 m0, s48
	s_nop 0
	global_load_lds_dwordx4 v159, s[4:5]
	v_add_u32_e32 v159, s16, v159
	s_mov_b32 m0, s49
	s_nop 0
	global_load_lds_dwordx4 v159, s[4:5]
	s_waitcnt vmcnt(8)
	s_waitcnt lgkmcnt(0)
	s_barrier
	s_waitcnt lgkmcnt(0)
	v_mfma_f32_16x16x32_bf16 v[62:65], v[168:171], v[192:195], v[62:65]
	v_mfma_f32_16x16x32_bf16 v[58:61], v[164:167], v[192:195], v[58:61]
	v_mfma_f32_16x16x32_bf16 v[46:49], v[168:171], v[200:203], v[46:49]
	v_mfma_f32_16x16x32_bf16 v[42:45], v[164:167], v[200:203], v[42:45]
	v_mfma_f32_16x16x32_bf16 v[30:33], v[168:171], v[214:217], v[30:33]
	v_mfma_f32_16x16x32_bf16 v[26:29], v[164:167], v[214:217], v[26:29]
	v_mfma_f32_16x16x32_bf16 v[14:17], v[168:171], v[222:225], v[14:17]
	v_mfma_f32_16x16x32_bf16 v[10:13], v[164:167], v[222:225], v[10:13]
	v_mfma_f32_16x16x32_bf16 v[62:65], v[160:163], v[196:199], v[62:65]
	v_mfma_f32_16x16x32_bf16 v[58:61], v[176:179], v[196:199], v[58:61]
	v_mfma_f32_16x16x32_bf16 v[46:49], v[160:163], v[204:207], v[46:49]
	v_mfma_f32_16x16x32_bf16 v[42:45], v[176:179], v[204:207], v[42:45]
	v_mfma_f32_16x16x32_bf16 v[30:33], v[160:163], v[218:221], v[30:33]
	v_mfma_f32_16x16x32_bf16 v[26:29], v[176:179], v[218:221], v[26:29]
	v_mfma_f32_16x16x32_bf16 v[14:17], v[160:163], v[226:229], v[14:17]
	v_mfma_f32_16x16x32_bf16 v[10:13], v[176:179], v[226:229], v[10:13]
	v_mfma_f32_16x16x32_bf16 v[54:57], v[172:175], v[192:195], v[54:57]
	v_mfma_f32_16x16x32_bf16 v[50:53], v[184:187], v[192:195], v[50:53]
	v_mfma_f32_16x16x32_bf16 v[38:41], v[172:175], v[200:203], v[38:41]
	v_mfma_f32_16x16x32_bf16 v[34:37], v[184:187], v[200:203], v[34:37]
	v_mfma_f32_16x16x32_bf16 v[22:25], v[172:175], v[214:217], v[22:25]
	v_mfma_f32_16x16x32_bf16 v[18:21], v[184:187], v[214:217], v[18:21]
	v_mfma_f32_16x16x32_bf16 v[6:9], v[172:175], v[222:225], v[6:9]
	v_mfma_f32_16x16x32_bf16 v[2:5], v[184:187], v[222:225], v[2:5]
	v_mfma_f32_16x16x32_bf16 v[54:57], v[180:183], v[196:199], v[54:57]
	v_mfma_f32_16x16x32_bf16 v[50:53], v[188:191], v[196:199], v[50:53]
	v_mfma_f32_16x16x32_bf16 v[38:41], v[180:183], v[204:207], v[38:41]
	v_mfma_f32_16x16x32_bf16 v[34:37], v[188:191], v[204:207], v[34:37]
	v_mfma_f32_16x16x32_bf16 v[22:25], v[180:183], v[218:221], v[22:25]
	v_mfma_f32_16x16x32_bf16 v[18:21], v[188:191], v[218:221], v[18:21]
	v_mfma_f32_16x16x32_bf16 v[6:9], v[180:183], v[226:229], v[6:9]
	v_mfma_f32_16x16x32_bf16 v[2:5], v[188:191], v[226:229], v[2:5]
	s_barrier
	s_add_i32 s71, s71, 2
	s_addk_i32 s14, 0x100
	s_addk_i32 s70, 0x100
	s_cmp_ge_i32 s71, s52
	s_cbranch_scc0 .LBB0_296

.LBB0_430:
	s_setprio 0
	s_cmp_lt_i32 s41, 4
	s_cbranch_scc1 .LBB0_480
	s_waitcnt vmcnt(0)
	v_cmp_eq_u32_e32 vcc, 0, v0
	s_waitcnt vmcnt(0) lgkmcnt(0)
	s_barrier
	s_and_saveexec_b64 s[2:3], vcc
	s_cbranch_execz .LBB0_479
	v_mov_b32_e32 v1, s92
	s_waitcnt vmcnt(0) expcnt(0) lgkmcnt(0)
	ds_read_b32 v3, v1
	ds_read_b32 v1, v1 offset:4
	s_waitcnt lgkmcnt(1)
	v_cmp_ne_u32_e32 vcc, 0, v3
	s_cbranch_vccnz .LBB0_447
	v_readlane_b32 s4, v254, 1
	v_readlane_b32 s5, v254, 2
	s_load_dwordx2 s[8:9], s[4:5], 0x4
	s_add_u32 s4, s42, 0x1000
	s_addc_u32 s5, s43, 0
	s_add_u32 s6, s42, 0x1100
	s_addc_u32 s7, s43, 0
	s_waitcnt lgkmcnt(0)
	s_mul_i32 s18, s8, s34
	s_add_u32 s8, s42, 0x1200
	s_mul_i32 s18, s18, s9
	s_addc_u32 s9, s43, 0
	s_add_u32 s10, s42, 0x1300
	s_addc_u32 s11, s43, 0
	s_mov_b32 s19, 1
	v_mov_b32_e32 v17, 0
	s_branch .LBB0_435

.Lstag9_done:
	s_cmp_gt_i32 s40, 9
	s_cselect_b64 s[2:3], -1, 0
	s_cmp_lt_i32 s41, 10
	s_cselect_b64 s[4:5], -1, 0
	s_or_b64 s[2:3], s[2:3], s[4:5]
	s_and_b64 vcc, exec, s[2:3]
	s_cbranch_vccnz .LBB0_1384
	s_cmp_ge_u32 s27, 4
	s_cbranch_scc0 .Lsp_9
	s_setprio 1
.Lsp_9:
	v_mov_b32_e32 v2, v0
	s_cmpk_lt_i32 s26, 0x420
	s_movk_i32 s7, 0x800
	v_readfirstlane_b32 s6, v2
	s_movk_i32 s5, 0x800
	s_movk_i32 s10, 0x800
	s_cselect_b64 s[2:3], -1, 0
	s_cmpk_gt_i32 s26, 0x41f
	s_cbranch_scc1 .LBB0_1173
	s_ashr_i32 s4, s26, 31
	s_lshr_b32 s4, s4, 29
	s_add_i32 s4, s26, s4
	s_ashr_i32 s8, s4, 3
	s_and_b32 s4, s4, -8
	s_sub_i32 s4, s26, s4
	s_cmp_lt_i32 s4, 0
	s_movk_i32 s9, 0x85
	s_cselect_b32 s9, s9, 0x84
	s_mul_i32 s4, s4, s9
	s_add_i32 s4, s4, s8
	s_ashr_i32 s8, s4, 31
	s_lshr_b32 s8, s8, 26
	s_add_i32 s8, s4, s8
	s_ashr_i32 s9, s8, 6
	s_lshl_b32 s11, s9, 3
	s_sub_i32 s9, 0x84, s11
	s_waitcnt lgkmcnt(0)
	s_min_u32 s12, s9, 8
	s_andn2_b32 s8, s8, 63
	s_sub_i32 s4, s4, s8
	v_cvt_f32_ubyte0_e32 v3, s12
	v_cvt_f32_i32_e32 v1, s4
	v_rcp_iflag_f32_e32 v4, v3
	s_ashr_i32 s8, s4, 30
	s_or_b32 s13, s8, 1
	v_mul_f32_e32 v4, v1, v4
	v_trunc_f32_e32 v4, v4
	v_fma_f32 v1, -v4, v3, v1
	v_cvt_i32_f32_e32 v4, v4
	v_cmp_ge_f32_e64 s[8:9], |v1|, v3
	s_and_b64 s[8:9], s[8:9], exec
	s_cselect_b32 s8, s13, 0
	v_readfirstlane_b32 s9, v4
	s_add_i32 s8, s9, s8
	s_mul_i32 s9, s8, s12
	s_sub_i32 s4, s4, s9
	s_sext_i32_i8 s4, s4
	s_add_i32 s4, s11, s4
	s_sext_i32_i8 s62, s8
	s_lshl_b32 s58, s4, 20
	s_lshl_b32 s59, s62, 20

.LBB0_1181:
	s_andn2_b64 vcc, exec, s[16:17]
	s_waitcnt lgkmcnt(0)
	s_cbranch_vccnz .Lzs_4
	s_add_i32 s6, s58, 0x80
	s_add_i32 s58, s59, 0x100
	s_mov_b32 s59, 0
	ds_read_b128 v[114:117], v206
	ds_read_b128 v[118:121], v207
	ds_read_b128 v[122:125], v202
	ds_read_b128 v[126:129], v203
	ds_read_b128 v[146:149], v208
	ds_read_b128 v[150:153], v209
	ds_read_b128 v[154:157], v211
	ds_read_b128 v[158:161], v213
	s_add_i32 s60, s6, 0x80
	s_cmp_eq_u32 s90, s59
	s_cselect_b32 s61, s5, s58
	s_cselect_b32 s60, s7, s60
	v_add_u32_e32 v194, s6, v221
	s_add_i32 m0, s70, 0xc000
	ds_read_b128 v[162:165], v222
	ds_read_b128 v[170:173], v222 offset:1024
	ds_read_b128 v[174:177], v222 offset:2048
	ds_read_b128 v[178:181], v222 offset:3072
	ds_read_b128 v[182:185], v222 offset:4096
	ds_read_b128 v[186:189], v222 offset:5120
	ds_read_b128 v[190:193], v222 offset:6144
	ds_read_b128 v[226:229], v222 offset:7168
	global_load_lds_dwordx4 v194, s[8:9]
	v_add_u32_e32 v194, s6, v220
	s_add_i32 m0, s70, 0xe000
	s_nop 0
	global_load_lds_dwordx4 v194, s[8:9]
	s_waitcnt vmcnt(8)
	s_waitcnt lgkmcnt(0)
	s_barrier
	s_waitcnt lgkmcnt(0)
	v_mfma_f32_16x16x32_bf16 v[142:145], v[122:125], v[162:165], 0
	v_mfma_f32_16x16x32_bf16 v[138:141], v[118:121], v[162:165], 0
	v_mfma_f32_16x16x32_bf16 v[110:113], v[122:125], v[174:177], 0
	v_mfma_f32_16x16x32_bf16 v[106:109], v[118:121], v[174:177], 0
	v_mfma_f32_16x16x32_bf16 v[94:97], v[122:125], v[182:185], 0
	v_mfma_f32_16x16x32_bf16 v[90:93], v[118:121], v[182:185], 0
	v_mfma_f32_16x16x32_bf16 v[78:81], v[122:125], v[190:193], 0
	v_mfma_f32_16x16x32_bf16 v[74:77], v[118:121], v[190:193], 0
	v_mfma_f32_16x16x32_bf16 v[142:145], v[114:117], v[170:173], v[142:145]
	v_mfma_f32_16x16x32_bf16 v[138:141], v[146:149], v[170:173], v[138:141]
	v_mfma_f32_16x16x32_bf16 v[110:113], v[114:117], v[178:181], v[110:113]
	v_mfma_f32_16x16x32_bf16 v[106:109], v[146:149], v[178:181], v[106:109]
	v_mfma_f32_16x16x32_bf16 v[94:97], v[114:117], v[186:189], v[94:97]
	v_mfma_f32_16x16x32_bf16 v[90:93], v[146:149], v[186:189], v[90:93]
	v_mfma_f32_16x16x32_bf16 v[78:81], v[114:117], v[226:229], v[78:81]
	v_mfma_f32_16x16x32_bf16 v[74:77], v[146:149], v[226:229], v[74:77]
	v_mfma_f32_16x16x32_bf16 v[134:137], v[126:129], v[162:165], 0
	v_mfma_f32_16x16x32_bf16 v[130:133], v[154:157], v[162:165], 0
	v_mfma_f32_16x16x32_bf16 v[102:105], v[126:129], v[174:177], 0
	v_mfma_f32_16x16x32_bf16 v[98:101], v[154:157], v[174:177], 0
	v_mfma_f32_16x16x32_bf16 v[86:89], v[126:129], v[182:185], 0
	v_mfma_f32_16x16x32_bf16 v[82:85], v[154:157], v[182:185], 0
	v_mfma_f32_16x16x32_bf16 v[70:73], v[126:129], v[190:193], 0
	v_mfma_f32_16x16x32_bf16 v[66:69], v[154:157], v[190:193], 0
	v_mfma_f32_16x16x32_bf16 v[134:137], v[150:153], v[170:173], v[134:137]
	v_mfma_f32_16x16x32_bf16 v[130:133], v[158:161], v[170:173], v[130:133]
	v_mfma_f32_16x16x32_bf16 v[102:105], v[150:153], v[178:181], v[102:105]
	v_mfma_f32_16x16x32_bf16 v[98:101], v[158:161], v[178:181], v[98:101]
	v_mfma_f32_16x16x32_bf16 v[86:89], v[150:153], v[186:189], v[86:89]
	v_mfma_f32_16x16x32_bf16 v[82:85], v[158:161], v[186:189], v[82:85]
	v_mfma_f32_16x16x32_bf16 v[70:73], v[150:153], v[226:229], v[70:73]
	v_mfma_f32_16x16x32_bf16 v[66:69], v[158:161], v[226:229], v[66:69]
	s_barrier
	s_mov_b32 m0, s71
	v_add_u32_e32 v194, s61, v196
	ds_read_b128 v[162:165], v222 offset:16384
	ds_read_b128 v[170:173], v222 offset:17408
	ds_read_b128 v[174:177], v222 offset:18432
	ds_read_b128 v[178:181], v222 offset:19456
	ds_read_b128 v[182:185], v222 offset:20480
	ds_read_b128 v[186:189], v222 offset:21504
	ds_read_b128 v[190:193], v222 offset:22528
	ds_read_b128 v[226:229], v222 offset:23552
	global_load_lds_dwordx4 v194, s[20:21]
	v_add_u32_e32 v194, s35, v194
	s_mov_b32 m0, s72
	s_nop 0
	global_load_lds_dwordx4 v194, s[20:21]
	v_add_u32_e32 v194, s61, v197
	s_mov_b32 m0, s73
	s_nop 0
	global_load_lds_dwordx4 v194, s[20:21]
	v_add_u32_e32 v194, s35, v194
	s_mov_b32 m0, s76
	s_nop 0
	global_load_lds_dwordx4 v194, s[20:21]
	v_add_u32_e32 v194, s60, v1
	s_mov_b32 m0, s70
	s_nop 0
	global_load_lds_dwordx4 v194, s[8:9]
	v_add_u32_e32 v194, s29, v194
	s_mov_b32 m0, s77
	s_nop 0
	global_load_lds_dwordx4 v194, s[8:9]
	s_waitcnt vmcnt(8)
	s_waitcnt lgkmcnt(0)
	s_barrier
	s_waitcnt lgkmcnt(0)
	v_mfma_f32_16x16x32_bf16 v[62:65], v[122:125], v[162:165], 0
	v_mfma_f32_16x16x32_bf16 v[58:61], v[118:121], v[162:165], 0
	v_mfma_f32_16x16x32_bf16 v[46:49], v[122:125], v[174:177], 0
	v_mfma_f32_16x16x32_bf16 v[42:45], v[118:121], v[174:177], 0
	v_mfma_f32_16x16x32_bf16 v[30:33], v[122:125], v[182:185], 0
	v_mfma_f32_16x16x32_bf16 v[26:29], v[118:121], v[182:185], 0
	v_mfma_f32_16x16x32_bf16 v[14:17], v[122:125], v[190:193], 0
	v_mfma_f32_16x16x32_bf16 v[10:13], v[118:121], v[190:193], 0
	v_mfma_f32_16x16x32_bf16 v[62:65], v[114:117], v[170:173], v[62:65]
	v_mfma_f32_16x16x32_bf16 v[58:61], v[146:149], v[170:173], v[58:61]
	v_mfma_f32_16x16x32_bf16 v[46:49], v[114:117], v[178:181], v[46:49]
	v_mfma_f32_16x16x32_bf16 v[42:45], v[146:149], v[178:181], v[42:45]
	v_mfma_f32_16x16x32_bf16 v[30:33], v[114:117], v[186:189], v[30:33]
	v_mfma_f32_16x16x32_bf16 v[26:29], v[146:149], v[186:189], v[26:29]
	v_mfma_f32_16x16x32_bf16 v[14:17], v[114:117], v[226:229], v[14:17]
	v_mfma_f32_16x16x32_bf16 v[10:13], v[146:149], v[226:229], v[10:13]
	v_mfma_f32_16x16x32_bf16 v[54:57], v[126:129], v[162:165], 0
	v_mfma_f32_16x16x32_bf16 v[50:53], v[154:157], v[162:165], 0
	v_mfma_f32_16x16x32_bf16 v[38:41], v[126:129], v[174:177], 0
	v_mfma_f32_16x16x32_bf16 v[34:37], v[154:157], v[174:177], 0
	v_mfma_f32_16x16x32_bf16 v[22:25], v[126:129], v[182:185], 0
	v_mfma_f32_16x16x32_bf16 v[18:21], v[154:157], v[182:185], 0
	v_mfma_f32_16x16x32_bf16 v[6:9], v[126:129], v[190:193], 0
	v_mfma_f32_16x16x32_bf16 v[2:5], v[154:157], v[190:193], 0
	v_mfma_f32_16x16x32_bf16 v[54:57], v[150:153], v[170:173], v[54:57]
	v_mfma_f32_16x16x32_bf16 v[50:53], v[158:161], v[170:173], v[50:53]
	v_mfma_f32_16x16x32_bf16 v[38:41], v[150:153], v[178:181], v[38:41]
	v_mfma_f32_16x16x32_bf16 v[34:37], v[158:161], v[178:181], v[34:37]
	v_mfma_f32_16x16x32_bf16 v[22:25], v[150:153], v[186:189], v[22:25]
	v_mfma_f32_16x16x32_bf16 v[18:21], v[158:161], v[186:189], v[18:21]
	v_mfma_f32_16x16x32_bf16 v[6:9], v[150:153], v[226:229], v[6:9]
	v_mfma_f32_16x16x32_bf16 v[2:5], v[158:161], v[226:229], v[2:5]
	s_barrier
	s_branch .Lmid_4
.LBB0_1183:
	ds_read_b128 v[114:117], v206
	ds_read_b128 v[118:121], v207
	ds_read_b128 v[122:125], v202
	ds_read_b128 v[126:129], v203
	ds_read_b128 v[146:149], v208
	ds_read_b128 v[150:153], v209
	ds_read_b128 v[154:157], v211
	ds_read_b128 v[158:161], v213
	s_add_i32 s60, s6, 0x80
	s_cmp_eq_u32 s90, s59
	s_cselect_b32 s61, s5, s58
	s_cselect_b32 s60, s7, s60
	v_add_u32_e32 v194, s6, v221
	s_add_i32 m0, s70, 0xc000
	ds_read_b128 v[162:165], v222
	ds_read_b128 v[170:173], v222 offset:1024
	ds_read_b128 v[174:177], v222 offset:2048
	ds_read_b128 v[178:181], v222 offset:3072
	ds_read_b128 v[182:185], v222 offset:4096
	ds_read_b128 v[186:189], v222 offset:5120
	ds_read_b128 v[190:193], v222 offset:6144
	ds_read_b128 v[226:229], v222 offset:7168
	global_load_lds_dwordx4 v194, s[8:9]
	v_add_u32_e32 v194, s6, v220
	s_add_i32 m0, s70, 0xe000
	s_nop 0
	global_load_lds_dwordx4 v194, s[8:9]
	s_waitcnt vmcnt(8)
	s_waitcnt lgkmcnt(0)
	s_barrier
	s_waitcnt lgkmcnt(0)
	v_mfma_f32_16x16x32_bf16 v[142:145], v[122:125], v[162:165], v[142:145]
	v_mfma_f32_16x16x32_bf16 v[138:141], v[118:121], v[162:165], v[138:141]
	v_mfma_f32_16x16x32_bf16 v[110:113], v[122:125], v[174:177], v[110:113]
	v_mfma_f32_16x16x32_bf16 v[106:109], v[118:121], v[174:177], v[106:109]
	v_mfma_f32_16x16x32_bf16 v[94:97], v[122:125], v[182:185], v[94:97]
	v_mfma_f32_16x16x32_bf16 v[90:93], v[118:121], v[182:185], v[90:93]
	v_mfma_f32_16x16x32_bf16 v[78:81], v[122:125], v[190:193], v[78:81]
	v_mfma_f32_16x16x32_bf16 v[74:77], v[118:121], v[190:193], v[74:77]
	v_mfma_f32_16x16x32_bf16 v[142:145], v[114:117], v[170:173], v[142:145]
	v_mfma_f32_16x16x32_bf16 v[138:141], v[146:149], v[170:173], v[138:141]
	v_mfma_f32_16x16x32_bf16 v[110:113], v[114:117], v[178:181], v[110:113]
	v_mfma_f32_16x16x32_bf16 v[106:109], v[146:149], v[178:181], v[106:109]
	v_mfma_f32_16x16x32_bf16 v[94:97], v[114:117], v[186:189], v[94:97]
	v_mfma_f32_16x16x32_bf16 v[90:93], v[146:149], v[186:189], v[90:93]
	v_mfma_f32_16x16x32_bf16 v[78:81], v[114:117], v[226:229], v[78:81]
	v_mfma_f32_16x16x32_bf16 v[74:77], v[146:149], v[226:229], v[74:77]
	v_mfma_f32_16x16x32_bf16 v[134:137], v[126:129], v[162:165], v[134:137]
	v_mfma_f32_16x16x32_bf16 v[130:133], v[154:157], v[162:165], v[130:133]
	v_mfma_f32_16x16x32_bf16 v[102:105], v[126:129], v[174:177], v[102:105]
	v_mfma_f32_16x16x32_bf16 v[98:101], v[154:157], v[174:177], v[98:101]
	v_mfma_f32_16x16x32_bf16 v[86:89], v[126:129], v[182:185], v[86:89]
	v_mfma_f32_16x16x32_bf16 v[82:85], v[154:157], v[182:185], v[82:85]
	v_mfma_f32_16x16x32_bf16 v[70:73], v[126:129], v[190:193], v[70:73]
	v_mfma_f32_16x16x32_bf16 v[66:69], v[154:157], v[190:193], v[66:69]
	v_mfma_f32_16x16x32_bf16 v[134:137], v[150:153], v[170:173], v[134:137]
	v_mfma_f32_16x16x32_bf16 v[130:133], v[158:161], v[170:173], v[130:133]
	v_mfma_f32_16x16x32_bf16 v[102:105], v[150:153], v[178:181], v[102:105]
	v_mfma_f32_16x16x32_bf16 v[98:101], v[158:161], v[178:181], v[98:101]
	v_mfma_f32_16x16x32_bf16 v[86:89], v[150:153], v[186:189], v[86:89]
	v_mfma_f32_16x16x32_bf16 v[82:85], v[158:161], v[186:189], v[82:85]
	v_mfma_f32_16x16x32_bf16 v[70:73], v[150:153], v[226:229], v[70:73]
	v_mfma_f32_16x16x32_bf16 v[66:69], v[158:161], v[226:229], v[66:69]
	s_barrier
	s_mov_b32 m0, s71
	v_add_u32_e32 v194, s61, v196
	ds_read_b128 v[162:165], v222 offset:16384
	ds_read_b128 v[170:173], v222 offset:17408
	ds_read_b128 v[174:177], v222 offset:18432
	ds_read_b128 v[178:181], v222 offset:19456
	ds_read_b128 v[182:185], v222 offset:20480
	ds_read_b128 v[186:189], v222 offset:21504
	ds_read_b128 v[190:193], v222 offset:22528
	ds_read_b128 v[226:229], v222 offset:23552
	global_load_lds_dwordx4 v194, s[20:21]
	v_add_u32_e32 v194, s35, v194
	s_mov_b32 m0, s72
	s_nop 0
	global_load_lds_dwordx4 v194, s[20:21]
	v_add_u32_e32 v194, s61, v197
	s_mov_b32 m0, s73
	s_nop 0
	global_load_lds_dwordx4 v194, s[20:21]
	v_add_u32_e32 v194, s35, v194
	s_mov_b32 m0, s76
	s_nop 0
	global_load_lds_dwordx4 v194, s[20:21]
	v_add_u32_e32 v194, s60, v1
	s_mov_b32 m0, s70
	s_nop 0
	global_load_lds_dwordx4 v194, s[8:9]
	v_add_u32_e32 v194, s29, v194
	s_mov_b32 m0, s77
	s_nop 0
	global_load_lds_dwordx4 v194, s[8:9]
	s_waitcnt vmcnt(8)
	s_waitcnt lgkmcnt(0)
	s_barrier
	s_waitcnt lgkmcnt(0)
	v_mfma_f32_16x16x32_bf16 v[62:65], v[122:125], v[162:165], v[62:65]
	v_mfma_f32_16x16x32_bf16 v[58:61], v[118:121], v[162:165], v[58:61]
	v_mfma_f32_16x16x32_bf16 v[46:49], v[122:125], v[174:177], v[46:49]
	v_mfma_f32_16x16x32_bf16 v[42:45], v[118:121], v[174:177], v[42:45]
	v_mfma_f32_16x16x32_bf16 v[30:33], v[122:125], v[182:185], v[30:33]
	v_mfma_f32_16x16x32_bf16 v[26:29], v[118:121], v[182:185], v[26:29]
	v_mfma_f32_16x16x32_bf16 v[14:17], v[122:125], v[190:193], v[14:17]
	v_mfma_f32_16x16x32_bf16 v[10:13], v[118:121], v[190:193], v[10:13]
	v_mfma_f32_16x16x32_bf16 v[62:65], v[114:117], v[170:173], v[62:65]
	v_mfma_f32_16x16x32_bf16 v[58:61], v[146:149], v[170:173], v[58:61]
	v_mfma_f32_16x16x32_bf16 v[46:49], v[114:117], v[178:181], v[46:49]
	v_mfma_f32_16x16x32_bf16 v[42:45], v[146:149], v[178:181], v[42:45]
	v_mfma_f32_16x16x32_bf16 v[30:33], v[114:117], v[186:189], v[30:33]
	v_mfma_f32_16x16x32_bf16 v[26:29], v[146:149], v[186:189], v[26:29]
	v_mfma_f32_16x16x32_bf16 v[14:17], v[114:117], v[226:229], v[14:17]
	v_mfma_f32_16x16x32_bf16 v[10:13], v[146:149], v[226:229], v[10:13]
	v_mfma_f32_16x16x32_bf16 v[54:57], v[126:129], v[162:165], v[54:57]
	v_mfma_f32_16x16x32_bf16 v[50:53], v[154:157], v[162:165], v[50:53]
	v_mfma_f32_16x16x32_bf16 v[38:41], v[126:129], v[174:177], v[38:41]
	v_mfma_f32_16x16x32_bf16 v[34:37], v[154:157], v[174:177], v[34:37]
	v_mfma_f32_16x16x32_bf16 v[22:25], v[126:129], v[182:185], v[22:25]
	v_mfma_f32_16x16x32_bf16 v[18:21], v[154:157], v[182:185], v[18:21]
	v_mfma_f32_16x16x32_bf16 v[6:9], v[126:129], v[190:193], v[6:9]
	v_mfma_f32_16x16x32_bf16 v[2:5], v[154:157], v[190:193], v[2:5]
	v_mfma_f32_16x16x32_bf16 v[54:57], v[150:153], v[170:173], v[54:57]
	v_mfma_f32_16x16x32_bf16 v[50:53], v[158:161], v[170:173], v[50:53]
	v_mfma_f32_16x16x32_bf16 v[38:41], v[150:153], v[178:181], v[38:41]
	v_mfma_f32_16x16x32_bf16 v[34:37], v[158:161], v[178:181], v[34:37]
	v_mfma_f32_16x16x32_bf16 v[22:25], v[150:153], v[186:189], v[22:25]
	v_mfma_f32_16x16x32_bf16 v[18:21], v[158:161], v[186:189], v[18:21]
	v_mfma_f32_16x16x32_bf16 v[6:9], v[150:153], v[226:229], v[6:9]
	v_mfma_f32_16x16x32_bf16 v[2:5], v[158:161], v[226:229], v[2:5]
	s_barrier
.Lmid_4:
	ds_read_b128 v[114:117], v214
	ds_read_b128 v[118:121], v215
	ds_read_b128 v[122:125], v204
	ds_read_b128 v[126:129], v205
	ds_read_b128 v[146:149], v216
	ds_read_b128 v[150:153], v217
	ds_read_b128 v[154:157], v218
	ds_read_b128 v[158:161], v219
	s_mov_b32 m0, s78
	v_add_u32_e32 v194, s60, v198
	ds_read_b128 v[162:165], v222 offset:32768
	ds_read_b128 v[170:173], v222 offset:33792
	ds_read_b128 v[174:177], v222 offset:34816
	ds_read_b128 v[178:181], v222 offset:35840
	ds_read_b128 v[182:185], v222 offset:36864
	ds_read_b128 v[186:189], v222 offset:37888
	ds_read_b128 v[190:193], v222 offset:38912
	ds_read_b128 v[226:229], v222 offset:39936
	global_load_lds_dwordx4 v194, s[8:9]
	v_add_u32_e32 v194, s29, v194
	s_mov_b32 m0, s79
	s_nop 0
	global_load_lds_dwordx4 v194, s[8:9]
	s_waitcnt vmcnt(8)
	s_waitcnt lgkmcnt(0)
	s_barrier
	s_waitcnt lgkmcnt(0)
	v_mfma_f32_16x16x32_bf16 v[142:145], v[122:125], v[162:165], v[142:145]
	v_mfma_f32_16x16x32_bf16 v[138:141], v[118:121], v[162:165], v[138:141]
	v_mfma_f32_16x16x32_bf16 v[110:113], v[122:125], v[174:177], v[110:113]
	v_mfma_f32_16x16x32_bf16 v[106:109], v[118:121], v[174:177], v[106:109]
	v_mfma_f32_16x16x32_bf16 v[94:97], v[122:125], v[182:185], v[94:97]
	v_mfma_f32_16x16x32_bf16 v[90:93], v[118:121], v[182:185], v[90:93]
	v_mfma_f32_16x16x32_bf16 v[78:81], v[122:125], v[190:193], v[78:81]
	v_mfma_f32_16x16x32_bf16 v[74:77], v[118:121], v[190:193], v[74:77]
	v_mfma_f32_16x16x32_bf16 v[142:145], v[114:117], v[170:173], v[142:145]
	v_mfma_f32_16x16x32_bf16 v[138:141], v[146:149], v[170:173], v[138:141]
	v_mfma_f32_16x16x32_bf16 v[110:113], v[114:117], v[178:181], v[110:113]
	v_mfma_f32_16x16x32_bf16 v[106:109], v[146:149], v[178:181], v[106:109]
	v_mfma_f32_16x16x32_bf16 v[94:97], v[114:117], v[186:189], v[94:97]
	v_mfma_f32_16x16x32_bf16 v[90:93], v[146:149], v[186:189], v[90:93]
	v_mfma_f32_16x16x32_bf16 v[78:81], v[114:117], v[226:229], v[78:81]
	v_mfma_f32_16x16x32_bf16 v[74:77], v[146:149], v[226:229], v[74:77]
	v_mfma_f32_16x16x32_bf16 v[134:137], v[126:129], v[162:165], v[134:137]
	v_mfma_f32_16x16x32_bf16 v[130:133], v[154:157], v[162:165], v[130:133]
	v_mfma_f32_16x16x32_bf16 v[102:105], v[126:129], v[174:177], v[102:105]
	v_mfma_f32_16x16x32_bf16 v[98:101], v[154:157], v[174:177], v[98:101]
	v_mfma_f32_16x16x32_bf16 v[86:89], v[126:129], v[182:185], v[86:89]
	v_mfma_f32_16x16x32_bf16 v[82:85], v[154:157], v[182:185], v[82:85]
	v_mfma_f32_16x16x32_bf16 v[70:73], v[126:129], v[190:193], v[70:73]
	v_mfma_f32_16x16x32_bf16 v[66:69], v[154:157], v[190:193], v[66:69]
	v_mfma_f32_16x16x32_bf16 v[134:137], v[150:153], v[170:173], v[134:137]
	v_mfma_f32_16x16x32_bf16 v[130:133], v[158:161], v[170:173], v[130:133]
	v_mfma_f32_16x16x32_bf16 v[102:105], v[150:153], v[178:181], v[102:105]
	v_mfma_f32_16x16x32_bf16 v[98:101], v[158:161], v[178:181], v[98:101]
	v_mfma_f32_16x16x32_bf16 v[86:89], v[150:153], v[186:189], v[86:89]
	v_mfma_f32_16x16x32_bf16 v[82:85], v[158:161], v[186:189], v[82:85]
	v_mfma_f32_16x16x32_bf16 v[70:73], v[150:153], v[226:229], v[70:73]
	v_mfma_f32_16x16x32_bf16 v[66:69], v[158:161], v[226:229], v[66:69]
	s_barrier
	s_addk_i32 s61, 0x80
	s_mov_b32 m0, s81
	v_add_u32_e32 v194, s61, v196
	ds_read_b128 v[162:165], v222 offset:49152
	ds_read_b128 v[170:173], v222 offset:50176
	ds_read_b128 v[174:177], v222 offset:51200
	ds_read_b128 v[178:181], v222 offset:52224
	ds_read_b128 v[182:185], v222 offset:53248
	ds_read_b128 v[186:189], v222 offset:54272
	ds_read_b128 v[190:193], v222 offset:55296
	ds_read_b128 v[226:229], v222 offset:56320
	global_load_lds_dwordx4 v194, s[20:21]
	v_add_u32_e32 v194, s35, v194
	s_mov_b32 m0, s82
	s_nop 0
	global_load_lds_dwordx4 v194, s[20:21]
	v_add_u32_e32 v194, s61, v197
	s_mov_b32 m0, s85
	s_nop 0
	global_load_lds_dwordx4 v194, s[20:21]
	v_add_u32_e32 v194, s35, v194
	s_mov_b32 m0, s86
	s_nop 0
	global_load_lds_dwordx4 v194, s[20:21]
	v_add_u32_e32 v194, s60, v201
	s_mov_b32 m0, s83
	s_nop 0
	global_load_lds_dwordx4 v194, s[8:9]
	v_add_u32_e32 v194, s29, v194
	s_mov_b32 m0, s84
	s_nop 0
	global_load_lds_dwordx4 v194, s[8:9]
	s_waitcnt vmcnt(8)
	s_waitcnt lgkmcnt(0)
	s_barrier
	s_waitcnt lgkmcnt(0)
	v_mfma_f32_16x16x32_bf16 v[62:65], v[122:125], v[162:165], v[62:65]
	v_mfma_f32_16x16x32_bf16 v[58:61], v[118:121], v[162:165], v[58:61]
	v_mfma_f32_16x16x32_bf16 v[46:49], v[122:125], v[174:177], v[46:49]
	v_mfma_f32_16x16x32_bf16 v[42:45], v[118:121], v[174:177], v[42:45]
	v_mfma_f32_16x16x32_bf16 v[30:33], v[122:125], v[182:185], v[30:33]
	v_mfma_f32_16x16x32_bf16 v[26:29], v[118:121], v[182:185], v[26:29]
	v_mfma_f32_16x16x32_bf16 v[14:17], v[122:125], v[190:193], v[14:17]
	v_mfma_f32_16x16x32_bf16 v[10:13], v[118:121], v[190:193], v[10:13]
	v_mfma_f32_16x16x32_bf16 v[62:65], v[114:117], v[170:173], v[62:65]
	v_mfma_f32_16x16x32_bf16 v[58:61], v[146:149], v[170:173], v[58:61]
	v_mfma_f32_16x16x32_bf16 v[46:49], v[114:117], v[178:181], v[46:49]
	v_mfma_f32_16x16x32_bf16 v[42:45], v[146:149], v[178:181], v[42:45]
	v_mfma_f32_16x16x32_bf16 v[30:33], v[114:117], v[186:189], v[30:33]
	v_mfma_f32_16x16x32_bf16 v[26:29], v[146:149], v[186:189], v[26:29]
	v_mfma_f32_16x16x32_bf16 v[14:17], v[114:117], v[226:229], v[14:17]
	v_mfma_f32_16x16x32_bf16 v[10:13], v[146:149], v[226:229], v[10:13]
	v_mfma_f32_16x16x32_bf16 v[54:57], v[126:129], v[162:165], v[54:57]
	v_mfma_f32_16x16x32_bf16 v[50:53], v[154:157], v[162:165], v[50:53]
	v_mfma_f32_16x16x32_bf16 v[38:41], v[126:129], v[174:177], v[38:41]
	v_mfma_f32_16x16x32_bf16 v[34:37], v[154:157], v[174:177], v[34:37]
	v_mfma_f32_16x16x32_bf16 v[22:25], v[126:129], v[182:185], v[22:25]
	v_mfma_f32_16x16x32_bf16 v[18:21], v[154:157], v[182:185], v[18:21]
	v_mfma_f32_16x16x32_bf16 v[6:9], v[126:129], v[190:193], v[6:9]
	v_mfma_f32_16x16x32_bf16 v[2:5], v[154:157], v[190:193], v[2:5]
	v_mfma_f32_16x16x32_bf16 v[54:57], v[150:153], v[170:173], v[54:57]
	v_mfma_f32_16x16x32_bf16 v[50:53], v[158:161], v[170:173], v[50:53]
	v_mfma_f32_16x16x32_bf16 v[38:41], v[150:153], v[178:181], v[38:41]
	v_mfma_f32_16x16x32_bf16 v[34:37], v[158:161], v[178:181], v[34:37]
	v_mfma_f32_16x16x32_bf16 v[22:25], v[150:153], v[186:189], v[22:25]
	v_mfma_f32_16x16x32_bf16 v[18:21], v[158:161], v[186:189], v[18:21]
	v_mfma_f32_16x16x32_bf16 v[6:9], v[150:153], v[226:229], v[6:9]
	v_mfma_f32_16x16x32_bf16 v[2:5], v[158:161], v[226:229], v[2:5]
	s_barrier
	s_add_i32 s59, s59, 2
	s_addk_i32 s6, 0x100
	s_addk_i32 s58, 0x100
	s_cmp_ge_i32 s59, s87
	s_cbranch_scc0 .LBB0_1183

.LBB0_1333:
	s_setprio 0
	s_cmp_lt_i32 s41, 11
	s_cbranch_scc1 .LBB0_1383
	s_waitcnt vmcnt(0)
	v_cmp_eq_u32_e32 vcc, 0, v0
	s_waitcnt vmcnt(0) lgkmcnt(0)
	s_barrier
	s_and_saveexec_b64 s[2:3], vcc
	s_cbranch_execz .LBB0_1382
	v_mov_b32_e32 v1, s92
	s_waitcnt vmcnt(0) expcnt(0) lgkmcnt(0)
	ds_read_b32 v3, v1
	ds_read_b32 v1, v1 offset:4
	s_waitcnt lgkmcnt(1)
	v_cmp_ne_u32_e32 vcc, 0, v3
	s_cbranch_vccnz .LBB0_1350
	v_readlane_b32 s4, v254, 1
	v_readlane_b32 s5, v254, 2
	s_load_dwordx2 s[8:9], s[4:5], 0x4
	s_add_u32 s4, s42, 0x1000
	s_addc_u32 s5, s43, 0
	s_add_u32 s6, s42, 0x1100
	s_addc_u32 s7, s43, 0
	s_waitcnt lgkmcnt(0)
	s_mul_i32 s18, s8, s34
	s_add_u32 s8, s42, 0x1200
	s_mul_i32 s18, s18, s9
	s_addc_u32 s9, s43, 0
	s_add_u32 s10, s42, 0x1300
	s_addc_u32 s11, s43, 0
	s_mov_b32 s19, 1
	v_mov_b32_e32 v17, 0
	s_branch .LBB0_1338

.LBB0_1383:
.LBB0_1384:
	s_cmp_gt_i32 s40, 11
	s_cselect_b64 s[2:3], -1, 0
	s_cmp_lt_i32 s41, 12
	s_cselect_b64 s[4:5], -1, 0
	s_or_b64 s[2:3], s[2:3], s[4:5]
	s_and_b64 vcc, exec, s[2:3]
	s_cbranch_vccnz .LBB0_1590
	s_cmp_ge_u32 s27, 4
	s_cbranch_scc0 .Lsp_11
	s_setprio 1
.Lsp_11:
	s_add_u32 s20, s38, 0x2800000
	s_addc_u32 s21, s39, 0
	v_mov_b32_e32 v2, v0
	s_movk_i32 s3, 0x400
	v_readfirstlane_b32 s2, v2
	s_movk_i32 s74, 0x400
	s_movk_i32 s4, 0x400
	s_cmpk_gt_i32 s26, 0x16af
	s_cbranch_scc1 .LBB0_1412
	s_add_u32 s25, s38, 0xa4a00000
	s_addc_u32 s35, s39, 0
	s_ashr_i32 s44, s26, 31
	s_lshr_b32 s5, s44, 29
	s_add_i32 s5, s26, s5
	s_ashr_i32 s6, s5, 3
	s_and_b32 s5, s5, -8
	s_sub_i32 s5, s26, s5
	s_cmp_lt_i32 s5, 0
	s_movk_i32 s7, 0x2d7
	s_cselect_b32 s7, s7, 0x2d6
	s_mul_i32 s5, s5, s7
	s_add_i32 s5, s5, s6
	s_mul_hi_i32 s6, s5, 0x2e8ba2e9
	s_lshr_b32 s7, s6, 31
	s_ashr_i32 s6, s6, 6
	s_add_i32 s6, s6, s7
	s_lshl_b32 s8, s6, 3
	s_sub_i32 s7, 0x84, s8
	s_min_u32 s9, s7, 8
	s_mulk_i32 s6, 0x160
	s_sub_i32 s5, s5, s6
	v_cvt_f32_ubyte0_e32 v4, s9
	v_cvt_f32_i32_e32 v1, s5
	v_rcp_iflag_f32_e32 v5, v4
	s_ashr_i32 s6, s5, 30
	s_or_b32 s10, s6, 1
	s_waitcnt lgkmcnt(0)
	v_and_b32_e32 v3, 63, v2
	v_mul_f32_e32 v5, v1, v5
	v_trunc_f32_e32 v5, v5
	v_fma_f32 v1, -v5, v4, v1
	v_cvt_i32_f32_e32 v5, v5
	v_cmp_ge_f32_e64 s[6:7], |v1|, v4
	s_and_b64 s[6:7], s[6:7], exec
	s_cselect_b32 s6, s10, 0
	v_readfirstlane_b32 s7, v5
	s_add_i32 s6, s7, s6
	s_mul_i32 s7, s6, s9
	s_sub_i32 s5, s5, s7
	s_sext_i32_i16 s5, s5
	s_add_i32 s8, s8, s5
	s_cmp_gt_u32 s2, 63
	s_sext_i32_i16 s90, s6
	s_cselect_b64 s[6:7], -1, 0
	s_and_b64 vcc, exec, s[6:7]
	v_lshrrev_b32_e32 v4, 5, v3
	s_cbranch_vccnz .LBB0_1388
	s_min_i32 s5, s8, 0x80
	s_mul_hi_i32 s9, s90, 0x2e8ba2e9
	s_lshr_b32 s5, s5, 5
	s_lshr_b32 s10, s9, 31
	s_lshr_b32 s9, s9, 3
	s_add_i32 s9, s9, s10
	s_mul_i32 s10, s5, 0x2c00
	s_mul_i32 s9, s9, 44
	s_ashr_i32 s11, s10, 31
	s_sub_i32 s9, s90, s9
	s_lshl_b64 s[10:11], s[10:11], 2
	s_add_u32 s5, s25, s10
	s_addc_u32 s12, s35, s11
	s_lshl_b32 s10, s9, 7
	s_ashr_i32 s11, s10, 31
	s_lshl_b64 s[10:11], s[10:11], 2
	s_add_u32 s10, s5, s10
	v_lshlrev_b32_e32 v1, 4, v3
	s_addc_u32 s11, s12, s11
	v_and_b32_e32 v6, 0x1f0, v1
	v_mov_b32_e32 v7, 0
	v_mul_u32_u24_e32 v1, 0x1600, v4
	v_lshl_add_u64 v[8:9], s[10:11], 0, v[6:7]
	v_lshlrev_b32_e32 v6, 2, v1
	v_lshl_add_u64 v[6:7], v[8:9], 0, v[6:7]
	s_add_i32 m0, 0, 0x21400
	s_nop 0
	global_load_lds_dwordx4 v[6:7], off

.Lphr_0:
	ds_read_b128 v[18:21], v177
	ds_read_b128 v[22:25], v178
	ds_read_b128 v[26:29], v185
	ds_read_b128 v[30:33], v186
	ds_read_b128 v[2:5], v179
	ds_read_b128 v[6:9], v180
	ds_read_b128 v[10:13], v187
	ds_read_b128 v[14:17], v188
	s_add_i32 s75, s92, 0x80
	s_and_b64 s[30:31], s[30:31], exec
	s_cselect_b32 s75, s75, s91
	s_cselect_b32 s96, s93, s29
	s_add_i32 s30, s75, 0x80
	s_add_i32 s31, s96, 0x80
	v_mov_b32_e32 v162, v1
	ds_read_b128 v[198:201], v193
	ds_read_b128 v[202:205], v193 offset:1024
	ds_read_b128 v[214:217], v193 offset:2048
	ds_read_b128 v[218:221], v193 offset:3072
	ds_read_b128 v[222:225], v193 offset:4096
	ds_read_b128 v[226:229], v193 offset:5120
	ds_read_b128 v[230:233], v193 offset:6144
	ds_read_b128 v[234:237], v193 offset:7168
	s_add_i32 s97, s92, s65
	v_add_u32_e32 v162, s97, v162
	s_add_i32 m0, s47, 0xc000
	s_add_i32 s97, s92, s74
	global_load_lds_dwordx4 v162, s[10:11]
	v_mov_b32_e32 v162, v1
	s_add_i32 m0, s47, 0xe000
	v_add_u32_e32 v162, s97, v162
	global_load_lds_dwordx4 v162, s[10:11]
	s_waitcnt vmcnt(8)
	s_waitcnt lgkmcnt(0)
	s_barrier
	s_waitcnt lgkmcnt(0)
	v_mfma_f32_16x16x128_f8f6f4 v[158:161], v[18:25], v[198:205], 0
	v_mfma_f32_16x16x128_f8f6f4 v[150:153], v[26:33], v[198:205], 0
	v_mfma_f32_16x16x128_f8f6f4 v[142:145], v[18:25], v[214:221], 0
	v_mfma_f32_16x16x128_f8f6f4 v[134:137], v[26:33], v[214:221], 0
	v_mfma_f32_16x16x128_f8f6f4 v[126:129], v[18:25], v[222:229], 0
	v_mfma_f32_16x16x128_f8f6f4 v[118:121], v[26:33], v[222:229], 0
	v_mfma_f32_16x16x128_f8f6f4 v[110:113], v[18:25], v[230:237], 0
	v_mfma_f32_16x16x128_f8f6f4 v[102:105], v[26:33], v[230:237], 0
	v_mfma_f32_16x16x128_f8f6f4 v[154:157], v[2:9], v[198:205], 0
	v_mfma_f32_16x16x128_f8f6f4 v[146:149], v[10:17], v[198:205], 0
	v_mfma_f32_16x16x128_f8f6f4 v[138:141], v[2:9], v[214:221], 0
	v_mfma_f32_16x16x128_f8f6f4 v[130:133], v[10:17], v[214:221], 0
	v_mfma_f32_16x16x128_f8f6f4 v[122:125], v[2:9], v[222:229], 0
	v_mfma_f32_16x16x128_f8f6f4 v[114:117], v[10:17], v[222:229], 0
	v_mfma_f32_16x16x128_f8f6f4 v[106:109], v[2:9], v[230:237], 0
	v_mfma_f32_16x16x128_f8f6f4 v[98:101], v[10:17], v[230:237], 0
	s_barrier
	v_mov_b32_e32 v162, v174
	ds_read_b128 v[198:201], v193 offset:16384
	ds_read_b128 v[202:205], v193 offset:17408
	ds_read_b128 v[214:217], v193 offset:18432
	ds_read_b128 v[218:221], v193 offset:19456
	ds_read_b128 v[222:225], v193 offset:20480
	ds_read_b128 v[226:229], v193 offset:21504
	ds_read_b128 v[230:233], v193 offset:22528
	ds_read_b128 v[234:237], v193 offset:23552
	s_mov_b32 m0, s48
	v_add_u32_e32 v162, s96, v162
	global_load_lds_dwordx4 v162, s[20:21]
	v_mov_b32_e32 v162, v174
	s_add_i32 s96, s96, s46
	v_add_u32_e32 v162, s96, v162
	s_mov_b32 m0, s49
	s_add_i32 s96, s96, s46
	global_load_lds_dwordx4 v162, s[20:21]
	v_mov_b32_e32 v162, v174
	s_mov_b32 m0, s50
	v_add_u32_e32 v162, s96, v162
	global_load_lds_dwordx4 v162, s[20:21]
	v_mov_b32_e32 v162, v174
	s_add_i32 s96, s96, s46
	v_add_u32_e32 v162, s96, v162
	s_mov_b32 m0, s51
	s_nop 0
	global_load_lds_dwordx4 v162, s[20:21]
	v_mov_b32_e32 v162, v1
	s_mov_b32 m0, s47
	v_add_u32_e32 v162, s75, v162
	global_load_lds_dwordx4 v162, s[10:11]
	v_mov_b32_e32 v162, v1
	s_add_i32 s75, s75, s45
	v_add_u32_e32 v162, s75, v162
	s_mov_b32 m0, s52
	s_nop 0
	global_load_lds_dwordx4 v162, s[10:11]
	s_waitcnt vmcnt(8)
	s_waitcnt lgkmcnt(0)
	s_barrier
	s_waitcnt lgkmcnt(0)
	v_mfma_f32_16x16x128_f8f6f4 v[94:97], v[18:25], v[198:205], 0
	v_mfma_f32_16x16x128_f8f6f4 v[86:89], v[26:33], v[198:205], 0
	v_mfma_f32_16x16x128_f8f6f4 v[78:81], v[18:25], v[214:221], 0
	v_mfma_f32_16x16x128_f8f6f4 v[70:73], v[26:33], v[214:221], 0
	v_mfma_f32_16x16x128_f8f6f4 v[62:65], v[18:25], v[222:229], 0
	v_mfma_f32_16x16x128_f8f6f4 v[54:57], v[26:33], v[222:229], 0
	v_mfma_f32_16x16x128_f8f6f4 v[46:49], v[18:25], v[230:237], 0
	v_mfma_f32_16x16x128_f8f6f4 v[38:41], v[26:33], v[230:237], 0
	v_mfma_f32_16x16x128_f8f6f4 v[90:93], v[2:9], v[198:205], 0
	v_mfma_f32_16x16x128_f8f6f4 v[82:85], v[10:17], v[198:205], 0
	v_mfma_f32_16x16x128_f8f6f4 v[74:77], v[2:9], v[214:221], 0
	v_mfma_f32_16x16x128_f8f6f4 v[66:69], v[10:17], v[214:221], 0
	v_mfma_f32_16x16x128_f8f6f4 v[58:61], v[2:9], v[222:229], 0
	v_mfma_f32_16x16x128_f8f6f4 v[50:53], v[10:17], v[222:229], 0
	v_mfma_f32_16x16x128_f8f6f4 v[42:45], v[2:9], v[230:237], 0
	v_mfma_f32_16x16x128_f8f6f4 v[34:37], v[10:17], v[230:237], 0
	s_barrier
	s_branch .Lmidr_0
.LBB0_1397:
	ds_read_b128 v[18:21], v177
	ds_read_b128 v[22:25], v178
	ds_read_b128 v[26:29], v185
	ds_read_b128 v[30:33], v186
	ds_read_b128 v[2:5], v179
	ds_read_b128 v[6:9], v180
	ds_read_b128 v[10:13], v187
	ds_read_b128 v[14:17], v188
	s_add_i32 s75, s92, 0x80
	s_and_b64 s[30:31], s[30:31], exec
	s_cselect_b32 s75, s75, s91
	s_cselect_b32 s96, s93, s29
	s_add_i32 s30, s75, 0x80
	s_add_i32 s31, s96, 0x80
	v_mov_b32_e32 v162, v1
	ds_read_b128 v[198:201], v193
	ds_read_b128 v[202:205], v193 offset:1024
	ds_read_b128 v[214:217], v193 offset:2048
	ds_read_b128 v[218:221], v193 offset:3072
	ds_read_b128 v[222:225], v193 offset:4096
	ds_read_b128 v[226:229], v193 offset:5120
	ds_read_b128 v[230:233], v193 offset:6144
	ds_read_b128 v[234:237], v193 offset:7168
	s_add_i32 s97, s92, s65
	v_add_u32_e32 v162, s97, v162
	s_add_i32 m0, s47, 0xc000
	s_add_i32 s97, s92, s74
	global_load_lds_dwordx4 v162, s[10:11]
	v_mov_b32_e32 v162, v1
	s_add_i32 m0, s47, 0xe000
	v_add_u32_e32 v162, s97, v162
	global_load_lds_dwordx4 v162, s[10:11]
	s_waitcnt vmcnt(8)
	s_waitcnt lgkmcnt(0)
	s_barrier
	s_waitcnt lgkmcnt(0)
	v_mfma_f32_16x16x128_f8f6f4 v[158:161], v[18:25], v[198:205], v[158:161]
	v_mfma_f32_16x16x128_f8f6f4 v[150:153], v[26:33], v[198:205], v[150:153]
	v_mfma_f32_16x16x128_f8f6f4 v[142:145], v[18:25], v[214:221], v[142:145]
	v_mfma_f32_16x16x128_f8f6f4 v[134:137], v[26:33], v[214:221], v[134:137]
	v_mfma_f32_16x16x128_f8f6f4 v[126:129], v[18:25], v[222:229], v[126:129]
	v_mfma_f32_16x16x128_f8f6f4 v[118:121], v[26:33], v[222:229], v[118:121]
	v_mfma_f32_16x16x128_f8f6f4 v[110:113], v[18:25], v[230:237], v[110:113]
	v_mfma_f32_16x16x128_f8f6f4 v[102:105], v[26:33], v[230:237], v[102:105]
	v_mfma_f32_16x16x128_f8f6f4 v[154:157], v[2:9], v[198:205], v[154:157]
	v_mfma_f32_16x16x128_f8f6f4 v[146:149], v[10:17], v[198:205], v[146:149]
	v_mfma_f32_16x16x128_f8f6f4 v[138:141], v[2:9], v[214:221], v[138:141]
	v_mfma_f32_16x16x128_f8f6f4 v[130:133], v[10:17], v[214:221], v[130:133]
	v_mfma_f32_16x16x128_f8f6f4 v[122:125], v[2:9], v[222:229], v[122:125]
	v_mfma_f32_16x16x128_f8f6f4 v[114:117], v[10:17], v[222:229], v[114:117]
	v_mfma_f32_16x16x128_f8f6f4 v[106:109], v[2:9], v[230:237], v[106:109]
	v_mfma_f32_16x16x128_f8f6f4 v[98:101], v[10:17], v[230:237], v[98:101]
	s_barrier
	v_mov_b32_e32 v162, v174
	ds_read_b128 v[198:201], v193 offset:16384
	ds_read_b128 v[202:205], v193 offset:17408
	ds_read_b128 v[214:217], v193 offset:18432
	ds_read_b128 v[218:221], v193 offset:19456
	ds_read_b128 v[222:225], v193 offset:20480
	ds_read_b128 v[226:229], v193 offset:21504
	ds_read_b128 v[230:233], v193 offset:22528
	ds_read_b128 v[234:237], v193 offset:23552
	s_mov_b32 m0, s48
	v_add_u32_e32 v162, s96, v162
	global_load_lds_dwordx4 v162, s[20:21]
	v_mov_b32_e32 v162, v174
	s_add_i32 s96, s96, s46
	v_add_u32_e32 v162, s96, v162
	s_mov_b32 m0, s49
	s_add_i32 s96, s96, s46
	global_load_lds_dwordx4 v162, s[20:21]
	v_mov_b32_e32 v162, v174
	s_mov_b32 m0, s50
	v_add_u32_e32 v162, s96, v162
	global_load_lds_dwordx4 v162, s[20:21]
	v_mov_b32_e32 v162, v174
	s_add_i32 s96, s96, s46
	v_add_u32_e32 v162, s96, v162
	s_mov_b32 m0, s51
	s_nop 0
	global_load_lds_dwordx4 v162, s[20:21]
	v_mov_b32_e32 v162, v1
	s_mov_b32 m0, s47
	v_add_u32_e32 v162, s75, v162
	global_load_lds_dwordx4 v162, s[10:11]
	v_mov_b32_e32 v162, v1
	s_add_i32 s75, s75, s45
	v_add_u32_e32 v162, s75, v162
	s_mov_b32 m0, s52
	s_nop 0
	global_load_lds_dwordx4 v162, s[10:11]
	s_waitcnt vmcnt(8)
	s_waitcnt lgkmcnt(0)
	s_barrier
	s_waitcnt lgkmcnt(0)
	v_mfma_f32_16x16x128_f8f6f4 v[94:97], v[18:25], v[198:205], v[94:97]
	v_mfma_f32_16x16x128_f8f6f4 v[86:89], v[26:33], v[198:205], v[86:89]
	v_mfma_f32_16x16x128_f8f6f4 v[78:81], v[18:25], v[214:221], v[78:81]
	v_mfma_f32_16x16x128_f8f6f4 v[70:73], v[26:33], v[214:221], v[70:73]
	v_mfma_f32_16x16x128_f8f6f4 v[62:65], v[18:25], v[222:229], v[62:65]
	v_mfma_f32_16x16x128_f8f6f4 v[54:57], v[26:33], v[222:229], v[54:57]
	v_mfma_f32_16x16x128_f8f6f4 v[46:49], v[18:25], v[230:237], v[46:49]
	v_mfma_f32_16x16x128_f8f6f4 v[38:41], v[26:33], v[230:237], v[38:41]
	v_mfma_f32_16x16x128_f8f6f4 v[90:93], v[2:9], v[198:205], v[90:93]
	v_mfma_f32_16x16x128_f8f6f4 v[82:85], v[10:17], v[198:205], v[82:85]
	v_mfma_f32_16x16x128_f8f6f4 v[74:77], v[2:9], v[214:221], v[74:77]
	v_mfma_f32_16x16x128_f8f6f4 v[66:69], v[10:17], v[214:221], v[66:69]
	v_mfma_f32_16x16x128_f8f6f4 v[58:61], v[2:9], v[222:229], v[58:61]
	v_mfma_f32_16x16x128_f8f6f4 v[50:53], v[10:17], v[222:229], v[50:53]
	v_mfma_f32_16x16x128_f8f6f4 v[42:45], v[2:9], v[230:237], v[42:45]
	v_mfma_f32_16x16x128_f8f6f4 v[34:37], v[10:17], v[230:237], v[34:37]
	s_barrier
.Lmidr_0:
	ds_read_b128 v[2:5], v181
	ds_read_b128 v[6:9], v182
	ds_read_b128 v[10:13], v189
	ds_read_b128 v[14:17], v190
	ds_read_b128 v[18:21], v183
	ds_read_b128 v[22:25], v184
	ds_read_b128 v[26:29], v191
	ds_read_b128 v[30:33], v192
	v_mov_b32_e32 v162, v1
	ds_read_b128 v[198:201], v193 offset:32768
	ds_read_b128 v[202:205], v193 offset:33792
	ds_read_b128 v[214:217], v193 offset:34816
	ds_read_b128 v[218:221], v193 offset:35840
	ds_read_b128 v[222:225], v193 offset:36864
	ds_read_b128 v[226:229], v193 offset:37888
	ds_read_b128 v[230:233], v193 offset:38912
	ds_read_b128 v[234:237], v193 offset:39936
	s_add_i32 s75, s75, s45
	s_mov_b32 m0, s53
	v_add_u32_e32 v162, s75, v162
	global_load_lds_dwordx4 v162, s[10:11]
	v_mov_b32_e32 v162, v1
	s_add_i32 s75, s75, s45
	v_add_u32_e32 v162, s75, v162
	s_mov_b32 m0, s54
	s_nop 0
	global_load_lds_dwordx4 v162, s[10:11]
	s_waitcnt vmcnt(8)
	s_waitcnt lgkmcnt(0)
	s_barrier
	s_waitcnt lgkmcnt(0)
	v_mfma_f32_16x16x128_f8f6f4 v[158:161], v[2:9], v[198:205], v[158:161]
	v_mfma_f32_16x16x128_f8f6f4 v[150:153], v[10:17], v[198:205], v[150:153]
	v_mfma_f32_16x16x128_f8f6f4 v[142:145], v[2:9], v[214:221], v[142:145]
	v_mfma_f32_16x16x128_f8f6f4 v[134:137], v[10:17], v[214:221], v[134:137]
	v_mfma_f32_16x16x128_f8f6f4 v[126:129], v[2:9], v[222:229], v[126:129]
	v_mfma_f32_16x16x128_f8f6f4 v[118:121], v[10:17], v[222:229], v[118:121]
	v_mfma_f32_16x16x128_f8f6f4 v[110:113], v[2:9], v[230:237], v[110:113]
	v_mfma_f32_16x16x128_f8f6f4 v[102:105], v[10:17], v[230:237], v[102:105]
	v_mfma_f32_16x16x128_f8f6f4 v[154:157], v[18:25], v[198:205], v[154:157]
	v_mfma_f32_16x16x128_f8f6f4 v[146:149], v[26:33], v[198:205], v[146:149]
	v_mfma_f32_16x16x128_f8f6f4 v[138:141], v[18:25], v[214:221], v[138:141]
	v_mfma_f32_16x16x128_f8f6f4 v[130:133], v[26:33], v[214:221], v[130:133]
	v_mfma_f32_16x16x128_f8f6f4 v[122:125], v[18:25], v[222:229], v[122:125]
	v_mfma_f32_16x16x128_f8f6f4 v[114:117], v[26:33], v[222:229], v[114:117]
	v_mfma_f32_16x16x128_f8f6f4 v[106:109], v[18:25], v[230:237], v[106:109]
	v_mfma_f32_16x16x128_f8f6f4 v[98:101], v[26:33], v[230:237], v[98:101]
	s_barrier
	v_mov_b32_e32 v162, v174
	ds_read_b128 v[198:201], v193 offset:49152
	ds_read_b128 v[202:205], v193 offset:50176
	ds_read_b128 v[214:217], v193 offset:51200
	ds_read_b128 v[218:221], v193 offset:52224
	ds_read_b128 v[222:225], v193 offset:53248
	ds_read_b128 v[226:229], v193 offset:54272
	ds_read_b128 v[230:233], v193 offset:55296
	ds_read_b128 v[234:237], v193 offset:56320
	s_mov_b32 m0, s58
	v_add_u32_e32 v162, s31, v162
	global_load_lds_dwordx4 v162, s[20:21]
	v_mov_b32_e32 v162, v174
	s_add_i32 s31, s31, s46
	v_add_u32_e32 v162, s31, v162
	s_mov_b32 m0, s59
	s_add_i32 s31, s31, s46
	global_load_lds_dwordx4 v162, s[20:21]
	v_mov_b32_e32 v162, v174
	s_mov_b32 m0, s62
	v_add_u32_e32 v162, s31, v162
	global_load_lds_dwordx4 v162, s[20:21]
	v_mov_b32_e32 v162, v174
	s_add_i32 s31, s31, s46
	v_add_u32_e32 v162, s31, v162
	s_mov_b32 m0, s63
	s_nop 0
	global_load_lds_dwordx4 v162, s[20:21]
	v_mov_b32_e32 v162, v1
	s_mov_b32 m0, s60
	v_add_u32_e32 v162, s30, v162
	global_load_lds_dwordx4 v162, s[10:11]
	v_mov_b32_e32 v162, v1
	s_add_i32 s30, s30, s45
	v_add_u32_e32 v162, s30, v162
	s_mov_b32 m0, s61
	s_nop 0
	global_load_lds_dwordx4 v162, s[10:11]
	s_waitcnt vmcnt(8)
	s_waitcnt lgkmcnt(0)
	s_barrier
	s_waitcnt lgkmcnt(0)
	v_mfma_f32_16x16x128_f8f6f4 v[94:97], v[2:9], v[198:205], v[94:97]
	v_mfma_f32_16x16x128_f8f6f4 v[86:89], v[10:17], v[198:205], v[86:89]
	v_mfma_f32_16x16x128_f8f6f4 v[78:81], v[2:9], v[214:221], v[78:81]
	v_mfma_f32_16x16x128_f8f6f4 v[70:73], v[10:17], v[214:221], v[70:73]
	v_mfma_f32_16x16x128_f8f6f4 v[62:65], v[2:9], v[222:229], v[62:65]
	v_mfma_f32_16x16x128_f8f6f4 v[54:57], v[10:17], v[222:229], v[54:57]
	v_mfma_f32_16x16x128_f8f6f4 v[46:49], v[2:9], v[230:237], v[46:49]
	v_mfma_f32_16x16x128_f8f6f4 v[38:41], v[10:17], v[230:237], v[38:41]
	v_mfma_f32_16x16x128_f8f6f4 v[90:93], v[18:25], v[198:205], v[90:93]
	v_mfma_f32_16x16x128_f8f6f4 v[82:85], v[26:33], v[198:205], v[82:85]
	v_mfma_f32_16x16x128_f8f6f4 v[74:77], v[18:25], v[214:221], v[74:77]
	v_mfma_f32_16x16x128_f8f6f4 v[66:69], v[26:33], v[214:221], v[66:69]
	v_mfma_f32_16x16x128_f8f6f4 v[58:61], v[18:25], v[222:229], v[58:61]
	v_mfma_f32_16x16x128_f8f6f4 v[50:53], v[26:33], v[222:229], v[50:53]
	v_mfma_f32_16x16x128_f8f6f4 v[42:45], v[18:25], v[230:237], v[42:45]
	v_mfma_f32_16x16x128_f8f6f4 v[34:37], v[26:33], v[230:237], v[34:37]
	s_barrier
	s_add_i32 s94, s94, 2
	s_addk_i32 s92, 0x100
	s_addk_i32 s93, 0x100
	s_cmp_ge_i32 s94, s64
	s_cbranch_scc1 .LBB0_1400

.LBB0_1539:
	s_setprio 0
	s_cmp_lt_i32 s41, 13
	s_cbranch_scc1 .LBB0_1589
	s_waitcnt vmcnt(0)
	v_cmp_eq_u32_e32 vcc, 0, v0
	s_waitcnt vmcnt(0) lgkmcnt(0)
	s_barrier
	s_and_saveexec_b64 s[2:3], vcc
	s_cbranch_execz .LBB0_1588
	v_mov_b32_e32 v1, s92
	s_waitcnt vmcnt(0) expcnt(0) lgkmcnt(0)
	ds_read_b32 v3, v1
	ds_read_b32 v1, v1 offset:4
	s_waitcnt lgkmcnt(1)
	v_cmp_ne_u32_e32 vcc, 0, v3
	s_cbranch_vccnz .LBB0_1556
	v_readlane_b32 s4, v254, 1
	v_readlane_b32 s5, v254, 2
	s_load_dwordx2 s[8:9], s[4:5], 0x4
	s_add_u32 s4, s42, 0x1000
	s_addc_u32 s5, s43, 0
	s_add_u32 s6, s42, 0x1100
	s_addc_u32 s7, s43, 0
	s_waitcnt lgkmcnt(0)
	s_mul_i32 s18, s8, s34
	s_add_u32 s8, s42, 0x1200
	s_mul_i32 s18, s18, s9
	s_addc_u32 s9, s43, 0
	s_add_u32 s10, s42, 0x1300
	s_addc_u32 s11, s43, 0
	s_mov_b32 s19, 1
	v_mov_b32_e32 v17, 0
	s_branch .LBB0_1544

.Lstag12_done:
	s_cmp_gt_i32 s40, 12
	s_cselect_b64 s[2:3], -1, 0
	s_cmp_lt_i32 s41, 13
	s_cselect_b64 s[4:5], -1, 0
	s_or_b64 s[2:3], s[2:3], s[4:5]
	s_and_b64 vcc, exec, s[2:3]
	s_cbranch_vccnz .LBB0_1820
	s_cmp_ge_u32 s27, 4
	s_cbranch_scc0 .Lsp_12
	s_setprio 1
.Lsp_12:
	v_mov_b32_e32 v2, v0
	s_cmpk_lt_i32 s26, 0x420
	s_movk_i32 s6, 0xb00
	v_readfirstlane_b32 s5, v2
	s_movk_i32 s93, 0xb00
	s_movk_i32 s7, 0xb00
	s_cselect_b64 s[2:3], -1, 0
	s_cmpk_gt_i32 s26, 0x41f
	s_cbranch_scc1 .LBB0_1593
	s_ashr_i32 s4, s26, 31
	s_lshr_b32 s4, s4, 29
	s_add_i32 s4, s26, s4
	s_ashr_i32 s8, s4, 3
	s_and_b32 s4, s4, -8
	s_sub_i32 s4, s26, s4
	s_cmp_lt_i32 s4, 0
	s_movk_i32 s9, 0x85
	s_cselect_b32 s9, s9, 0x84
	s_mul_i32 s4, s4, s9
	s_add_i32 s4, s4, s8
	s_ashr_i32 s8, s4, 31
	s_lshr_b32 s8, s8, 26
	s_add_i32 s8, s4, s8
	s_ashr_i32 s9, s8, 6
	s_lshl_b32 s10, s9, 3
	s_sub_i32 s9, 0x84, s10
	s_min_u32 s11, s9, 8
	s_andn2_b32 s8, s8, 63
	s_sub_i32 s4, s4, s8
	s_waitcnt lgkmcnt(0)
	v_cvt_f32_ubyte0_e32 v3, s11
	v_cvt_f32_i32_e32 v1, s4
	v_rcp_iflag_f32_e32 v4, v3
	s_ashr_i32 s8, s4, 30
	s_or_b32 s12, s8, 1
	v_mul_f32_e32 v4, v1, v4
	v_trunc_f32_e32 v4, v4
	v_fma_f32 v1, -v4, v3, v1
	v_cvt_i32_f32_e32 v4, v4
	v_cmp_ge_f32_e64 s[8:9], |v1|, v3
	s_and_b64 s[8:9], s[8:9], exec
	s_cselect_b32 s8, s12, 0
	v_readfirstlane_b32 s9, v4
	s_add_i32 s8, s9, s8
	s_mul_i32 s9, s8, s11
	s_sub_i32 s4, s4, s9
	s_sext_i32_i8 s4, s4
	s_add_i32 s4, s10, s4
	s_sext_i32_i8 s60, s8
	s_mul_i32 s61, s4, 0x160000
	s_mul_i32 s62, s60, 0x160000

.LBB0_1601:
	s_andn2_b64 vcc, exec, s[12:13]
	s_cbranch_vccnz .Lzs_6
	s_add_i32 s6, s61, 0x80
	s_add_i32 s61, s62, 0x100
	s_mov_b32 s62, 0
	ds_read_b128 v[18:21], v235
	ds_read_b128 v[22:25], v236
	ds_read_b128 v[26:29], v243
	ds_read_b128 v[30:33], v244
	s_waitcnt lgkmcnt(0)
	ds_read_b128 v[2:5], v237
	ds_read_b128 v[6:9], v238
	ds_read_b128 v[10:13], v245
	ds_read_b128 v[14:17], v246
	s_add_i32 s63, s6, 0x80
	s_cmp_eq_u32 s89, s62
	s_cselect_b32 s65, s7, s63
	s_cselect_b32 s64, s5, s61
	s_add_i32 s63, s65, 0x80
	v_mov_b32_e32 v194, v1
	ds_read_b128 v[162:165], v251
	ds_read_b128 v[166:169], v251 offset:1024
	ds_read_b128 v[170:173], v251 offset:2048
	ds_read_b128 v[174:177], v251 offset:3072
	ds_read_b128 v[178:181], v251 offset:4096
	ds_read_b128 v[182:185], v251 offset:5120
	ds_read_b128 v[186:189], v251 offset:6144
	ds_read_b128 v[190:193], v251 offset:7168
	s_add_i32 s66, s6, s86
	v_add_u32_e32 v194, s66, v194
	s_add_i32 m0, s70, 0xc000
	s_add_i32 s66, s6, s93
	global_load_lds_dwordx4 v194, s[8:9]
	v_mov_b32_e32 v194, v1
	s_add_i32 m0, s70, 0xe000
	v_add_u32_e32 v194, s66, v194
	global_load_lds_dwordx4 v194, s[8:9]
	s_waitcnt vmcnt(8)
	s_waitcnt lgkmcnt(0)
	s_barrier
	s_waitcnt lgkmcnt(0)
	v_mfma_f32_16x16x128_f8f6f4 v[158:161], v[18:25], v[162:169], 0
	v_mfma_f32_16x16x128_f8f6f4 v[154:157], v[26:33], v[162:169], 0
	v_mfma_f32_16x16x128_f8f6f4 v[142:145], v[18:25], v[170:177], 0
	v_mfma_f32_16x16x128_f8f6f4 v[138:141], v[26:33], v[170:177], 0
	v_mfma_f32_16x16x128_f8f6f4 v[126:129], v[18:25], v[178:185], 0
	v_mfma_f32_16x16x128_f8f6f4 v[122:125], v[26:33], v[178:185], 0
	v_mfma_f32_16x16x128_f8f6f4 v[110:113], v[18:25], v[186:193], 0
	v_mfma_f32_16x16x128_f8f6f4 v[106:109], v[26:33], v[186:193], 0
	v_mfma_f32_16x16x128_f8f6f4 v[150:153], v[2:9], v[162:169], 0
	v_mfma_f32_16x16x128_f8f6f4 v[146:149], v[10:17], v[162:169], 0
	v_mfma_f32_16x16x128_f8f6f4 v[134:137], v[2:9], v[170:177], 0
	v_mfma_f32_16x16x128_f8f6f4 v[130:133], v[10:17], v[170:177], 0
	v_mfma_f32_16x16x128_f8f6f4 v[118:121], v[2:9], v[178:185], 0
	v_mfma_f32_16x16x128_f8f6f4 v[114:117], v[10:17], v[178:185], 0
	v_mfma_f32_16x16x128_f8f6f4 v[102:105], v[2:9], v[186:193], 0
	v_mfma_f32_16x16x128_f8f6f4 v[98:101], v[10:17], v[186:193], 0
	s_barrier
	v_mov_b32_e32 v194, v211
	ds_read_b128 v[162:165], v251 offset:16384
	ds_read_b128 v[166:169], v251 offset:17408
	ds_read_b128 v[170:173], v251 offset:18432
	ds_read_b128 v[174:177], v251 offset:19456
	ds_read_b128 v[178:181], v251 offset:20480
	ds_read_b128 v[182:185], v251 offset:21504
	ds_read_b128 v[186:189], v251 offset:22528
	ds_read_b128 v[190:193], v251 offset:23552
	s_mov_b32 m0, s71
	v_add_u32_e32 v194, s64, v194
	global_load_lds_dwordx4 v194, s[20:21]
	v_mov_b32_e32 v194, v211
	s_add_i32 s66, s64, s35
	v_add_u32_e32 v194, s66, v194
	s_mov_b32 m0, s72
	s_add_i32 s66, s66, s35
	global_load_lds_dwordx4 v194, s[20:21]
	v_mov_b32_e32 v194, v211
	s_mov_b32 m0, s73
	v_add_u32_e32 v194, s66, v194
	global_load_lds_dwordx4 v194, s[20:21]
	v_mov_b32_e32 v194, v211
	s_add_i32 s66, s66, s35
	v_add_u32_e32 v194, s66, v194
	s_mov_b32 m0, s76
	s_nop 0
	global_load_lds_dwordx4 v194, s[20:21]
	v_mov_b32_e32 v194, v1
	s_mov_b32 m0, s70
	v_add_u32_e32 v194, s65, v194
	global_load_lds_dwordx4 v194, s[8:9]
	v_mov_b32_e32 v194, v1
	s_add_i32 s65, s65, s23
	v_add_u32_e32 v194, s65, v194
	s_mov_b32 m0, s77
	s_nop 0
	global_load_lds_dwordx4 v194, s[8:9]
	s_waitcnt vmcnt(8)
	s_waitcnt lgkmcnt(0)
	s_barrier
	s_waitcnt lgkmcnt(0)
	v_mfma_f32_16x16x128_f8f6f4 v[94:97], v[18:25], v[162:169], 0
	v_mfma_f32_16x16x128_f8f6f4 v[90:93], v[26:33], v[162:169], 0
	v_mfma_f32_16x16x128_f8f6f4 v[78:81], v[18:25], v[170:177], 0
	v_mfma_f32_16x16x128_f8f6f4 v[74:77], v[26:33], v[170:177], 0
	v_mfma_f32_16x16x128_f8f6f4 v[62:65], v[18:25], v[178:185], 0
	v_mfma_f32_16x16x128_f8f6f4 v[58:61], v[26:33], v[178:185], 0
	v_mfma_f32_16x16x128_f8f6f4 v[46:49], v[18:25], v[186:193], 0
	v_mfma_f32_16x16x128_f8f6f4 v[42:45], v[26:33], v[186:193], 0
	v_mfma_f32_16x16x128_f8f6f4 v[86:89], v[2:9], v[162:169], 0
	v_mfma_f32_16x16x128_f8f6f4 v[82:85], v[10:17], v[162:169], 0
	v_mfma_f32_16x16x128_f8f6f4 v[70:73], v[2:9], v[170:177], 0
	v_mfma_f32_16x16x128_f8f6f4 v[66:69], v[10:17], v[170:177], 0
	v_mfma_f32_16x16x128_f8f6f4 v[54:57], v[2:9], v[178:185], 0
	v_mfma_f32_16x16x128_f8f6f4 v[50:53], v[10:17], v[178:185], 0
	v_mfma_f32_16x16x128_f8f6f4 v[38:41], v[2:9], v[186:193], 0
	v_mfma_f32_16x16x128_f8f6f4 v[34:37], v[10:17], v[186:193], 0
	s_barrier
	s_branch .Lmid_5
.LBB0_1603:
	ds_read_b128 v[18:21], v235
	ds_read_b128 v[22:25], v236
	ds_read_b128 v[26:29], v243
	ds_read_b128 v[30:33], v244
	s_waitcnt lgkmcnt(0)
	ds_read_b128 v[2:5], v237
	ds_read_b128 v[6:9], v238
	ds_read_b128 v[10:13], v245
	ds_read_b128 v[14:17], v246
	s_add_i32 s63, s6, 0x80
	s_cmp_eq_u32 s89, s62
	s_cselect_b32 s65, s7, s63
	s_cselect_b32 s64, s5, s61
	s_add_i32 s63, s65, 0x80
	v_mov_b32_e32 v194, v1
	ds_read_b128 v[162:165], v251
	ds_read_b128 v[166:169], v251 offset:1024
	ds_read_b128 v[170:173], v251 offset:2048
	ds_read_b128 v[174:177], v251 offset:3072
	ds_read_b128 v[178:181], v251 offset:4096
	ds_read_b128 v[182:185], v251 offset:5120
	ds_read_b128 v[186:189], v251 offset:6144
	ds_read_b128 v[190:193], v251 offset:7168
	s_add_i32 s66, s6, s86
	v_add_u32_e32 v194, s66, v194
	s_add_i32 m0, s70, 0xc000
	s_add_i32 s66, s6, s93
	global_load_lds_dwordx4 v194, s[8:9]
	v_mov_b32_e32 v194, v1
	s_add_i32 m0, s70, 0xe000
	v_add_u32_e32 v194, s66, v194
	global_load_lds_dwordx4 v194, s[8:9]
	s_waitcnt vmcnt(8)
	s_waitcnt lgkmcnt(0)
	s_barrier
	s_waitcnt lgkmcnt(0)
	v_mfma_f32_16x16x128_f8f6f4 v[158:161], v[18:25], v[162:169], v[158:161]
	v_mfma_f32_16x16x128_f8f6f4 v[154:157], v[26:33], v[162:169], v[154:157]
	v_mfma_f32_16x16x128_f8f6f4 v[142:145], v[18:25], v[170:177], v[142:145]
	v_mfma_f32_16x16x128_f8f6f4 v[138:141], v[26:33], v[170:177], v[138:141]
	v_mfma_f32_16x16x128_f8f6f4 v[126:129], v[18:25], v[178:185], v[126:129]
	v_mfma_f32_16x16x128_f8f6f4 v[122:125], v[26:33], v[178:185], v[122:125]
	v_mfma_f32_16x16x128_f8f6f4 v[110:113], v[18:25], v[186:193], v[110:113]
	v_mfma_f32_16x16x128_f8f6f4 v[106:109], v[26:33], v[186:193], v[106:109]
	v_mfma_f32_16x16x128_f8f6f4 v[150:153], v[2:9], v[162:169], v[150:153]
	v_mfma_f32_16x16x128_f8f6f4 v[146:149], v[10:17], v[162:169], v[146:149]
	v_mfma_f32_16x16x128_f8f6f4 v[134:137], v[2:9], v[170:177], v[134:137]
	v_mfma_f32_16x16x128_f8f6f4 v[130:133], v[10:17], v[170:177], v[130:133]
	v_mfma_f32_16x16x128_f8f6f4 v[118:121], v[2:9], v[178:185], v[118:121]
	v_mfma_f32_16x16x128_f8f6f4 v[114:117], v[10:17], v[178:185], v[114:117]
	v_mfma_f32_16x16x128_f8f6f4 v[102:105], v[2:9], v[186:193], v[102:105]
	v_mfma_f32_16x16x128_f8f6f4 v[98:101], v[10:17], v[186:193], v[98:101]
	s_barrier
	v_mov_b32_e32 v194, v211
	ds_read_b128 v[162:165], v251 offset:16384
	ds_read_b128 v[166:169], v251 offset:17408
	ds_read_b128 v[170:173], v251 offset:18432
	ds_read_b128 v[174:177], v251 offset:19456
	ds_read_b128 v[178:181], v251 offset:20480
	ds_read_b128 v[182:185], v251 offset:21504
	ds_read_b128 v[186:189], v251 offset:22528
	ds_read_b128 v[190:193], v251 offset:23552
	s_mov_b32 m0, s71
	v_add_u32_e32 v194, s64, v194
	global_load_lds_dwordx4 v194, s[20:21]
	v_mov_b32_e32 v194, v211
	s_add_i32 s66, s64, s35
	v_add_u32_e32 v194, s66, v194
	s_mov_b32 m0, s72
	s_add_i32 s66, s66, s35
	global_load_lds_dwordx4 v194, s[20:21]
	v_mov_b32_e32 v194, v211
	s_mov_b32 m0, s73
	v_add_u32_e32 v194, s66, v194
	global_load_lds_dwordx4 v194, s[20:21]
	v_mov_b32_e32 v194, v211
	s_add_i32 s66, s66, s35
	v_add_u32_e32 v194, s66, v194
	s_mov_b32 m0, s76
	s_nop 0
	global_load_lds_dwordx4 v194, s[20:21]
	v_mov_b32_e32 v194, v1
	s_mov_b32 m0, s70
	v_add_u32_e32 v194, s65, v194
	global_load_lds_dwordx4 v194, s[8:9]
	v_mov_b32_e32 v194, v1
	s_add_i32 s65, s65, s23
	v_add_u32_e32 v194, s65, v194
	s_mov_b32 m0, s77
	s_nop 0
	global_load_lds_dwordx4 v194, s[8:9]
	s_waitcnt vmcnt(8)
	s_waitcnt lgkmcnt(0)
	s_barrier
	s_waitcnt lgkmcnt(0)
	v_mfma_f32_16x16x128_f8f6f4 v[94:97], v[18:25], v[162:169], v[94:97]
	v_mfma_f32_16x16x128_f8f6f4 v[90:93], v[26:33], v[162:169], v[90:93]
	v_mfma_f32_16x16x128_f8f6f4 v[78:81], v[18:25], v[170:177], v[78:81]
	v_mfma_f32_16x16x128_f8f6f4 v[74:77], v[26:33], v[170:177], v[74:77]
	v_mfma_f32_16x16x128_f8f6f4 v[62:65], v[18:25], v[178:185], v[62:65]
	v_mfma_f32_16x16x128_f8f6f4 v[58:61], v[26:33], v[178:185], v[58:61]
	v_mfma_f32_16x16x128_f8f6f4 v[46:49], v[18:25], v[186:193], v[46:49]
	v_mfma_f32_16x16x128_f8f6f4 v[42:45], v[26:33], v[186:193], v[42:45]
	v_mfma_f32_16x16x128_f8f6f4 v[86:89], v[2:9], v[162:169], v[86:89]
	v_mfma_f32_16x16x128_f8f6f4 v[82:85], v[10:17], v[162:169], v[82:85]
	v_mfma_f32_16x16x128_f8f6f4 v[70:73], v[2:9], v[170:177], v[70:73]
	v_mfma_f32_16x16x128_f8f6f4 v[66:69], v[10:17], v[170:177], v[66:69]
	v_mfma_f32_16x16x128_f8f6f4 v[54:57], v[2:9], v[178:185], v[54:57]
	v_mfma_f32_16x16x128_f8f6f4 v[50:53], v[10:17], v[178:185], v[50:53]
	v_mfma_f32_16x16x128_f8f6f4 v[38:41], v[2:9], v[186:193], v[38:41]
	v_mfma_f32_16x16x128_f8f6f4 v[34:37], v[10:17], v[186:193], v[34:37]
	s_barrier
.Lmid_5:
	ds_read_b128 v[2:5], v239
	ds_read_b128 v[6:9], v240
	ds_read_b128 v[10:13], v247
	ds_read_b128 v[14:17], v248
	ds_read_b128 v[18:21], v241
	ds_read_b128 v[22:25], v242
	ds_read_b128 v[26:29], v249
	ds_read_b128 v[30:33], v250
	v_mov_b32_e32 v194, v1
	ds_read_b128 v[162:165], v251 offset:32768
	ds_read_b128 v[166:169], v251 offset:33792
	ds_read_b128 v[170:173], v251 offset:34816
	ds_read_b128 v[174:177], v251 offset:35840
	ds_read_b128 v[178:181], v251 offset:36864
	ds_read_b128 v[182:185], v251 offset:37888
	ds_read_b128 v[186:189], v251 offset:38912
	ds_read_b128 v[190:193], v251 offset:39936
	s_add_i32 s65, s65, s23
	s_mov_b32 m0, s78
	v_add_u32_e32 v194, s65, v194
	global_load_lds_dwordx4 v194, s[8:9]
	v_mov_b32_e32 v194, v1
	s_add_i32 s65, s65, s23
	v_add_u32_e32 v194, s65, v194
	s_mov_b32 m0, s44
	s_nop 0
	global_load_lds_dwordx4 v194, s[8:9]
	s_waitcnt vmcnt(8)
	s_waitcnt lgkmcnt(0)
	s_barrier
	s_waitcnt lgkmcnt(0)
	v_mfma_f32_16x16x128_f8f6f4 v[158:161], v[2:9], v[162:169], v[158:161]
	v_mfma_f32_16x16x128_f8f6f4 v[154:157], v[10:17], v[162:169], v[154:157]
	v_mfma_f32_16x16x128_f8f6f4 v[142:145], v[2:9], v[170:177], v[142:145]
	v_mfma_f32_16x16x128_f8f6f4 v[138:141], v[10:17], v[170:177], v[138:141]
	v_mfma_f32_16x16x128_f8f6f4 v[126:129], v[2:9], v[178:185], v[126:129]
	v_mfma_f32_16x16x128_f8f6f4 v[122:125], v[10:17], v[178:185], v[122:125]
	v_mfma_f32_16x16x128_f8f6f4 v[110:113], v[2:9], v[186:193], v[110:113]
	v_mfma_f32_16x16x128_f8f6f4 v[106:109], v[10:17], v[186:193], v[106:109]
	v_mfma_f32_16x16x128_f8f6f4 v[150:153], v[18:25], v[162:169], v[150:153]
	v_mfma_f32_16x16x128_f8f6f4 v[146:149], v[26:33], v[162:169], v[146:149]
	v_mfma_f32_16x16x128_f8f6f4 v[134:137], v[18:25], v[170:177], v[134:137]
	v_mfma_f32_16x16x128_f8f6f4 v[130:133], v[26:33], v[170:177], v[130:133]
	v_mfma_f32_16x16x128_f8f6f4 v[118:121], v[18:25], v[178:185], v[118:121]
	v_mfma_f32_16x16x128_f8f6f4 v[114:117], v[26:33], v[178:185], v[114:117]
	v_mfma_f32_16x16x128_f8f6f4 v[102:105], v[18:25], v[186:193], v[102:105]
	v_mfma_f32_16x16x128_f8f6f4 v[98:101], v[26:33], v[186:193], v[98:101]
	s_barrier
	v_mov_b32_e32 v194, v211
	ds_read_b128 v[162:165], v251 offset:49152
	ds_read_b128 v[166:169], v251 offset:50176
	ds_read_b128 v[170:173], v251 offset:51200
	ds_read_b128 v[174:177], v251 offset:52224
	ds_read_b128 v[178:181], v251 offset:53248
	ds_read_b128 v[182:185], v251 offset:54272
	ds_read_b128 v[186:189], v251 offset:55296
	ds_read_b128 v[190:193], v251 offset:56320
	s_addk_i32 s64, 0x80
	s_mov_b32 m0, s79
	v_add_u32_e32 v194, s64, v194
	global_load_lds_dwordx4 v194, s[20:21]
	v_mov_b32_e32 v194, v211
	s_add_i32 s64, s64, s35
	v_add_u32_e32 v194, s64, v194
	s_mov_b32 m0, s80
	s_add_i32 s64, s64, s35
	global_load_lds_dwordx4 v194, s[20:21]
	v_mov_b32_e32 v194, v211
	s_mov_b32 m0, s83
	v_add_u32_e32 v194, s64, v194
	global_load_lds_dwordx4 v194, s[20:21]
	v_mov_b32_e32 v194, v211
	s_add_i32 s64, s64, s35
	v_add_u32_e32 v194, s64, v194
	s_mov_b32 m0, s84
	s_nop 0
	global_load_lds_dwordx4 v194, s[20:21]
	v_mov_b32_e32 v194, v1
	s_mov_b32 m0, s81
	v_add_u32_e32 v194, s63, v194
	global_load_lds_dwordx4 v194, s[8:9]
	v_mov_b32_e32 v194, v1
	s_add_i32 s63, s63, s23
	v_add_u32_e32 v194, s63, v194
	s_mov_b32 m0, s82
	s_nop 0
	global_load_lds_dwordx4 v194, s[8:9]
	s_waitcnt vmcnt(8)
	s_waitcnt lgkmcnt(0)
	s_barrier
	s_waitcnt lgkmcnt(0)
	v_mfma_f32_16x16x128_f8f6f4 v[94:97], v[2:9], v[162:169], v[94:97]
	v_mfma_f32_16x16x128_f8f6f4 v[90:93], v[10:17], v[162:169], v[90:93]
	v_mfma_f32_16x16x128_f8f6f4 v[78:81], v[2:9], v[170:177], v[78:81]
	v_mfma_f32_16x16x128_f8f6f4 v[74:77], v[10:17], v[170:177], v[74:77]
	v_mfma_f32_16x16x128_f8f6f4 v[62:65], v[2:9], v[178:185], v[62:65]
	v_mfma_f32_16x16x128_f8f6f4 v[58:61], v[10:17], v[178:185], v[58:61]
	v_mfma_f32_16x16x128_f8f6f4 v[46:49], v[2:9], v[186:193], v[46:49]
	v_mfma_f32_16x16x128_f8f6f4 v[42:45], v[10:17], v[186:193], v[42:45]
	v_mfma_f32_16x16x128_f8f6f4 v[86:89], v[18:25], v[162:169], v[86:89]
	v_mfma_f32_16x16x128_f8f6f4 v[82:85], v[26:33], v[162:169], v[82:85]
	v_mfma_f32_16x16x128_f8f6f4 v[70:73], v[18:25], v[170:177], v[70:73]
	v_mfma_f32_16x16x128_f8f6f4 v[66:69], v[26:33], v[170:177], v[66:69]
	v_mfma_f32_16x16x128_f8f6f4 v[54:57], v[18:25], v[178:185], v[54:57]
	v_mfma_f32_16x16x128_f8f6f4 v[50:53], v[26:33], v[178:185], v[50:53]
	v_mfma_f32_16x16x128_f8f6f4 v[38:41], v[18:25], v[186:193], v[38:41]
	v_mfma_f32_16x16x128_f8f6f4 v[34:37], v[26:33], v[186:193], v[34:37]
	s_barrier
	s_add_i32 s62, s62, 2
	s_addk_i32 s6, 0x100
	s_addk_i32 s61, 0x100
	s_cmp_ge_i32 s62, s85
	s_cbranch_scc0 .LBB0_1603

.LBB0_1769:
	s_setprio 0
	s_cmp_lt_i32 s41, 14
	s_cbranch_scc1 .LBB0_1819
	s_waitcnt vmcnt(0)
	v_cmp_eq_u32_e32 vcc, 0, v0
	s_waitcnt vmcnt(0) lgkmcnt(0)
	s_barrier
	s_and_saveexec_b64 s[2:3], vcc
	s_cbranch_execz .LBB0_1818
	v_mov_b32_e32 v1, s92
	s_waitcnt vmcnt(0) expcnt(0) lgkmcnt(0)
	ds_read_b32 v3, v1
	ds_read_b32 v1, v1 offset:4
	s_waitcnt lgkmcnt(1)
	v_cmp_ne_u32_e32 vcc, 0, v3
	s_cbranch_vccnz .LBB0_1786
	v_readlane_b32 s4, v254, 1
	v_readlane_b32 s5, v254, 2
	s_load_dwordx2 s[8:9], s[4:5], 0x4
	s_add_u32 s4, s42, 0x1000
	s_addc_u32 s5, s43, 0
	s_add_u32 s6, s42, 0x1100
	s_addc_u32 s7, s43, 0
	s_waitcnt lgkmcnt(0)
	s_mul_i32 s18, s8, s34
	s_add_u32 s8, s42, 0x1200
	s_mul_i32 s18, s18, s9
	s_addc_u32 s9, s43, 0
	s_add_u32 s10, s42, 0x1300
	s_addc_u32 s11, s43, 0
	s_mov_b32 s19, 1
	v_mov_b32_e32 v17, 0
	s_branch .LBB0_1774

.LBB0_1819:
.LBB0_1820:
	s_cmp_gt_i32 s40, 14
	s_cselect_b64 s[2:3], -1, 0
	s_cmp_lt_i32 s41, 15
	s_cselect_b64 s[4:5], -1, 0
	s_or_b64 s[2:3], s[2:3], s[4:5]
	s_and_b64 vcc, exec, s[2:3]
	s_cbranch_vccnz .LBB0_2032
	s_cmp_ge_u32 s27, 4
	s_cbranch_scc0 .Lsp_14
	s_setprio 1
.Lsp_14:
	s_add_u32 s20, s38, 0x6a00000
	s_addc_u32 s21, s39, 0
	v_mov_b32_e32 v2, v0
	s_movk_i32 s14, 0x800
	v_readfirstlane_b32 s5, v2
	s_movk_i32 s4, 0x800
	s_movk_i32 s10, 0x800
	s_cmpk_gt_i32 s26, 0x7bb
	s_cbranch_scc1 .LBB0_1854
	s_ashr_i32 s35, s26, 31
	s_lshr_b32 s2, s35, 29
	s_add_i32 s6, s26, s2
	s_and_b32 s2, s6, -8
	s_sub_i32 s8, s26, s2
	s_cmp_gt_i32 s8, 3
	s_cbranch_scc0 .LBB0_1824
	s_mul_i32 s2, s8, 0xf7
	s_add_i32 s7, s2, 4
	s_cbranch_execz .LBB0_1825
	s_branch .LBB0_1826

.Lphr_1:
	ds_read_b128 v[132:135], v170
	ds_read_b128 v[136:139], v171
	ds_read_b128 v[140:143], v166
	ds_read_b128 v[154:157], v167
	ds_read_b128 v[188:191], v172
	ds_read_b128 v[192:195], v173
	ds_read_b128 v[196:199], v174
	ds_read_b128 v[200:203], v175
	s_add_i32 s75, s94, 0x80
	s_and_b64 s[50:51], s[50:51], exec
	s_cselect_b32 s50, s75, s49
	s_cselect_b32 s75, s95, s93
	s_add_i32 s51, s75, 0x80
	v_add_u32_e32 v144, s94, v183
	s_add_i32 m0, s52, 0xc000
	ds_read_b128 v[204:207], v184
	ds_read_b128 v[214:217], v184 offset:1024
	ds_read_b128 v[218:221], v184 offset:2048
	ds_read_b128 v[222:225], v184 offset:3072
	ds_read_b128 v[226:229], v184 offset:4096
	ds_read_b128 v[230:233], v184 offset:5120
	ds_read_b128 v[234:237], v184 offset:6144
	ds_read_b128 v[238:241], v184 offset:7168
	global_load_lds_dwordx4 v144, s[8:9]
	v_add_u32_e32 v144, s94, v182
	s_add_i32 m0, s52, 0xe000
	s_nop 0
	global_load_lds_dwordx4 v144, s[8:9]
	s_waitcnt vmcnt(8)
	s_waitcnt lgkmcnt(0)
	s_barrier
	s_waitcnt lgkmcnt(0)
	v_mfma_f32_16x16x32_bf16 v[126:129], v[140:143], v[204:207], 0
	v_mfma_f32_16x16x32_bf16 v[122:125], v[136:139], v[204:207], 0
	v_mfma_f32_16x16x32_bf16 v[110:113], v[140:143], v[218:221], 0
	v_mfma_f32_16x16x32_bf16 v[106:109], v[136:139], v[218:221], 0
	v_mfma_f32_16x16x32_bf16 v[94:97], v[140:143], v[226:229], 0
	v_mfma_f32_16x16x32_bf16 v[90:93], v[136:139], v[226:229], 0
	v_mfma_f32_16x16x32_bf16 v[78:81], v[140:143], v[234:237], 0
	v_mfma_f32_16x16x32_bf16 v[74:77], v[136:139], v[234:237], 0
	v_mfma_f32_16x16x32_bf16 v[126:129], v[132:135], v[214:217], v[126:129]
	v_mfma_f32_16x16x32_bf16 v[122:125], v[188:191], v[214:217], v[122:125]
	v_mfma_f32_16x16x32_bf16 v[110:113], v[132:135], v[222:225], v[110:113]
	v_mfma_f32_16x16x32_bf16 v[106:109], v[188:191], v[222:225], v[106:109]
	v_mfma_f32_16x16x32_bf16 v[94:97], v[132:135], v[230:233], v[94:97]
	v_mfma_f32_16x16x32_bf16 v[90:93], v[188:191], v[230:233], v[90:93]
	v_mfma_f32_16x16x32_bf16 v[78:81], v[132:135], v[238:241], v[78:81]
	v_mfma_f32_16x16x32_bf16 v[74:77], v[188:191], v[238:241], v[74:77]
	v_mfma_f32_16x16x32_bf16 v[118:121], v[154:157], v[204:207], 0
	v_mfma_f32_16x16x32_bf16 v[114:117], v[196:199], v[204:207], 0
	v_mfma_f32_16x16x32_bf16 v[102:105], v[154:157], v[218:221], 0
	v_mfma_f32_16x16x32_bf16 v[98:101], v[196:199], v[218:221], 0
	v_mfma_f32_16x16x32_bf16 v[86:89], v[154:157], v[226:229], 0
	v_mfma_f32_16x16x32_bf16 v[82:85], v[196:199], v[226:229], 0
	v_mfma_f32_16x16x32_bf16 v[70:73], v[154:157], v[234:237], 0
	v_mfma_f32_16x16x32_bf16 v[66:69], v[196:199], v[234:237], 0
	v_mfma_f32_16x16x32_bf16 v[118:121], v[192:195], v[214:217], v[118:121]
	v_mfma_f32_16x16x32_bf16 v[114:117], v[200:203], v[214:217], v[114:117]
	v_mfma_f32_16x16x32_bf16 v[102:105], v[192:195], v[222:225], v[102:105]
	v_mfma_f32_16x16x32_bf16 v[98:101], v[200:203], v[222:225], v[98:101]
	v_mfma_f32_16x16x32_bf16 v[86:89], v[192:195], v[230:233], v[86:89]
	v_mfma_f32_16x16x32_bf16 v[82:85], v[200:203], v[230:233], v[82:85]
	v_mfma_f32_16x16x32_bf16 v[70:73], v[192:195], v[238:241], v[70:73]
	v_mfma_f32_16x16x32_bf16 v[66:69], v[200:203], v[238:241], v[66:69]
	s_barrier
	s_mov_b32 m0, s53
	v_add_u32_e32 v144, s75, v160
	ds_read_b128 v[204:207], v184 offset:16384
	ds_read_b128 v[214:217], v184 offset:17408
	ds_read_b128 v[218:221], v184 offset:18432
	ds_read_b128 v[222:225], v184 offset:19456
	ds_read_b128 v[226:229], v184 offset:20480
	ds_read_b128 v[230:233], v184 offset:21504
	ds_read_b128 v[234:237], v184 offset:22528
	ds_read_b128 v[238:241], v184 offset:23552
	global_load_lds_dwordx4 v144, s[20:21]
	v_add_u32_e32 v144, s45, v144
	s_mov_b32 m0, s54
	s_nop 0
	global_load_lds_dwordx4 v144, s[20:21]
	v_add_u32_e32 v144, s75, v161
	s_mov_b32 m0, s55
	s_nop 0
	global_load_lds_dwordx4 v144, s[20:21]
	v_add_u32_e32 v144, s45, v144
	s_mov_b32 m0, s56
	s_nop 0
	global_load_lds_dwordx4 v144, s[20:21]
	v_add_u32_e32 v144, s50, v1
	s_mov_b32 m0, s52
	s_nop 0
	global_load_lds_dwordx4 v144, s[8:9]
	v_add_u32_e32 v144, s44, v144
	s_mov_b32 m0, s57
	s_nop 0
	global_load_lds_dwordx4 v144, s[8:9]
	s_waitcnt vmcnt(8)
	s_waitcnt lgkmcnt(0)
	s_barrier
	s_waitcnt lgkmcnt(0)
	v_mfma_f32_16x16x32_bf16 v[62:65], v[140:143], v[204:207], 0
	v_mfma_f32_16x16x32_bf16 v[58:61], v[136:139], v[204:207], 0
	v_mfma_f32_16x16x32_bf16 v[46:49], v[140:143], v[218:221], 0
	v_mfma_f32_16x16x32_bf16 v[42:45], v[136:139], v[218:221], 0
	v_mfma_f32_16x16x32_bf16 v[30:33], v[140:143], v[226:229], 0
	v_mfma_f32_16x16x32_bf16 v[26:29], v[136:139], v[226:229], 0
	v_mfma_f32_16x16x32_bf16 v[14:17], v[140:143], v[234:237], 0
	v_mfma_f32_16x16x32_bf16 v[10:13], v[136:139], v[234:237], 0
	v_mfma_f32_16x16x32_bf16 v[62:65], v[132:135], v[214:217], v[62:65]
	v_mfma_f32_16x16x32_bf16 v[58:61], v[188:191], v[214:217], v[58:61]
	v_mfma_f32_16x16x32_bf16 v[46:49], v[132:135], v[222:225], v[46:49]
	v_mfma_f32_16x16x32_bf16 v[42:45], v[188:191], v[222:225], v[42:45]
	v_mfma_f32_16x16x32_bf16 v[30:33], v[132:135], v[230:233], v[30:33]
	v_mfma_f32_16x16x32_bf16 v[26:29], v[188:191], v[230:233], v[26:29]
	v_mfma_f32_16x16x32_bf16 v[14:17], v[132:135], v[238:241], v[14:17]
	v_mfma_f32_16x16x32_bf16 v[10:13], v[188:191], v[238:241], v[10:13]
	v_mfma_f32_16x16x32_bf16 v[54:57], v[154:157], v[204:207], 0
	v_mfma_f32_16x16x32_bf16 v[50:53], v[196:199], v[204:207], 0
	v_mfma_f32_16x16x32_bf16 v[38:41], v[154:157], v[218:221], 0
	v_mfma_f32_16x16x32_bf16 v[34:37], v[196:199], v[218:221], 0
	v_mfma_f32_16x16x32_bf16 v[22:25], v[154:157], v[226:229], 0
	v_mfma_f32_16x16x32_bf16 v[18:21], v[196:199], v[226:229], 0
	v_mfma_f32_16x16x32_bf16 v[6:9], v[154:157], v[234:237], 0
	v_mfma_f32_16x16x32_bf16 v[2:5], v[196:199], v[234:237], 0
	v_mfma_f32_16x16x32_bf16 v[54:57], v[192:195], v[214:217], v[54:57]
	v_mfma_f32_16x16x32_bf16 v[50:53], v[200:203], v[214:217], v[50:53]
	v_mfma_f32_16x16x32_bf16 v[38:41], v[192:195], v[222:225], v[38:41]
	v_mfma_f32_16x16x32_bf16 v[34:37], v[200:203], v[222:225], v[34:37]
	v_mfma_f32_16x16x32_bf16 v[22:25], v[192:195], v[230:233], v[22:25]
	v_mfma_f32_16x16x32_bf16 v[18:21], v[200:203], v[230:233], v[18:21]
	v_mfma_f32_16x16x32_bf16 v[6:9], v[192:195], v[238:241], v[6:9]
	v_mfma_f32_16x16x32_bf16 v[2:5], v[200:203], v[238:241], v[2:5]
	s_barrier
	s_branch .Lmidr_1
.LBB0_1841:
	ds_read_b128 v[132:135], v170
	ds_read_b128 v[136:139], v171
	ds_read_b128 v[140:143], v166
	ds_read_b128 v[154:157], v167
	ds_read_b128 v[188:191], v172
	ds_read_b128 v[192:195], v173
	ds_read_b128 v[196:199], v174
	ds_read_b128 v[200:203], v175
	s_add_i32 s75, s94, 0x80
	s_and_b64 s[50:51], s[50:51], exec
	s_cselect_b32 s50, s75, s49
	s_cselect_b32 s75, s95, s93
	s_add_i32 s51, s75, 0x80
	v_add_u32_e32 v144, s94, v183
	s_add_i32 m0, s52, 0xc000
	ds_read_b128 v[204:207], v184
	ds_read_b128 v[214:217], v184 offset:1024
	ds_read_b128 v[218:221], v184 offset:2048
	ds_read_b128 v[222:225], v184 offset:3072
	ds_read_b128 v[226:229], v184 offset:4096
	ds_read_b128 v[230:233], v184 offset:5120
	ds_read_b128 v[234:237], v184 offset:6144
	ds_read_b128 v[238:241], v184 offset:7168
	global_load_lds_dwordx4 v144, s[8:9]
	v_add_u32_e32 v144, s94, v182
	s_add_i32 m0, s52, 0xe000
	s_nop 0
	global_load_lds_dwordx4 v144, s[8:9]
	s_waitcnt vmcnt(8)
	s_waitcnt lgkmcnt(0)
	s_barrier
	s_waitcnt lgkmcnt(0)
	v_mfma_f32_16x16x32_bf16 v[126:129], v[140:143], v[204:207], v[126:129]
	v_mfma_f32_16x16x32_bf16 v[122:125], v[136:139], v[204:207], v[122:125]
	v_mfma_f32_16x16x32_bf16 v[110:113], v[140:143], v[218:221], v[110:113]
	v_mfma_f32_16x16x32_bf16 v[106:109], v[136:139], v[218:221], v[106:109]
	v_mfma_f32_16x16x32_bf16 v[94:97], v[140:143], v[226:229], v[94:97]
	v_mfma_f32_16x16x32_bf16 v[90:93], v[136:139], v[226:229], v[90:93]
	v_mfma_f32_16x16x32_bf16 v[78:81], v[140:143], v[234:237], v[78:81]
	v_mfma_f32_16x16x32_bf16 v[74:77], v[136:139], v[234:237], v[74:77]
	v_mfma_f32_16x16x32_bf16 v[126:129], v[132:135], v[214:217], v[126:129]
	v_mfma_f32_16x16x32_bf16 v[122:125], v[188:191], v[214:217], v[122:125]
	v_mfma_f32_16x16x32_bf16 v[110:113], v[132:135], v[222:225], v[110:113]
	v_mfma_f32_16x16x32_bf16 v[106:109], v[188:191], v[222:225], v[106:109]
	v_mfma_f32_16x16x32_bf16 v[94:97], v[132:135], v[230:233], v[94:97]
	v_mfma_f32_16x16x32_bf16 v[90:93], v[188:191], v[230:233], v[90:93]
	v_mfma_f32_16x16x32_bf16 v[78:81], v[132:135], v[238:241], v[78:81]
	v_mfma_f32_16x16x32_bf16 v[74:77], v[188:191], v[238:241], v[74:77]
	v_mfma_f32_16x16x32_bf16 v[118:121], v[154:157], v[204:207], v[118:121]
	v_mfma_f32_16x16x32_bf16 v[114:117], v[196:199], v[204:207], v[114:117]
	v_mfma_f32_16x16x32_bf16 v[102:105], v[154:157], v[218:221], v[102:105]
	v_mfma_f32_16x16x32_bf16 v[98:101], v[196:199], v[218:221], v[98:101]
	v_mfma_f32_16x16x32_bf16 v[86:89], v[154:157], v[226:229], v[86:89]
	v_mfma_f32_16x16x32_bf16 v[82:85], v[196:199], v[226:229], v[82:85]
	v_mfma_f32_16x16x32_bf16 v[70:73], v[154:157], v[234:237], v[70:73]
	v_mfma_f32_16x16x32_bf16 v[66:69], v[196:199], v[234:237], v[66:69]
	v_mfma_f32_16x16x32_bf16 v[118:121], v[192:195], v[214:217], v[118:121]
	v_mfma_f32_16x16x32_bf16 v[114:117], v[200:203], v[214:217], v[114:117]
	v_mfma_f32_16x16x32_bf16 v[102:105], v[192:195], v[222:225], v[102:105]
	v_mfma_f32_16x16x32_bf16 v[98:101], v[200:203], v[222:225], v[98:101]
	v_mfma_f32_16x16x32_bf16 v[86:89], v[192:195], v[230:233], v[86:89]
	v_mfma_f32_16x16x32_bf16 v[82:85], v[200:203], v[230:233], v[82:85]
	v_mfma_f32_16x16x32_bf16 v[70:73], v[192:195], v[238:241], v[70:73]
	v_mfma_f32_16x16x32_bf16 v[66:69], v[200:203], v[238:241], v[66:69]
	s_barrier
	s_mov_b32 m0, s53
	v_add_u32_e32 v144, s75, v160
	ds_read_b128 v[204:207], v184 offset:16384
	ds_read_b128 v[214:217], v184 offset:17408
	ds_read_b128 v[218:221], v184 offset:18432
	ds_read_b128 v[222:225], v184 offset:19456
	ds_read_b128 v[226:229], v184 offset:20480
	ds_read_b128 v[230:233], v184 offset:21504
	ds_read_b128 v[234:237], v184 offset:22528
	ds_read_b128 v[238:241], v184 offset:23552
	global_load_lds_dwordx4 v144, s[20:21]
	v_add_u32_e32 v144, s45, v144
	s_mov_b32 m0, s54
	s_nop 0
	global_load_lds_dwordx4 v144, s[20:21]
	v_add_u32_e32 v144, s75, v161
	s_mov_b32 m0, s55
	s_nop 0
	global_load_lds_dwordx4 v144, s[20:21]
	v_add_u32_e32 v144, s45, v144
	s_mov_b32 m0, s56
	s_nop 0
	global_load_lds_dwordx4 v144, s[20:21]
	v_add_u32_e32 v144, s50, v1
	s_mov_b32 m0, s52
	s_nop 0
	global_load_lds_dwordx4 v144, s[8:9]
	v_add_u32_e32 v144, s44, v144
	s_mov_b32 m0, s57
	s_nop 0
	global_load_lds_dwordx4 v144, s[8:9]
	s_waitcnt vmcnt(8)
	s_waitcnt lgkmcnt(0)
	s_barrier
	s_waitcnt lgkmcnt(0)
	v_mfma_f32_16x16x32_bf16 v[62:65], v[140:143], v[204:207], v[62:65]
	v_mfma_f32_16x16x32_bf16 v[58:61], v[136:139], v[204:207], v[58:61]
	v_mfma_f32_16x16x32_bf16 v[46:49], v[140:143], v[218:221], v[46:49]
	v_mfma_f32_16x16x32_bf16 v[42:45], v[136:139], v[218:221], v[42:45]
	v_mfma_f32_16x16x32_bf16 v[30:33], v[140:143], v[226:229], v[30:33]
	v_mfma_f32_16x16x32_bf16 v[26:29], v[136:139], v[226:229], v[26:29]
	v_mfma_f32_16x16x32_bf16 v[14:17], v[140:143], v[234:237], v[14:17]
	v_mfma_f32_16x16x32_bf16 v[10:13], v[136:139], v[234:237], v[10:13]
	v_mfma_f32_16x16x32_bf16 v[62:65], v[132:135], v[214:217], v[62:65]
	v_mfma_f32_16x16x32_bf16 v[58:61], v[188:191], v[214:217], v[58:61]
	v_mfma_f32_16x16x32_bf16 v[46:49], v[132:135], v[222:225], v[46:49]
	v_mfma_f32_16x16x32_bf16 v[42:45], v[188:191], v[222:225], v[42:45]
	v_mfma_f32_16x16x32_bf16 v[30:33], v[132:135], v[230:233], v[30:33]
	v_mfma_f32_16x16x32_bf16 v[26:29], v[188:191], v[230:233], v[26:29]
	v_mfma_f32_16x16x32_bf16 v[14:17], v[132:135], v[238:241], v[14:17]
	v_mfma_f32_16x16x32_bf16 v[10:13], v[188:191], v[238:241], v[10:13]
	v_mfma_f32_16x16x32_bf16 v[54:57], v[154:157], v[204:207], v[54:57]
	v_mfma_f32_16x16x32_bf16 v[50:53], v[196:199], v[204:207], v[50:53]
	v_mfma_f32_16x16x32_bf16 v[38:41], v[154:157], v[218:221], v[38:41]
	v_mfma_f32_16x16x32_bf16 v[34:37], v[196:199], v[218:221], v[34:37]
	v_mfma_f32_16x16x32_bf16 v[22:25], v[154:157], v[226:229], v[22:25]
	v_mfma_f32_16x16x32_bf16 v[18:21], v[196:199], v[226:229], v[18:21]
	v_mfma_f32_16x16x32_bf16 v[6:9], v[154:157], v[234:237], v[6:9]
	v_mfma_f32_16x16x32_bf16 v[2:5], v[196:199], v[234:237], v[2:5]
	v_mfma_f32_16x16x32_bf16 v[54:57], v[192:195], v[214:217], v[54:57]
	v_mfma_f32_16x16x32_bf16 v[50:53], v[200:203], v[214:217], v[50:53]
	v_mfma_f32_16x16x32_bf16 v[38:41], v[192:195], v[222:225], v[38:41]
	v_mfma_f32_16x16x32_bf16 v[34:37], v[200:203], v[222:225], v[34:37]
	v_mfma_f32_16x16x32_bf16 v[22:25], v[192:195], v[230:233], v[22:25]
	v_mfma_f32_16x16x32_bf16 v[18:21], v[200:203], v[230:233], v[18:21]
	v_mfma_f32_16x16x32_bf16 v[6:9], v[192:195], v[238:241], v[6:9]
	v_mfma_f32_16x16x32_bf16 v[2:5], v[200:203], v[238:241], v[2:5]
	s_barrier
.Lmidr_1:
	ds_read_b128 v[132:135], v176
	ds_read_b128 v[136:139], v177
	ds_read_b128 v[140:143], v168
	ds_read_b128 v[154:157], v169
	ds_read_b128 v[188:191], v178
	ds_read_b128 v[192:195], v179
	ds_read_b128 v[196:199], v180
	ds_read_b128 v[200:203], v181
	s_mov_b32 m0, s58
	v_add_u32_e32 v144, s50, v162
	ds_read_b128 v[204:207], v184 offset:32768
	ds_read_b128 v[214:217], v184 offset:33792
	ds_read_b128 v[218:221], v184 offset:34816
	ds_read_b128 v[222:225], v184 offset:35840
	ds_read_b128 v[226:229], v184 offset:36864
	ds_read_b128 v[230:233], v184 offset:37888
	ds_read_b128 v[234:237], v184 offset:38912
	ds_read_b128 v[238:241], v184 offset:39936
	global_load_lds_dwordx4 v144, s[8:9]
	v_add_u32_e32 v144, s44, v144
	s_mov_b32 m0, s59
	s_nop 0
	global_load_lds_dwordx4 v144, s[8:9]
	s_waitcnt vmcnt(8)
	s_waitcnt lgkmcnt(0)
	s_barrier
	s_waitcnt lgkmcnt(0)
	v_mfma_f32_16x16x32_bf16 v[126:129], v[140:143], v[204:207], v[126:129]
	v_mfma_f32_16x16x32_bf16 v[122:125], v[136:139], v[204:207], v[122:125]
	v_mfma_f32_16x16x32_bf16 v[110:113], v[140:143], v[218:221], v[110:113]
	v_mfma_f32_16x16x32_bf16 v[106:109], v[136:139], v[218:221], v[106:109]
	v_mfma_f32_16x16x32_bf16 v[94:97], v[140:143], v[226:229], v[94:97]
	v_mfma_f32_16x16x32_bf16 v[90:93], v[136:139], v[226:229], v[90:93]
	v_mfma_f32_16x16x32_bf16 v[78:81], v[140:143], v[234:237], v[78:81]
	v_mfma_f32_16x16x32_bf16 v[74:77], v[136:139], v[234:237], v[74:77]
	v_mfma_f32_16x16x32_bf16 v[126:129], v[132:135], v[214:217], v[126:129]
	v_mfma_f32_16x16x32_bf16 v[122:125], v[188:191], v[214:217], v[122:125]
	v_mfma_f32_16x16x32_bf16 v[110:113], v[132:135], v[222:225], v[110:113]
	v_mfma_f32_16x16x32_bf16 v[106:109], v[188:191], v[222:225], v[106:109]
	v_mfma_f32_16x16x32_bf16 v[94:97], v[132:135], v[230:233], v[94:97]
	v_mfma_f32_16x16x32_bf16 v[90:93], v[188:191], v[230:233], v[90:93]
	v_mfma_f32_16x16x32_bf16 v[78:81], v[132:135], v[238:241], v[78:81]
	v_mfma_f32_16x16x32_bf16 v[74:77], v[188:191], v[238:241], v[74:77]
	v_mfma_f32_16x16x32_bf16 v[118:121], v[154:157], v[204:207], v[118:121]
	v_mfma_f32_16x16x32_bf16 v[114:117], v[196:199], v[204:207], v[114:117]
	v_mfma_f32_16x16x32_bf16 v[102:105], v[154:157], v[218:221], v[102:105]
	v_mfma_f32_16x16x32_bf16 v[98:101], v[196:199], v[218:221], v[98:101]
	v_mfma_f32_16x16x32_bf16 v[86:89], v[154:157], v[226:229], v[86:89]
	v_mfma_f32_16x16x32_bf16 v[82:85], v[196:199], v[226:229], v[82:85]
	v_mfma_f32_16x16x32_bf16 v[70:73], v[154:157], v[234:237], v[70:73]
	v_mfma_f32_16x16x32_bf16 v[66:69], v[196:199], v[234:237], v[66:69]
	v_mfma_f32_16x16x32_bf16 v[118:121], v[192:195], v[214:217], v[118:121]
	v_mfma_f32_16x16x32_bf16 v[114:117], v[200:203], v[214:217], v[114:117]
	v_mfma_f32_16x16x32_bf16 v[102:105], v[192:195], v[222:225], v[102:105]
	v_mfma_f32_16x16x32_bf16 v[98:101], v[200:203], v[222:225], v[98:101]
	v_mfma_f32_16x16x32_bf16 v[86:89], v[192:195], v[230:233], v[86:89]
	v_mfma_f32_16x16x32_bf16 v[82:85], v[200:203], v[230:233], v[82:85]
	v_mfma_f32_16x16x32_bf16 v[70:73], v[192:195], v[238:241], v[70:73]
	v_mfma_f32_16x16x32_bf16 v[66:69], v[200:203], v[238:241], v[66:69]
	s_barrier
	s_mov_b32 m0, s64
	v_add_u32_e32 v144, s51, v160
	ds_read_b128 v[204:207], v184 offset:49152
	ds_read_b128 v[214:217], v184 offset:50176
	ds_read_b128 v[218:221], v184 offset:51200
	ds_read_b128 v[222:225], v184 offset:52224
	ds_read_b128 v[226:229], v184 offset:53248
	ds_read_b128 v[230:233], v184 offset:54272
	ds_read_b128 v[234:237], v184 offset:55296
	ds_read_b128 v[238:241], v184 offset:56320
	global_load_lds_dwordx4 v144, s[20:21]
	v_add_u32_e32 v144, s45, v144
	s_mov_b32 m0, s65
	s_nop 0
	global_load_lds_dwordx4 v144, s[20:21]
	v_add_u32_e32 v144, s51, v161
	s_mov_b32 m0, s68
	s_nop 0
	global_load_lds_dwordx4 v144, s[20:21]
	v_add_u32_e32 v144, s45, v144
	s_mov_b32 m0, s69
	s_nop 0
	global_load_lds_dwordx4 v144, s[20:21]
	v_add_u32_e32 v144, s50, v165
	s_mov_b32 m0, s66
	s_nop 0
	global_load_lds_dwordx4 v144, s[8:9]
	v_add_u32_e32 v144, s44, v144
	s_mov_b32 m0, s67
	s_nop 0
	global_load_lds_dwordx4 v144, s[8:9]
	s_waitcnt vmcnt(8)
	s_waitcnt lgkmcnt(0)
	s_barrier
	s_waitcnt lgkmcnt(0)
	v_mfma_f32_16x16x32_bf16 v[62:65], v[140:143], v[204:207], v[62:65]
	v_mfma_f32_16x16x32_bf16 v[58:61], v[136:139], v[204:207], v[58:61]
	v_mfma_f32_16x16x32_bf16 v[46:49], v[140:143], v[218:221], v[46:49]
	v_mfma_f32_16x16x32_bf16 v[42:45], v[136:139], v[218:221], v[42:45]
	v_mfma_f32_16x16x32_bf16 v[30:33], v[140:143], v[226:229], v[30:33]
	v_mfma_f32_16x16x32_bf16 v[26:29], v[136:139], v[226:229], v[26:29]
	v_mfma_f32_16x16x32_bf16 v[14:17], v[140:143], v[234:237], v[14:17]
	v_mfma_f32_16x16x32_bf16 v[10:13], v[136:139], v[234:237], v[10:13]
	v_mfma_f32_16x16x32_bf16 v[62:65], v[132:135], v[214:217], v[62:65]
	v_mfma_f32_16x16x32_bf16 v[58:61], v[188:191], v[214:217], v[58:61]
	v_mfma_f32_16x16x32_bf16 v[46:49], v[132:135], v[222:225], v[46:49]
	v_mfma_f32_16x16x32_bf16 v[42:45], v[188:191], v[222:225], v[42:45]
	v_mfma_f32_16x16x32_bf16 v[30:33], v[132:135], v[230:233], v[30:33]
	v_mfma_f32_16x16x32_bf16 v[26:29], v[188:191], v[230:233], v[26:29]
	v_mfma_f32_16x16x32_bf16 v[14:17], v[132:135], v[238:241], v[14:17]
	v_mfma_f32_16x16x32_bf16 v[10:13], v[188:191], v[238:241], v[10:13]
	v_mfma_f32_16x16x32_bf16 v[54:57], v[154:157], v[204:207], v[54:57]
	v_mfma_f32_16x16x32_bf16 v[50:53], v[196:199], v[204:207], v[50:53]
	v_mfma_f32_16x16x32_bf16 v[38:41], v[154:157], v[218:221], v[38:41]
	v_mfma_f32_16x16x32_bf16 v[34:37], v[196:199], v[218:221], v[34:37]
	v_mfma_f32_16x16x32_bf16 v[22:25], v[154:157], v[226:229], v[22:25]
	v_mfma_f32_16x16x32_bf16 v[18:21], v[196:199], v[226:229], v[18:21]
	v_mfma_f32_16x16x32_bf16 v[6:9], v[154:157], v[234:237], v[6:9]
	v_mfma_f32_16x16x32_bf16 v[2:5], v[196:199], v[234:237], v[2:5]
	v_mfma_f32_16x16x32_bf16 v[54:57], v[192:195], v[214:217], v[54:57]
	v_mfma_f32_16x16x32_bf16 v[50:53], v[200:203], v[214:217], v[50:53]
	v_mfma_f32_16x16x32_bf16 v[38:41], v[192:195], v[222:225], v[38:41]
	v_mfma_f32_16x16x32_bf16 v[34:37], v[200:203], v[222:225], v[34:37]
	v_mfma_f32_16x16x32_bf16 v[22:25], v[192:195], v[230:233], v[22:25]
	v_mfma_f32_16x16x32_bf16 v[18:21], v[200:203], v[230:233], v[18:21]
	v_mfma_f32_16x16x32_bf16 v[6:9], v[192:195], v[238:241], v[6:9]
	v_mfma_f32_16x16x32_bf16 v[2:5], v[200:203], v[238:241], v[2:5]
	s_barrier
	s_add_i32 s96, s96, 2
	s_addk_i32 s94, 0x100
	s_addk_i32 s95, 0x100
	s_cmp_ge_i32 s96, s62
	s_cbranch_scc1 .LBB0_1844

.LBB0_1981:
	s_setprio 0
	s_cmp_lt_i32 s41, 16
	s_cbranch_scc1 .LBB0_2031
	s_waitcnt vmcnt(0)
	v_cmp_eq_u32_e32 vcc, 0, v0
	s_waitcnt vmcnt(0) lgkmcnt(0)
	s_barrier
	s_and_saveexec_b64 s[2:3], vcc
	s_cbranch_execz .LBB0_2030
	v_mov_b32_e32 v1, s92
	s_waitcnt vmcnt(0) expcnt(0) lgkmcnt(0)
	ds_read_b32 v3, v1
	ds_read_b32 v1, v1 offset:4
	s_waitcnt lgkmcnt(1)
	v_cmp_ne_u32_e32 vcc, 0, v3
	s_cbranch_vccnz .LBB0_1998
	v_readlane_b32 s4, v254, 1
	v_readlane_b32 s5, v254, 2
	s_load_dwordx2 s[8:9], s[4:5], 0x4
	s_add_u32 s4, s42, 0x1000
	s_addc_u32 s5, s43, 0
	s_add_u32 s6, s42, 0x1100
	s_addc_u32 s7, s43, 0
	s_waitcnt lgkmcnt(0)
	s_mul_i32 s18, s8, s34
	s_add_u32 s8, s42, 0x1200
	s_mul_i32 s18, s18, s9
	s_addc_u32 s9, s43, 0
	s_add_u32 s10, s42, 0x1300
	s_addc_u32 s11, s43, 0
	s_mov_b32 s19, 1
	v_mov_b32_e32 v17, 0
	s_branch .LBB0_1986

.LBB0_2578:
.LBB0_2579:
	s_cmp_gt_i32 s40, 20
	s_cselect_b64 s[2:3], -1, 0
	s_cmp_lt_i32 s41, 21
	s_cselect_b64 s[4:5], -1, 0
	s_or_b64 s[2:3], s[2:3], s[4:5]
	s_and_b64 vcc, exec, s[2:3]
	s_cbranch_vccnz .LBB0_2722
	s_cmp_ge_u32 s27, 4
	s_cbranch_scc0 .Lsp_20
	s_setprio 1
.Lsp_20:
	v_mov_b32_e32 v2, v0
	s_cmpk_lt_i32 s26, 0x400
	s_waitcnt lgkmcnt(0)
	s_movk_i32 s12, 0x600
	v_readfirstlane_b32 s14, v2
	s_movk_i32 s16, 0x600
	s_movk_i32 s10, 0x600
	s_cselect_b64 s[2:3], -1, 0
	s_cmpk_gt_i32 s26, 0x3ff
	s_cbranch_scc1 .LBB0_2583
	s_ashr_i32 s4, s26, 31
	s_lshr_b32 s4, s4, 29
	s_add_i32 s6, s26, s4
	s_and_b32 s4, s6, -8
	s_sub_i32 s7, s26, s4
	s_cmp_gt_i32 s7, -1
	s_cbranch_scc0 .LBB0_2668
	s_lshl_b32 s8, s7, 7
	s_cbranch_execz .LBB0_2669
	s_branch .LBB0_2670

.LBB0_2595:
	s_andn2_b64 vcc, exec, s[12:13]
	s_cbranch_vccnz .Lzs_11
	s_add_i32 s60, s64, 0x80
	s_addk_i32 s63, 0x100
	s_mov_b32 s64, 0
	ds_read_b128 v[130:133], v206
	ds_read_b128 v[134:137], v207
	ds_read_b128 v[138:141], v202
	ds_read_b128 v[142:145], v203
	ds_read_b128 v[146:149], v208
	ds_read_b128 v[150:153], v209
	ds_read_b128 v[154:157], v211
	ds_read_b128 v[158:161], v213
	s_add_i32 s65, s60, 0x80
	s_cmp_eq_u32 s84, s64
	s_cselect_b32 s75, s61, s63
	s_cselect_b32 s65, s5, s65
	v_add_u32_e32 v194, s60, v221
	s_add_i32 m0, s45, 0xc000
	ds_read_b128 v[162:165], v222
	ds_read_b128 v[166:169], v222 offset:1024
	ds_read_b128 v[170:173], v222 offset:2048
	ds_read_b128 v[174:177], v222 offset:3072
	ds_read_b128 v[182:185], v222 offset:4096
	ds_read_b128 v[186:189], v222 offset:5120
	ds_read_b128 v[190:193], v222 offset:6144
	ds_read_b128 v[224:227], v222 offset:7168
	global_load_lds_dwordx4 v194, s[6:7]
	v_add_u32_e32 v194, s60, v220
	s_add_i32 m0, s45, 0xe000
	s_nop 0
	global_load_lds_dwordx4 v194, s[6:7]
	s_waitcnt vmcnt(8)
	s_waitcnt lgkmcnt(0)
	s_barrier
	s_waitcnt lgkmcnt(0)
	v_mfma_f32_16x16x32_bf16 v[126:129], v[138:141], v[162:165], 0
	v_mfma_f32_16x16x32_bf16 v[122:125], v[134:137], v[162:165], 0
	v_mfma_f32_16x16x32_bf16 v[110:113], v[138:141], v[170:173], 0
	v_mfma_f32_16x16x32_bf16 v[106:109], v[134:137], v[170:173], 0
	v_mfma_f32_16x16x32_bf16 v[94:97], v[138:141], v[182:185], 0
	v_mfma_f32_16x16x32_bf16 v[90:93], v[134:137], v[182:185], 0
	v_mfma_f32_16x16x32_bf16 v[78:81], v[138:141], v[190:193], 0
	v_mfma_f32_16x16x32_bf16 v[74:77], v[134:137], v[190:193], 0
	v_mfma_f32_16x16x32_bf16 v[126:129], v[130:133], v[166:169], v[126:129]
	v_mfma_f32_16x16x32_bf16 v[122:125], v[146:149], v[166:169], v[122:125]
	v_mfma_f32_16x16x32_bf16 v[110:113], v[130:133], v[174:177], v[110:113]
	v_mfma_f32_16x16x32_bf16 v[106:109], v[146:149], v[174:177], v[106:109]
	v_mfma_f32_16x16x32_bf16 v[94:97], v[130:133], v[186:189], v[94:97]
	v_mfma_f32_16x16x32_bf16 v[90:93], v[146:149], v[186:189], v[90:93]
	v_mfma_f32_16x16x32_bf16 v[78:81], v[130:133], v[224:227], v[78:81]
	v_mfma_f32_16x16x32_bf16 v[74:77], v[146:149], v[224:227], v[74:77]
	v_mfma_f32_16x16x32_bf16 v[118:121], v[142:145], v[162:165], 0
	v_mfma_f32_16x16x32_bf16 v[114:117], v[154:157], v[162:165], 0
	v_mfma_f32_16x16x32_bf16 v[102:105], v[142:145], v[170:173], 0
	v_mfma_f32_16x16x32_bf16 v[98:101], v[154:157], v[170:173], 0
	v_mfma_f32_16x16x32_bf16 v[86:89], v[142:145], v[182:185], 0
	v_mfma_f32_16x16x32_bf16 v[82:85], v[154:157], v[182:185], 0
	v_mfma_f32_16x16x32_bf16 v[70:73], v[142:145], v[190:193], 0
	v_mfma_f32_16x16x32_bf16 v[66:69], v[154:157], v[190:193], 0
	v_mfma_f32_16x16x32_bf16 v[118:121], v[150:153], v[166:169], v[118:121]
	v_mfma_f32_16x16x32_bf16 v[114:117], v[158:161], v[166:169], v[114:117]
	v_mfma_f32_16x16x32_bf16 v[102:105], v[150:153], v[174:177], v[102:105]
	v_mfma_f32_16x16x32_bf16 v[98:101], v[158:161], v[174:177], v[98:101]
	v_mfma_f32_16x16x32_bf16 v[86:89], v[150:153], v[186:189], v[86:89]
	v_mfma_f32_16x16x32_bf16 v[82:85], v[158:161], v[186:189], v[82:85]
	v_mfma_f32_16x16x32_bf16 v[70:73], v[150:153], v[224:227], v[70:73]
	v_mfma_f32_16x16x32_bf16 v[66:69], v[158:161], v[224:227], v[66:69]
	s_barrier
	s_mov_b32 m0, s66
	v_add_u32_e32 v194, s75, v196
	ds_read_b128 v[162:165], v222 offset:16384
	ds_read_b128 v[166:169], v222 offset:17408
	ds_read_b128 v[170:173], v222 offset:18432
	ds_read_b128 v[174:177], v222 offset:19456
	ds_read_b128 v[182:185], v222 offset:20480
	ds_read_b128 v[186:189], v222 offset:21504
	ds_read_b128 v[190:193], v222 offset:22528
	ds_read_b128 v[224:227], v222 offset:23552
	global_load_lds_dwordx4 v194, s[8:9]
	v_add_u32_e32 v194, s44, v194
	s_mov_b32 m0, s67
	s_nop 0
	global_load_lds_dwordx4 v194, s[8:9]
	v_add_u32_e32 v194, s75, v197
	s_mov_b32 m0, s68
	s_nop 0
	global_load_lds_dwordx4 v194, s[8:9]
	v_add_u32_e32 v194, s44, v194
	s_mov_b32 m0, s69
	s_nop 0
	global_load_lds_dwordx4 v194, s[8:9]
	v_add_u32_e32 v194, s65, v1
	s_mov_b32 m0, s45
	s_nop 0
	global_load_lds_dwordx4 v194, s[6:7]
	v_add_u32_e32 v194, s35, v194
	s_mov_b32 m0, s70
	s_nop 0
	global_load_lds_dwordx4 v194, s[6:7]
	s_waitcnt vmcnt(8)
	s_waitcnt lgkmcnt(0)
	s_barrier
	s_waitcnt lgkmcnt(0)
	v_mfma_f32_16x16x32_bf16 v[62:65], v[138:141], v[162:165], 0
	v_mfma_f32_16x16x32_bf16 v[58:61], v[134:137], v[162:165], 0
	v_mfma_f32_16x16x32_bf16 v[46:49], v[138:141], v[170:173], 0
	v_mfma_f32_16x16x32_bf16 v[42:45], v[134:137], v[170:173], 0
	v_mfma_f32_16x16x32_bf16 v[30:33], v[138:141], v[182:185], 0
	v_mfma_f32_16x16x32_bf16 v[26:29], v[134:137], v[182:185], 0
	v_mfma_f32_16x16x32_bf16 v[14:17], v[138:141], v[190:193], 0
	v_mfma_f32_16x16x32_bf16 v[10:13], v[134:137], v[190:193], 0
	v_mfma_f32_16x16x32_bf16 v[62:65], v[130:133], v[166:169], v[62:65]
	v_mfma_f32_16x16x32_bf16 v[58:61], v[146:149], v[166:169], v[58:61]
	v_mfma_f32_16x16x32_bf16 v[46:49], v[130:133], v[174:177], v[46:49]
	v_mfma_f32_16x16x32_bf16 v[42:45], v[146:149], v[174:177], v[42:45]
	v_mfma_f32_16x16x32_bf16 v[30:33], v[130:133], v[186:189], v[30:33]
	v_mfma_f32_16x16x32_bf16 v[26:29], v[146:149], v[186:189], v[26:29]
	v_mfma_f32_16x16x32_bf16 v[14:17], v[130:133], v[224:227], v[14:17]
	v_mfma_f32_16x16x32_bf16 v[10:13], v[146:149], v[224:227], v[10:13]
	v_mfma_f32_16x16x32_bf16 v[54:57], v[142:145], v[162:165], 0
	v_mfma_f32_16x16x32_bf16 v[50:53], v[154:157], v[162:165], 0
	v_mfma_f32_16x16x32_bf16 v[38:41], v[142:145], v[170:173], 0
	v_mfma_f32_16x16x32_bf16 v[34:37], v[154:157], v[170:173], 0
	v_mfma_f32_16x16x32_bf16 v[22:25], v[142:145], v[182:185], 0
	v_mfma_f32_16x16x32_bf16 v[18:21], v[154:157], v[182:185], 0
	v_mfma_f32_16x16x32_bf16 v[6:9], v[142:145], v[190:193], 0
	v_mfma_f32_16x16x32_bf16 v[2:5], v[154:157], v[190:193], 0
	v_mfma_f32_16x16x32_bf16 v[54:57], v[150:153], v[166:169], v[54:57]
	v_mfma_f32_16x16x32_bf16 v[50:53], v[158:161], v[166:169], v[50:53]
	v_mfma_f32_16x16x32_bf16 v[38:41], v[150:153], v[174:177], v[38:41]
	v_mfma_f32_16x16x32_bf16 v[34:37], v[158:161], v[174:177], v[34:37]
	v_mfma_f32_16x16x32_bf16 v[22:25], v[150:153], v[186:189], v[22:25]
	v_mfma_f32_16x16x32_bf16 v[18:21], v[158:161], v[186:189], v[18:21]
	v_mfma_f32_16x16x32_bf16 v[6:9], v[150:153], v[224:227], v[6:9]
	v_mfma_f32_16x16x32_bf16 v[2:5], v[158:161], v[224:227], v[2:5]
	s_barrier
	s_branch .Lmid_9
.LBB0_2597:
	ds_read_b128 v[130:133], v206
	ds_read_b128 v[134:137], v207
	ds_read_b128 v[138:141], v202
	ds_read_b128 v[142:145], v203
	ds_read_b128 v[146:149], v208
	ds_read_b128 v[150:153], v209
	ds_read_b128 v[154:157], v211
	ds_read_b128 v[158:161], v213
	s_add_i32 s65, s60, 0x80
	s_cmp_eq_u32 s84, s64
	s_cselect_b32 s75, s61, s63
	s_cselect_b32 s65, s5, s65
	v_add_u32_e32 v194, s60, v221
	s_add_i32 m0, s45, 0xc000
	ds_read_b128 v[162:165], v222
	ds_read_b128 v[166:169], v222 offset:1024
	ds_read_b128 v[170:173], v222 offset:2048
	ds_read_b128 v[174:177], v222 offset:3072
	ds_read_b128 v[182:185], v222 offset:4096
	ds_read_b128 v[186:189], v222 offset:5120
	ds_read_b128 v[190:193], v222 offset:6144
	ds_read_b128 v[224:227], v222 offset:7168
	global_load_lds_dwordx4 v194, s[6:7]
	v_add_u32_e32 v194, s60, v220
	s_add_i32 m0, s45, 0xe000
	s_nop 0
	global_load_lds_dwordx4 v194, s[6:7]
	s_waitcnt vmcnt(8)
	s_waitcnt lgkmcnt(0)
	s_barrier
	s_waitcnt lgkmcnt(0)
	v_mfma_f32_16x16x32_bf16 v[126:129], v[138:141], v[162:165], v[126:129]
	v_mfma_f32_16x16x32_bf16 v[122:125], v[134:137], v[162:165], v[122:125]
	v_mfma_f32_16x16x32_bf16 v[110:113], v[138:141], v[170:173], v[110:113]
	v_mfma_f32_16x16x32_bf16 v[106:109], v[134:137], v[170:173], v[106:109]
	v_mfma_f32_16x16x32_bf16 v[94:97], v[138:141], v[182:185], v[94:97]
	v_mfma_f32_16x16x32_bf16 v[90:93], v[134:137], v[182:185], v[90:93]
	v_mfma_f32_16x16x32_bf16 v[78:81], v[138:141], v[190:193], v[78:81]
	v_mfma_f32_16x16x32_bf16 v[74:77], v[134:137], v[190:193], v[74:77]
	v_mfma_f32_16x16x32_bf16 v[126:129], v[130:133], v[166:169], v[126:129]
	v_mfma_f32_16x16x32_bf16 v[122:125], v[146:149], v[166:169], v[122:125]
	v_mfma_f32_16x16x32_bf16 v[110:113], v[130:133], v[174:177], v[110:113]
	v_mfma_f32_16x16x32_bf16 v[106:109], v[146:149], v[174:177], v[106:109]
	v_mfma_f32_16x16x32_bf16 v[94:97], v[130:133], v[186:189], v[94:97]
	v_mfma_f32_16x16x32_bf16 v[90:93], v[146:149], v[186:189], v[90:93]
	v_mfma_f32_16x16x32_bf16 v[78:81], v[130:133], v[224:227], v[78:81]
	v_mfma_f32_16x16x32_bf16 v[74:77], v[146:149], v[224:227], v[74:77]
	v_mfma_f32_16x16x32_bf16 v[118:121], v[142:145], v[162:165], v[118:121]
	v_mfma_f32_16x16x32_bf16 v[114:117], v[154:157], v[162:165], v[114:117]
	v_mfma_f32_16x16x32_bf16 v[102:105], v[142:145], v[170:173], v[102:105]
	v_mfma_f32_16x16x32_bf16 v[98:101], v[154:157], v[170:173], v[98:101]
	v_mfma_f32_16x16x32_bf16 v[86:89], v[142:145], v[182:185], v[86:89]
	v_mfma_f32_16x16x32_bf16 v[82:85], v[154:157], v[182:185], v[82:85]
	v_mfma_f32_16x16x32_bf16 v[70:73], v[142:145], v[190:193], v[70:73]
	v_mfma_f32_16x16x32_bf16 v[66:69], v[154:157], v[190:193], v[66:69]
	v_mfma_f32_16x16x32_bf16 v[118:121], v[150:153], v[166:169], v[118:121]
	v_mfma_f32_16x16x32_bf16 v[114:117], v[158:161], v[166:169], v[114:117]
	v_mfma_f32_16x16x32_bf16 v[102:105], v[150:153], v[174:177], v[102:105]
	v_mfma_f32_16x16x32_bf16 v[98:101], v[158:161], v[174:177], v[98:101]
	v_mfma_f32_16x16x32_bf16 v[86:89], v[150:153], v[186:189], v[86:89]
	v_mfma_f32_16x16x32_bf16 v[82:85], v[158:161], v[186:189], v[82:85]
	v_mfma_f32_16x16x32_bf16 v[70:73], v[150:153], v[224:227], v[70:73]
	v_mfma_f32_16x16x32_bf16 v[66:69], v[158:161], v[224:227], v[66:69]
	s_barrier
	s_mov_b32 m0, s66
	v_add_u32_e32 v194, s75, v196
	ds_read_b128 v[162:165], v222 offset:16384
	ds_read_b128 v[166:169], v222 offset:17408
	ds_read_b128 v[170:173], v222 offset:18432
	ds_read_b128 v[174:177], v222 offset:19456
	ds_read_b128 v[182:185], v222 offset:20480
	ds_read_b128 v[186:189], v222 offset:21504
	ds_read_b128 v[190:193], v222 offset:22528
	ds_read_b128 v[224:227], v222 offset:23552
	global_load_lds_dwordx4 v194, s[8:9]
	v_add_u32_e32 v194, s44, v194
	s_mov_b32 m0, s67
	s_nop 0
	global_load_lds_dwordx4 v194, s[8:9]
	v_add_u32_e32 v194, s75, v197
	s_mov_b32 m0, s68
	s_nop 0
	global_load_lds_dwordx4 v194, s[8:9]
	v_add_u32_e32 v194, s44, v194
	s_mov_b32 m0, s69
	s_nop 0
	global_load_lds_dwordx4 v194, s[8:9]
	v_add_u32_e32 v194, s65, v1
	s_mov_b32 m0, s45
	s_nop 0
	global_load_lds_dwordx4 v194, s[6:7]
	v_add_u32_e32 v194, s35, v194
	s_mov_b32 m0, s70
	s_nop 0
	global_load_lds_dwordx4 v194, s[6:7]
	s_waitcnt vmcnt(8)
	s_waitcnt lgkmcnt(0)
	s_barrier
	s_waitcnt lgkmcnt(0)
	v_mfma_f32_16x16x32_bf16 v[62:65], v[138:141], v[162:165], v[62:65]
	v_mfma_f32_16x16x32_bf16 v[58:61], v[134:137], v[162:165], v[58:61]
	v_mfma_f32_16x16x32_bf16 v[46:49], v[138:141], v[170:173], v[46:49]
	v_mfma_f32_16x16x32_bf16 v[42:45], v[134:137], v[170:173], v[42:45]
	v_mfma_f32_16x16x32_bf16 v[30:33], v[138:141], v[182:185], v[30:33]
	v_mfma_f32_16x16x32_bf16 v[26:29], v[134:137], v[182:185], v[26:29]
	v_mfma_f32_16x16x32_bf16 v[14:17], v[138:141], v[190:193], v[14:17]
	v_mfma_f32_16x16x32_bf16 v[10:13], v[134:137], v[190:193], v[10:13]
	v_mfma_f32_16x16x32_bf16 v[62:65], v[130:133], v[166:169], v[62:65]
	v_mfma_f32_16x16x32_bf16 v[58:61], v[146:149], v[166:169], v[58:61]
	v_mfma_f32_16x16x32_bf16 v[46:49], v[130:133], v[174:177], v[46:49]
	v_mfma_f32_16x16x32_bf16 v[42:45], v[146:149], v[174:177], v[42:45]
	v_mfma_f32_16x16x32_bf16 v[30:33], v[130:133], v[186:189], v[30:33]
	v_mfma_f32_16x16x32_bf16 v[26:29], v[146:149], v[186:189], v[26:29]
	v_mfma_f32_16x16x32_bf16 v[14:17], v[130:133], v[224:227], v[14:17]
	v_mfma_f32_16x16x32_bf16 v[10:13], v[146:149], v[224:227], v[10:13]
	v_mfma_f32_16x16x32_bf16 v[54:57], v[142:145], v[162:165], v[54:57]
	v_mfma_f32_16x16x32_bf16 v[50:53], v[154:157], v[162:165], v[50:53]
	v_mfma_f32_16x16x32_bf16 v[38:41], v[142:145], v[170:173], v[38:41]
	v_mfma_f32_16x16x32_bf16 v[34:37], v[154:157], v[170:173], v[34:37]
	v_mfma_f32_16x16x32_bf16 v[22:25], v[142:145], v[182:185], v[22:25]
	v_mfma_f32_16x16x32_bf16 v[18:21], v[154:157], v[182:185], v[18:21]
	v_mfma_f32_16x16x32_bf16 v[6:9], v[142:145], v[190:193], v[6:9]
	v_mfma_f32_16x16x32_bf16 v[2:5], v[154:157], v[190:193], v[2:5]
	v_mfma_f32_16x16x32_bf16 v[54:57], v[150:153], v[166:169], v[54:57]
	v_mfma_f32_16x16x32_bf16 v[50:53], v[158:161], v[166:169], v[50:53]
	v_mfma_f32_16x16x32_bf16 v[38:41], v[150:153], v[174:177], v[38:41]
	v_mfma_f32_16x16x32_bf16 v[34:37], v[158:161], v[174:177], v[34:37]
	v_mfma_f32_16x16x32_bf16 v[22:25], v[150:153], v[186:189], v[22:25]
	v_mfma_f32_16x16x32_bf16 v[18:21], v[158:161], v[186:189], v[18:21]
	v_mfma_f32_16x16x32_bf16 v[6:9], v[150:153], v[224:227], v[6:9]
	v_mfma_f32_16x16x32_bf16 v[2:5], v[158:161], v[224:227], v[2:5]
	s_barrier
.Lmid_9:
	ds_read_b128 v[130:133], v214
	ds_read_b128 v[134:137], v215
	ds_read_b128 v[138:141], v204
	ds_read_b128 v[142:145], v205
	ds_read_b128 v[146:149], v216
	ds_read_b128 v[150:153], v217
	ds_read_b128 v[154:157], v218
	ds_read_b128 v[158:161], v219
	s_mov_b32 m0, s71
	v_add_u32_e32 v194, s65, v198
	ds_read_b128 v[162:165], v222 offset:32768
	ds_read_b128 v[166:169], v222 offset:33792
	ds_read_b128 v[170:173], v222 offset:34816
	ds_read_b128 v[174:177], v222 offset:35840
	ds_read_b128 v[182:185], v222 offset:36864
	ds_read_b128 v[186:189], v222 offset:37888
	ds_read_b128 v[190:193], v222 offset:38912
	ds_read_b128 v[224:227], v222 offset:39936
	global_load_lds_dwordx4 v194, s[6:7]
	v_add_u32_e32 v194, s35, v194
	s_mov_b32 m0, s72
	s_nop 0
	global_load_lds_dwordx4 v194, s[6:7]
	s_waitcnt vmcnt(8)
	s_waitcnt lgkmcnt(0)
	s_barrier
	s_waitcnt lgkmcnt(0)
	v_mfma_f32_16x16x32_bf16 v[126:129], v[138:141], v[162:165], v[126:129]
	v_mfma_f32_16x16x32_bf16 v[122:125], v[134:137], v[162:165], v[122:125]
	v_mfma_f32_16x16x32_bf16 v[110:113], v[138:141], v[170:173], v[110:113]
	v_mfma_f32_16x16x32_bf16 v[106:109], v[134:137], v[170:173], v[106:109]
	v_mfma_f32_16x16x32_bf16 v[94:97], v[138:141], v[182:185], v[94:97]
	v_mfma_f32_16x16x32_bf16 v[90:93], v[134:137], v[182:185], v[90:93]
	v_mfma_f32_16x16x32_bf16 v[78:81], v[138:141], v[190:193], v[78:81]
	v_mfma_f32_16x16x32_bf16 v[74:77], v[134:137], v[190:193], v[74:77]
	v_mfma_f32_16x16x32_bf16 v[126:129], v[130:133], v[166:169], v[126:129]
	v_mfma_f32_16x16x32_bf16 v[122:125], v[146:149], v[166:169], v[122:125]
	v_mfma_f32_16x16x32_bf16 v[110:113], v[130:133], v[174:177], v[110:113]
	v_mfma_f32_16x16x32_bf16 v[106:109], v[146:149], v[174:177], v[106:109]
	v_mfma_f32_16x16x32_bf16 v[94:97], v[130:133], v[186:189], v[94:97]
	v_mfma_f32_16x16x32_bf16 v[90:93], v[146:149], v[186:189], v[90:93]
	v_mfma_f32_16x16x32_bf16 v[78:81], v[130:133], v[224:227], v[78:81]
	v_mfma_f32_16x16x32_bf16 v[74:77], v[146:149], v[224:227], v[74:77]
	v_mfma_f32_16x16x32_bf16 v[118:121], v[142:145], v[162:165], v[118:121]
	v_mfma_f32_16x16x32_bf16 v[114:117], v[154:157], v[162:165], v[114:117]
	v_mfma_f32_16x16x32_bf16 v[102:105], v[142:145], v[170:173], v[102:105]
	v_mfma_f32_16x16x32_bf16 v[98:101], v[154:157], v[170:173], v[98:101]
	v_mfma_f32_16x16x32_bf16 v[86:89], v[142:145], v[182:185], v[86:89]
	v_mfma_f32_16x16x32_bf16 v[82:85], v[154:157], v[182:185], v[82:85]
	v_mfma_f32_16x16x32_bf16 v[70:73], v[142:145], v[190:193], v[70:73]
	v_mfma_f32_16x16x32_bf16 v[66:69], v[154:157], v[190:193], v[66:69]
	v_mfma_f32_16x16x32_bf16 v[118:121], v[150:153], v[166:169], v[118:121]
	v_mfma_f32_16x16x32_bf16 v[114:117], v[158:161], v[166:169], v[114:117]
	v_mfma_f32_16x16x32_bf16 v[102:105], v[150:153], v[174:177], v[102:105]
	v_mfma_f32_16x16x32_bf16 v[98:101], v[158:161], v[174:177], v[98:101]
	v_mfma_f32_16x16x32_bf16 v[86:89], v[150:153], v[186:189], v[86:89]
	v_mfma_f32_16x16x32_bf16 v[82:85], v[158:161], v[186:189], v[82:85]
	v_mfma_f32_16x16x32_bf16 v[70:73], v[150:153], v[224:227], v[70:73]
	v_mfma_f32_16x16x32_bf16 v[66:69], v[158:161], v[224:227], v[66:69]
	s_barrier
	s_addk_i32 s75, 0x80
	s_mov_b32 m0, s77
	v_add_u32_e32 v194, s75, v196
	ds_read_b128 v[162:165], v222 offset:49152
	ds_read_b128 v[166:169], v222 offset:50176
	ds_read_b128 v[170:173], v222 offset:51200
	ds_read_b128 v[174:177], v222 offset:52224
	ds_read_b128 v[182:185], v222 offset:53248
	ds_read_b128 v[186:189], v222 offset:54272
	ds_read_b128 v[190:193], v222 offset:55296
	ds_read_b128 v[224:227], v222 offset:56320
	global_load_lds_dwordx4 v194, s[8:9]
	v_add_u32_e32 v194, s44, v194
	s_mov_b32 m0, s78
	s_nop 0
	global_load_lds_dwordx4 v194, s[8:9]
	v_add_u32_e32 v194, s75, v197
	s_mov_b32 m0, s81
	s_nop 0
	global_load_lds_dwordx4 v194, s[8:9]
	v_add_u32_e32 v194, s44, v194
	s_mov_b32 m0, s82
	s_nop 0
	global_load_lds_dwordx4 v194, s[8:9]
	v_add_u32_e32 v194, s65, v201
	s_mov_b32 m0, s79
	s_nop 0
	global_load_lds_dwordx4 v194, s[6:7]
	v_add_u32_e32 v194, s35, v194
	s_mov_b32 m0, s80
	s_nop 0
	global_load_lds_dwordx4 v194, s[6:7]
	s_waitcnt vmcnt(8)
	s_waitcnt lgkmcnt(0)
	s_barrier
	s_waitcnt lgkmcnt(0)
	v_mfma_f32_16x16x32_bf16 v[62:65], v[138:141], v[162:165], v[62:65]
	v_mfma_f32_16x16x32_bf16 v[58:61], v[134:137], v[162:165], v[58:61]
	v_mfma_f32_16x16x32_bf16 v[46:49], v[138:141], v[170:173], v[46:49]
	v_mfma_f32_16x16x32_bf16 v[42:45], v[134:137], v[170:173], v[42:45]
	v_mfma_f32_16x16x32_bf16 v[30:33], v[138:141], v[182:185], v[30:33]
	v_mfma_f32_16x16x32_bf16 v[26:29], v[134:137], v[182:185], v[26:29]
	v_mfma_f32_16x16x32_bf16 v[14:17], v[138:141], v[190:193], v[14:17]
	v_mfma_f32_16x16x32_bf16 v[10:13], v[134:137], v[190:193], v[10:13]
	v_mfma_f32_16x16x32_bf16 v[62:65], v[130:133], v[166:169], v[62:65]
	v_mfma_f32_16x16x32_bf16 v[58:61], v[146:149], v[166:169], v[58:61]
	v_mfma_f32_16x16x32_bf16 v[46:49], v[130:133], v[174:177], v[46:49]
	v_mfma_f32_16x16x32_bf16 v[42:45], v[146:149], v[174:177], v[42:45]
	v_mfma_f32_16x16x32_bf16 v[30:33], v[130:133], v[186:189], v[30:33]
	v_mfma_f32_16x16x32_bf16 v[26:29], v[146:149], v[186:189], v[26:29]
	v_mfma_f32_16x16x32_bf16 v[14:17], v[130:133], v[224:227], v[14:17]
	v_mfma_f32_16x16x32_bf16 v[10:13], v[146:149], v[224:227], v[10:13]
	v_mfma_f32_16x16x32_bf16 v[54:57], v[142:145], v[162:165], v[54:57]
	v_mfma_f32_16x16x32_bf16 v[50:53], v[154:157], v[162:165], v[50:53]
	v_mfma_f32_16x16x32_bf16 v[38:41], v[142:145], v[170:173], v[38:41]
	v_mfma_f32_16x16x32_bf16 v[34:37], v[154:157], v[170:173], v[34:37]
	v_mfma_f32_16x16x32_bf16 v[22:25], v[142:145], v[182:185], v[22:25]
	v_mfma_f32_16x16x32_bf16 v[18:21], v[154:157], v[182:185], v[18:21]
	v_mfma_f32_16x16x32_bf16 v[6:9], v[142:145], v[190:193], v[6:9]
	v_mfma_f32_16x16x32_bf16 v[2:5], v[154:157], v[190:193], v[2:5]
	v_mfma_f32_16x16x32_bf16 v[54:57], v[150:153], v[166:169], v[54:57]
	v_mfma_f32_16x16x32_bf16 v[50:53], v[158:161], v[166:169], v[50:53]
	v_mfma_f32_16x16x32_bf16 v[38:41], v[150:153], v[174:177], v[38:41]
	v_mfma_f32_16x16x32_bf16 v[34:37], v[158:161], v[174:177], v[34:37]
	v_mfma_f32_16x16x32_bf16 v[22:25], v[150:153], v[186:189], v[22:25]
	v_mfma_f32_16x16x32_bf16 v[18:21], v[158:161], v[186:189], v[18:21]
	v_mfma_f32_16x16x32_bf16 v[6:9], v[150:153], v[224:227], v[6:9]
	v_mfma_f32_16x16x32_bf16 v[2:5], v[158:161], v[224:227], v[2:5]
	s_barrier
	s_add_i32 s64, s64, 2
	s_addk_i32 s60, 0x100
	s_addk_i32 s63, 0x100
	s_cmp_ge_i32 s64, s74
	s_cbranch_scc0 .LBB0_2597

.LBB0_2667:
	s_waitcnt vmcnt(0)
	v_readlane_b32 s92, v254, 3
	s_barrier
	s_setprio 0
	s_cmp_lt_i32 s41, 22
	s_cbranch_scc1 .LBB0_2721
	s_branch .LBB0_2672

.LBB0_2671:
	s_setprio 0
	s_cmp_lt_i32 s41, 22
	s_cbranch_scc1 .LBB0_2721

.LBB0_2917:
.LBB0_2918:
	s_cmp_gt_i32 s40, 23
	s_cselect_b64 s[2:3], -1, 0
	s_cmp_lt_i32 s41, 24
	s_cselect_b64 s[4:5], -1, 0
	s_or_b64 s[2:3], s[2:3], s[4:5]
	s_and_b64 vcc, exec, s[2:3]
	s_cbranch_vccnz .LBB0_2996
	s_cmp_ge_u32 s27, 4
	s_cbranch_scc0 .Lsp_23
	s_setprio 1
.Lsp_23:
	v_mov_b32_e32 v1, 0x6c2000
	global_load_dword v1, v1, s[38:39] offset:2048
	v_mov_b32_e32 v2, v0
	s_movk_i32 s14, 0x400
	s_movk_i32 s70, 0x400
	s_movk_i32 s17, 0x400
	v_readfirstlane_b32 s16, v2
	s_waitcnt vmcnt(0)
	v_readfirstlane_b32 s19, v1
	s_mul_i32 s2, s19, 44
	s_cmp_ge_i32 s26, s2
	s_cbranch_scc1 .LBB0_2945
	s_ashr_i32 s3, s2, 31
	s_lshr_b32 s4, s3, 29
	s_add_i32 s4, s2, s4
	s_ashr_i32 s21, s4, 3
	s_and_b32 s4, s4, -8
	s_ashr_i32 s31, s26, 31
	s_sub_i32 s30, s2, s4
	s_lshr_b32 s4, s31, 29
	s_add_i32 s6, s26, s4
	s_and_b32 s4, s6, -8
	s_sub_i32 s7, s26, s4
	s_add_i32 s35, s21, 1
	s_cmp_ge_i32 s7, s30
	s_mul_i32 s44, s35, s30
	s_cbranch_scc0 .LBB0_2922
	s_sub_i32 s4, s7, s30
	s_mul_i32 s4, s4, s21
	s_add_i32 s9, s44, s4
	s_cbranch_execz .LBB0_2923
	s_branch .LBB0_2924

.LBB0_2935:
	s_andn2_b64 vcc, exec, s[14:15]
	s_cbranch_vccnz .Lzs_12
	s_add_i32 s28, s82, 0x80
	s_add_i32 s82, s83, 0x100
	s_mov_b32 s83, 0
	ds_read_b128 v[18:21], v180
	ds_read_b128 v[22:25], v181
	ds_read_b128 v[26:29], v188
	ds_read_b128 v[30:33], v189
	ds_read_b128 v[2:5], v182
	ds_read_b128 v[6:9], v183
	ds_read_b128 v[10:13], v190
	ds_read_b128 v[14:17], v191
	s_add_i32 s84, s28, 0x80
	s_cmp_eq_u32 s67, s83
	s_cselect_b32 s86, s25, s84
	s_cselect_b32 s87, s29, s82
	s_add_i32 s84, s86, 0x80
	s_add_i32 s85, s87, 0x80
	v_mov_b32_e32 v172, v176
	ds_read_b128 v[164:167], v196
	ds_read_b128 v[168:171], v196 offset:1024
	ds_read_b128 v[198:201], v196 offset:2048
	ds_read_b128 v[202:205], v196 offset:3072
	ds_read_b128 v[214:217], v196 offset:4096
	ds_read_b128 v[218:221], v196 offset:5120
	ds_read_b128 v[222:225], v196 offset:6144
	ds_read_b128 v[226:229], v196 offset:7168
	s_add_i32 s88, s28, s65
	v_add_u32_e32 v172, s88, v172
	s_add_i32 m0, s49, 0xc000
	s_add_i32 s88, s28, s70
	global_load_lds_dwordx4 v172, s[4:5]
	v_mov_b32_e32 v172, v176
	s_add_i32 m0, s49, 0xe000
	v_add_u32_e32 v172, s88, v172
	global_load_lds_dwordx4 v172, s[4:5]
	s_waitcnt vmcnt(8)
	s_waitcnt lgkmcnt(0)
	s_barrier
	s_waitcnt lgkmcnt(0)
	v_mfma_f32_16x16x128_f8f6f4 v[158:161], v[18:25], v[164:171], 0
	v_mfma_f32_16x16x128_f8f6f4 v[154:157], v[26:33], v[164:171], 0
	v_mfma_f32_16x16x128_f8f6f4 v[150:153], v[18:25], v[198:205], 0
	v_mfma_f32_16x16x128_f8f6f4 v[146:149], v[26:33], v[198:205], 0
	v_mfma_f32_16x16x128_f8f6f4 v[138:141], v[18:25], v[214:221], 0
	v_mfma_f32_16x16x128_f8f6f4 v[130:133], v[26:33], v[214:221], 0
	v_mfma_f32_16x16x128_f8f6f4 v[122:125], v[18:25], v[222:229], 0
	v_mfma_f32_16x16x128_f8f6f4 v[114:117], v[26:33], v[222:229], 0
	v_mfma_f32_16x16x128_f8f6f4 v[142:145], v[2:9], v[164:171], 0
	v_mfma_f32_16x16x128_f8f6f4 v[134:137], v[10:17], v[164:171], 0
	v_mfma_f32_16x16x128_f8f6f4 v[126:129], v[2:9], v[198:205], 0
	v_mfma_f32_16x16x128_f8f6f4 v[118:121], v[10:17], v[198:205], 0
	v_mfma_f32_16x16x128_f8f6f4 v[110:113], v[2:9], v[214:221], 0
	v_mfma_f32_16x16x128_f8f6f4 v[106:109], v[10:17], v[214:221], 0
	v_mfma_f32_16x16x128_f8f6f4 v[102:105], v[2:9], v[222:229], 0
	v_mfma_f32_16x16x128_f8f6f4 v[98:101], v[10:17], v[222:229], 0
	s_barrier
	v_mov_b32_e32 v172, v177
	ds_read_b128 v[164:167], v196 offset:16384
	ds_read_b128 v[168:171], v196 offset:17408
	ds_read_b128 v[198:201], v196 offset:18432
	ds_read_b128 v[202:205], v196 offset:19456
	ds_read_b128 v[214:217], v196 offset:20480
	ds_read_b128 v[218:221], v196 offset:21504
	ds_read_b128 v[222:225], v196 offset:22528
	ds_read_b128 v[226:229], v196 offset:23552
	s_mov_b32 m0, s50
	v_add_u32_e32 v172, s87, v172
	global_load_lds_dwordx4 v172, s[6:7]
	v_mov_b32_e32 v172, v177
	s_add_i32 s87, s87, s48
	v_add_u32_e32 v172, s87, v172
	s_mov_b32 m0, s51
	s_add_i32 s87, s87, s48
	global_load_lds_dwordx4 v172, s[6:7]
	v_mov_b32_e32 v172, v177
	s_mov_b32 m0, s52
	v_add_u32_e32 v172, s87, v172
	global_load_lds_dwordx4 v172, s[6:7]
	v_mov_b32_e32 v172, v177
	s_add_i32 s87, s87, s48
	v_add_u32_e32 v172, s87, v172
	s_mov_b32 m0, s53
	s_nop 0
	global_load_lds_dwordx4 v172, s[6:7]
	v_mov_b32_e32 v172, v176
	s_mov_b32 m0, s49
	v_add_u32_e32 v172, s86, v172
	global_load_lds_dwordx4 v172, s[4:5]
	v_mov_b32_e32 v172, v176
	s_add_i32 s86, s86, s47
	v_add_u32_e32 v172, s86, v172
	s_mov_b32 m0, s54
	s_nop 0
	global_load_lds_dwordx4 v172, s[4:5]
	s_waitcnt vmcnt(8)
	s_waitcnt lgkmcnt(0)
	s_barrier
	s_waitcnt lgkmcnt(0)
	v_mfma_f32_16x16x128_f8f6f4 v[94:97], v[18:25], v[164:171], 0
	v_mfma_f32_16x16x128_f8f6f4 v[90:93], v[26:33], v[164:171], 0
	v_mfma_f32_16x16x128_f8f6f4 v[86:89], v[18:25], v[198:205], 0
	v_mfma_f32_16x16x128_f8f6f4 v[82:85], v[26:33], v[198:205], 0
	v_mfma_f32_16x16x128_f8f6f4 v[74:77], v[18:25], v[214:221], 0
	v_mfma_f32_16x16x128_f8f6f4 v[66:69], v[26:33], v[214:221], 0
	v_mfma_f32_16x16x128_f8f6f4 v[58:61], v[18:25], v[222:229], 0
	v_mfma_f32_16x16x128_f8f6f4 v[50:53], v[26:33], v[222:229], 0
	v_mfma_f32_16x16x128_f8f6f4 v[78:81], v[2:9], v[164:171], 0
	v_mfma_f32_16x16x128_f8f6f4 v[70:73], v[10:17], v[164:171], 0
	v_mfma_f32_16x16x128_f8f6f4 v[62:65], v[2:9], v[198:205], 0
	v_mfma_f32_16x16x128_f8f6f4 v[54:57], v[10:17], v[198:205], 0
	v_mfma_f32_16x16x128_f8f6f4 v[46:49], v[2:9], v[214:221], 0
	v_mfma_f32_16x16x128_f8f6f4 v[42:45], v[10:17], v[214:221], 0
	v_mfma_f32_16x16x128_f8f6f4 v[38:41], v[2:9], v[222:229], 0
	v_mfma_f32_16x16x128_f8f6f4 v[34:37], v[10:17], v[222:229], 0
	s_barrier
	s_branch .Lmid_10
.LBB0_2937:
	ds_read_b128 v[18:21], v180
	ds_read_b128 v[22:25], v181
	ds_read_b128 v[26:29], v188
	ds_read_b128 v[30:33], v189
	ds_read_b128 v[2:5], v182
	ds_read_b128 v[6:9], v183
	ds_read_b128 v[10:13], v190
	ds_read_b128 v[14:17], v191
	s_add_i32 s84, s28, 0x80
	s_cmp_eq_u32 s67, s83
	s_cselect_b32 s86, s25, s84
	s_cselect_b32 s87, s29, s82
	s_add_i32 s84, s86, 0x80
	s_add_i32 s85, s87, 0x80
	v_mov_b32_e32 v172, v176
	ds_read_b128 v[164:167], v196
	ds_read_b128 v[168:171], v196 offset:1024
	ds_read_b128 v[198:201], v196 offset:2048
	ds_read_b128 v[202:205], v196 offset:3072
	ds_read_b128 v[214:217], v196 offset:4096
	ds_read_b128 v[218:221], v196 offset:5120
	ds_read_b128 v[222:225], v196 offset:6144
	ds_read_b128 v[226:229], v196 offset:7168
	s_add_i32 s88, s28, s65
	v_add_u32_e32 v172, s88, v172
	s_add_i32 m0, s49, 0xc000
	s_add_i32 s88, s28, s70
	global_load_lds_dwordx4 v172, s[4:5]
	v_mov_b32_e32 v172, v176
	s_add_i32 m0, s49, 0xe000
	v_add_u32_e32 v172, s88, v172
	global_load_lds_dwordx4 v172, s[4:5]
	s_waitcnt vmcnt(8)
	s_waitcnt lgkmcnt(0)
	s_barrier
	s_waitcnt lgkmcnt(0)
	v_mfma_f32_16x16x128_f8f6f4 v[158:161], v[18:25], v[164:171], v[158:161]
	v_mfma_f32_16x16x128_f8f6f4 v[154:157], v[26:33], v[164:171], v[154:157]
	v_mfma_f32_16x16x128_f8f6f4 v[150:153], v[18:25], v[198:205], v[150:153]
	v_mfma_f32_16x16x128_f8f6f4 v[146:149], v[26:33], v[198:205], v[146:149]
	v_mfma_f32_16x16x128_f8f6f4 v[138:141], v[18:25], v[214:221], v[138:141]
	v_mfma_f32_16x16x128_f8f6f4 v[130:133], v[26:33], v[214:221], v[130:133]
	v_mfma_f32_16x16x128_f8f6f4 v[122:125], v[18:25], v[222:229], v[122:125]
	v_mfma_f32_16x16x128_f8f6f4 v[114:117], v[26:33], v[222:229], v[114:117]
	v_mfma_f32_16x16x128_f8f6f4 v[142:145], v[2:9], v[164:171], v[142:145]
	v_mfma_f32_16x16x128_f8f6f4 v[134:137], v[10:17], v[164:171], v[134:137]
	v_mfma_f32_16x16x128_f8f6f4 v[126:129], v[2:9], v[198:205], v[126:129]
	v_mfma_f32_16x16x128_f8f6f4 v[118:121], v[10:17], v[198:205], v[118:121]
	v_mfma_f32_16x16x128_f8f6f4 v[110:113], v[2:9], v[214:221], v[110:113]
	v_mfma_f32_16x16x128_f8f6f4 v[106:109], v[10:17], v[214:221], v[106:109]
	v_mfma_f32_16x16x128_f8f6f4 v[102:105], v[2:9], v[222:229], v[102:105]
	v_mfma_f32_16x16x128_f8f6f4 v[98:101], v[10:17], v[222:229], v[98:101]
	s_barrier
	v_mov_b32_e32 v172, v177
	ds_read_b128 v[164:167], v196 offset:16384
	ds_read_b128 v[168:171], v196 offset:17408
	ds_read_b128 v[198:201], v196 offset:18432
	ds_read_b128 v[202:205], v196 offset:19456
	ds_read_b128 v[214:217], v196 offset:20480
	ds_read_b128 v[218:221], v196 offset:21504
	ds_read_b128 v[222:225], v196 offset:22528
	ds_read_b128 v[226:229], v196 offset:23552
	s_mov_b32 m0, s50
	v_add_u32_e32 v172, s87, v172
	global_load_lds_dwordx4 v172, s[6:7]
	v_mov_b32_e32 v172, v177
	s_add_i32 s87, s87, s48
	v_add_u32_e32 v172, s87, v172
	s_mov_b32 m0, s51
	s_add_i32 s87, s87, s48
	global_load_lds_dwordx4 v172, s[6:7]
	v_mov_b32_e32 v172, v177
	s_mov_b32 m0, s52
	v_add_u32_e32 v172, s87, v172
	global_load_lds_dwordx4 v172, s[6:7]
	v_mov_b32_e32 v172, v177
	s_add_i32 s87, s87, s48
	v_add_u32_e32 v172, s87, v172
	s_mov_b32 m0, s53
	s_nop 0
	global_load_lds_dwordx4 v172, s[6:7]
	v_mov_b32_e32 v172, v176
	s_mov_b32 m0, s49
	v_add_u32_e32 v172, s86, v172
	global_load_lds_dwordx4 v172, s[4:5]
	v_mov_b32_e32 v172, v176
	s_add_i32 s86, s86, s47
	v_add_u32_e32 v172, s86, v172
	s_mov_b32 m0, s54
	s_nop 0
	global_load_lds_dwordx4 v172, s[4:5]
	s_waitcnt vmcnt(8)
	s_waitcnt lgkmcnt(0)
	s_barrier
	s_waitcnt lgkmcnt(0)
	v_mfma_f32_16x16x128_f8f6f4 v[94:97], v[18:25], v[164:171], v[94:97]
	v_mfma_f32_16x16x128_f8f6f4 v[90:93], v[26:33], v[164:171], v[90:93]
	v_mfma_f32_16x16x128_f8f6f4 v[86:89], v[18:25], v[198:205], v[86:89]
	v_mfma_f32_16x16x128_f8f6f4 v[82:85], v[26:33], v[198:205], v[82:85]
	v_mfma_f32_16x16x128_f8f6f4 v[74:77], v[18:25], v[214:221], v[74:77]
	v_mfma_f32_16x16x128_f8f6f4 v[66:69], v[26:33], v[214:221], v[66:69]
	v_mfma_f32_16x16x128_f8f6f4 v[58:61], v[18:25], v[222:229], v[58:61]
	v_mfma_f32_16x16x128_f8f6f4 v[50:53], v[26:33], v[222:229], v[50:53]
	v_mfma_f32_16x16x128_f8f6f4 v[78:81], v[2:9], v[164:171], v[78:81]
	v_mfma_f32_16x16x128_f8f6f4 v[70:73], v[10:17], v[164:171], v[70:73]
	v_mfma_f32_16x16x128_f8f6f4 v[62:65], v[2:9], v[198:205], v[62:65]
	v_mfma_f32_16x16x128_f8f6f4 v[54:57], v[10:17], v[198:205], v[54:57]
	v_mfma_f32_16x16x128_f8f6f4 v[46:49], v[2:9], v[214:221], v[46:49]
	v_mfma_f32_16x16x128_f8f6f4 v[42:45], v[10:17], v[214:221], v[42:45]
	v_mfma_f32_16x16x128_f8f6f4 v[38:41], v[2:9], v[222:229], v[38:41]
	v_mfma_f32_16x16x128_f8f6f4 v[34:37], v[10:17], v[222:229], v[34:37]
	s_barrier

.Ltx23_skip:
	ds_read_b128 v[2:5], v184
	ds_read_b128 v[6:9], v185
	ds_read_b128 v[10:13], v192
	ds_read_b128 v[14:17], v193
	ds_read_b128 v[18:21], v186
	ds_read_b128 v[22:25], v187
	ds_read_b128 v[26:29], v194
	ds_read_b128 v[30:33], v195
	v_mov_b32_e32 v172, v176
	ds_read_b128 v[164:167], v196 offset:32768
	ds_read_b128 v[168:171], v196 offset:33792
	ds_read_b128 v[198:201], v196 offset:34816
	ds_read_b128 v[202:205], v196 offset:35840
	ds_read_b128 v[214:217], v196 offset:36864
	ds_read_b128 v[218:221], v196 offset:37888
	ds_read_b128 v[222:225], v196 offset:38912
	ds_read_b128 v[226:229], v196 offset:39936
	s_add_i32 s86, s86, s47
	s_mov_b32 m0, s55
	v_add_u32_e32 v172, s86, v172
	global_load_lds_dwordx4 v172, s[4:5]
	v_mov_b32_e32 v172, v176
	s_add_i32 s86, s86, s47
	v_add_u32_e32 v172, s86, v172
	s_mov_b32 m0, s56
	s_nop 0
	global_load_lds_dwordx4 v172, s[4:5]
	s_waitcnt vmcnt(8)
	s_waitcnt lgkmcnt(0)
	s_barrier
	s_waitcnt lgkmcnt(0)
	v_mfma_f32_16x16x128_f8f6f4 v[158:161], v[2:9], v[164:171], v[158:161]
	v_mfma_f32_16x16x128_f8f6f4 v[154:157], v[10:17], v[164:171], v[154:157]
	v_mfma_f32_16x16x128_f8f6f4 v[150:153], v[2:9], v[198:205], v[150:153]
	v_mfma_f32_16x16x128_f8f6f4 v[146:149], v[10:17], v[198:205], v[146:149]
	v_mfma_f32_16x16x128_f8f6f4 v[138:141], v[2:9], v[214:221], v[138:141]
	v_mfma_f32_16x16x128_f8f6f4 v[130:133], v[10:17], v[214:221], v[130:133]
	v_mfma_f32_16x16x128_f8f6f4 v[122:125], v[2:9], v[222:229], v[122:125]
	v_mfma_f32_16x16x128_f8f6f4 v[114:117], v[10:17], v[222:229], v[114:117]
	v_mfma_f32_16x16x128_f8f6f4 v[142:145], v[18:25], v[164:171], v[142:145]
	v_mfma_f32_16x16x128_f8f6f4 v[134:137], v[26:33], v[164:171], v[134:137]
	v_mfma_f32_16x16x128_f8f6f4 v[126:129], v[18:25], v[198:205], v[126:129]
	v_mfma_f32_16x16x128_f8f6f4 v[118:121], v[26:33], v[198:205], v[118:121]
	v_mfma_f32_16x16x128_f8f6f4 v[110:113], v[18:25], v[214:221], v[110:113]
	v_mfma_f32_16x16x128_f8f6f4 v[106:109], v[26:33], v[214:221], v[106:109]
	v_mfma_f32_16x16x128_f8f6f4 v[102:105], v[18:25], v[222:229], v[102:105]
	v_mfma_f32_16x16x128_f8f6f4 v[98:101], v[26:33], v[222:229], v[98:101]
	s_barrier
	s_cmp_eq_u32 s67, s83
	s_cbranch_scc1 .Lh23_last
	v_mov_b32_e32 v172, v177
	ds_read_b128 v[164:167], v196 offset:49152
	ds_read_b128 v[168:171], v196 offset:50176
	ds_read_b128 v[198:201], v196 offset:51200
	ds_read_b128 v[202:205], v196 offset:52224
	ds_read_b128 v[214:217], v196 offset:53248
	ds_read_b128 v[218:221], v196 offset:54272
	ds_read_b128 v[222:225], v196 offset:55296
	ds_read_b128 v[226:229], v196 offset:56320
	s_mov_b32 m0, s58
	v_add_u32_e32 v172, s85, v172
	global_load_lds_dwordx4 v172, s[6:7]
	v_mov_b32_e32 v172, v177
	s_add_i32 s85, s85, s48
	v_add_u32_e32 v172, s85, v172
	s_mov_b32 m0, s59
	s_add_i32 s85, s85, s48
	global_load_lds_dwordx4 v172, s[6:7]
	v_mov_b32_e32 v172, v177
	s_mov_b32 m0, s62
	v_add_u32_e32 v172, s85, v172
	global_load_lds_dwordx4 v172, s[6:7]
	v_mov_b32_e32 v172, v177
	s_add_i32 s85, s85, s48
	v_add_u32_e32 v172, s85, v172
	s_mov_b32 m0, s63
	s_nop 0
	global_load_lds_dwordx4 v172, s[6:7]
	v_mov_b32_e32 v172, v176
	s_mov_b32 m0, s60
	v_add_u32_e32 v172, s84, v172
	global_load_lds_dwordx4 v172, s[4:5]
	v_mov_b32_e32 v172, v176
	s_add_i32 s84, s84, s47
	v_add_u32_e32 v172, s84, v172
	s_mov_b32 m0, s61
	s_nop 0
	global_load_lds_dwordx4 v172, s[4:5]
	s_waitcnt vmcnt(8)
	s_waitcnt lgkmcnt(0)
	s_barrier
	s_waitcnt lgkmcnt(0)
	v_mfma_f32_16x16x128_f8f6f4 v[94:97], v[2:9], v[164:171], v[94:97]
	v_mfma_f32_16x16x128_f8f6f4 v[90:93], v[10:17], v[164:171], v[90:93]
	v_mfma_f32_16x16x128_f8f6f4 v[86:89], v[2:9], v[198:205], v[86:89]
	v_mfma_f32_16x16x128_f8f6f4 v[82:85], v[10:17], v[198:205], v[82:85]
	v_mfma_f32_16x16x128_f8f6f4 v[74:77], v[2:9], v[214:221], v[74:77]
	v_mfma_f32_16x16x128_f8f6f4 v[66:69], v[10:17], v[214:221], v[66:69]
	v_mfma_f32_16x16x128_f8f6f4 v[58:61], v[2:9], v[222:229], v[58:61]
	v_mfma_f32_16x16x128_f8f6f4 v[50:53], v[10:17], v[222:229], v[50:53]
	v_mfma_f32_16x16x128_f8f6f4 v[78:81], v[18:25], v[164:171], v[78:81]
	v_mfma_f32_16x16x128_f8f6f4 v[70:73], v[26:33], v[164:171], v[70:73]
	v_mfma_f32_16x16x128_f8f6f4 v[62:65], v[18:25], v[198:205], v[62:65]
	v_mfma_f32_16x16x128_f8f6f4 v[54:57], v[26:33], v[198:205], v[54:57]
	v_mfma_f32_16x16x128_f8f6f4 v[46:49], v[18:25], v[214:221], v[46:49]
	v_mfma_f32_16x16x128_f8f6f4 v[42:45], v[26:33], v[214:221], v[42:45]
	v_mfma_f32_16x16x128_f8f6f4 v[38:41], v[18:25], v[222:229], v[38:41]
	v_mfma_f32_16x16x128_f8f6f4 v[34:37], v[26:33], v[222:229], v[34:37]
	s_barrier
	s_add_i32 s83, s83, 2
	s_addk_i32 s28, 0x100
	s_addk_i32 s82, 0x100
	s_cmp_ge_i32 s83, s64
	s_cbranch_scc0 .LBB0_2937
	s_branch .LBB0_2939
.Lh23_last:
	v_mov_b32_e32 v172, v177
	ds_read_b128 v[164:167], v196 offset:49152
	ds_read_b128 v[168:171], v196 offset:50176
	ds_read_b128 v[198:201], v196 offset:51200
	ds_read_b128 v[202:205], v196 offset:52224
	ds_read_b128 v[214:217], v196 offset:53248
	ds_read_b128 v[218:221], v196 offset:54272
	ds_read_b128 v[222:225], v196 offset:55296
	ds_read_b128 v[226:229], v196 offset:56320
	s_mov_b32 m0, s58
	v_add_u32_e32 v172, s85, v172
	global_load_lds_dwordx4 v172, s[6:7]
	v_mov_b32_e32 v172, v177
	s_add_i32 s85, s85, s48
	v_add_u32_e32 v172, s85, v172
	s_mov_b32 m0, s59
	s_add_i32 s85, s85, s48
	global_load_lds_dwordx4 v172, s[6:7]
	v_mov_b32_e32 v172, v177
	s_mov_b32 m0, s62
	v_add_u32_e32 v172, s85, v172
	global_load_lds_dwordx4 v172, s[6:7]
	v_mov_b32_e32 v172, v177
	s_add_i32 s85, s85, s48
	v_add_u32_e32 v172, s85, v172
	s_mov_b32 m0, s63
	s_nop 0
	global_load_lds_dwordx4 v172, s[6:7]
	v_mov_b32_e32 v172, v176
	s_mov_b32 m0, s60
	v_add_u32_e32 v172, s84, v172
	global_load_lds_dwordx4 v172, s[4:5]
	v_mov_b32_e32 v172, v176
	s_add_i32 s84, s84, s47
	v_add_u32_e32 v172, s84, v172
	s_mov_b32 m0, s61
	s_nop 0
	global_load_lds_dwordx4 v172, s[4:5]
	s_mul_hi_i32 s25, s81, 0x2e8ba2e9
	s_lshr_b32 s28, s25, 31
	s_lshr_b32 s25, s25, 3
	s_add_i32 s25, s25, s28
	s_mul_i32 s25, s25, 44
	s_sub_i32 s25, s81, s25
	s_lshl_b32 s28, s25, 7
	s_lshl_b32 s24, s24, 8
	s_add_i32 s24, s24, s66
	s_mul_i32 s24, s24, s71
	s_add_i32 s24, s24, s28
	s_add_i32 s24, s24, s8
	s_add_u32 s100, s12, s24
	s_addc_u32 s101, s13, 0
	s_mov_b32 s98, 0xbfb8aa3b
	v_mul_u32_u24_e32 v206, s71, v178
	v_lshl_add_u32 v206, v179, 3, v206
	v_pk_fma_f32 v[158:159], v[158:159], s[18:19], 0 op_sel_hi:[1,0,0]
	v_pk_fma_f32 v[160:161], v[160:161], s[18:19], 0 op_sel_hi:[1,0,0]
	v_pk_fma_f32 v[154:155], v[154:155], s[18:19], 0 op_sel_hi:[1,0,0]
	v_pk_fma_f32 v[156:157], v[156:157], s[18:19], 0 op_sel_hi:[1,0,0]
	v_pk_fma_f32 v[142:143], v[142:143], s[20:21], 0 op_sel_hi:[1,0,0]
	v_pk_fma_f32 v[144:145], v[144:145], s[20:21], 0 op_sel_hi:[1,0,0]
	v_pk_fma_f32 v[134:135], v[134:135], s[20:21], 0 op_sel_hi:[1,0,0]
	v_pk_fma_f32 v[136:137], v[136:137], s[20:21], 0 op_sel_hi:[1,0,0]
	v_pk_fma_f32 v[150:151], v[150:151], s[18:19], 0 op_sel_hi:[1,0,0]
	v_pk_fma_f32 v[152:153], v[152:153], s[18:19], 0 op_sel_hi:[1,0,0]
	v_pk_fma_f32 v[146:147], v[146:147], s[18:19], 0 op_sel_hi:[1,0,0]
	v_pk_fma_f32 v[148:149], v[148:149], s[18:19], 0 op_sel_hi:[1,0,0]
	v_pk_fma_f32 v[126:127], v[126:127], s[20:21], 0 op_sel_hi:[1,0,0]
	v_pk_fma_f32 v[128:129], v[128:129], s[20:21], 0 op_sel_hi:[1,0,0]
	v_pk_fma_f32 v[118:119], v[118:119], s[20:21], 0 op_sel_hi:[1,0,0]
	v_pk_fma_f32 v[120:121], v[120:121], s[20:21], 0 op_sel_hi:[1,0,0]
	v_pk_mul_f32 v[230:231], v[158:159], s[98:99] op_sel_hi:[1,0]
	v_pk_mul_f32 v[232:233], v[160:161], s[98:99] op_sel_hi:[1,0]
	v_pk_mul_f32 v[234:235], v[154:155], s[98:99] op_sel_hi:[1,0]
	v_pk_mul_f32 v[236:237], v[156:157], s[98:99] op_sel_hi:[1,0]
	v_pk_mul_f32 v[238:239], v[150:151], s[98:99] op_sel_hi:[1,0]
	v_pk_mul_f32 v[240:241], v[152:153], s[98:99] op_sel_hi:[1,0]
	v_pk_mul_f32 v[242:243], v[146:147], s[98:99] op_sel_hi:[1,0]
	v_pk_mul_f32 v[244:245], v[148:149], s[98:99] op_sel_hi:[1,0]
	v_exp_f32_e32 v230, v230
	v_exp_f32_e32 v231, v231
	v_exp_f32_e32 v232, v232
	v_exp_f32_e32 v233, v233
	v_exp_f32_e32 v234, v234
	v_exp_f32_e32 v235, v235
	v_exp_f32_e32 v236, v236
	v_exp_f32_e32 v237, v237
	v_exp_f32_e32 v238, v238
	v_exp_f32_e32 v239, v239
	v_exp_f32_e32 v240, v240
	v_exp_f32_e32 v241, v241
	v_exp_f32_e32 v242, v242
	v_exp_f32_e32 v243, v243
	v_exp_f32_e32 v244, v244
	v_exp_f32_e32 v245, v245
	v_pk_add_f32 v[230:231], v[230:231], 1.0 op_sel_hi:[1,0]
	v_pk_add_f32 v[232:233], v[232:233], 1.0 op_sel_hi:[1,0]
	v_pk_add_f32 v[234:235], v[234:235], 1.0 op_sel_hi:[1,0]
	v_pk_add_f32 v[236:237], v[236:237], 1.0 op_sel_hi:[1,0]
	v_pk_add_f32 v[238:239], v[238:239], 1.0 op_sel_hi:[1,0]
	v_pk_add_f32 v[240:241], v[240:241], 1.0 op_sel_hi:[1,0]
	v_pk_add_f32 v[242:243], v[242:243], 1.0 op_sel_hi:[1,0]
	v_pk_add_f32 v[244:245], v[244:245], 1.0 op_sel_hi:[1,0]
	v_rcp_f32_e32 v230, v230
	v_rcp_f32_e32 v231, v231
	v_rcp_f32_e32 v232, v232
	v_rcp_f32_e32 v233, v233
	v_rcp_f32_e32 v234, v234
	v_rcp_f32_e32 v235, v235
	v_rcp_f32_e32 v236, v236
	v_rcp_f32_e32 v237, v237
	v_rcp_f32_e32 v238, v238
	v_rcp_f32_e32 v239, v239
	v_rcp_f32_e32 v240, v240
	v_rcp_f32_e32 v241, v241
	v_rcp_f32_e32 v242, v242
	v_rcp_f32_e32 v243, v243
	v_rcp_f32_e32 v244, v244
	v_rcp_f32_e32 v245, v245
	v_pk_mul_f32 v[230:231], v[158:159], v[230:231]
	v_pk_mul_f32 v[232:233], v[160:161], v[232:233]
	v_pk_mul_f32 v[234:235], v[154:155], v[234:235]
	v_pk_mul_f32 v[236:237], v[156:157], v[236:237]
	v_pk_mul_f32 v[238:239], v[150:151], v[238:239]
	v_pk_mul_f32 v[240:241], v[152:153], v[240:241]
	v_pk_mul_f32 v[242:243], v[146:147], v[242:243]
	v_pk_mul_f32 v[244:245], v[148:149], v[244:245]
	v_pk_mul_f32 v[142:143], v[142:143], v[230:231]
	v_pk_mul_f32 v[144:145], v[144:145], v[232:233]
	v_pk_mul_f32 v[134:135], v[134:135], v[234:235]
	v_pk_mul_f32 v[136:137], v[136:137], v[236:237]
	v_pk_mul_f32 v[126:127], v[126:127], v[238:239]
	v_pk_mul_f32 v[128:129], v[128:129], v[240:241]
	v_pk_mul_f32 v[118:119], v[118:119], v[242:243]
	v_pk_mul_f32 v[120:121], v[120:121], v[244:245]
	v_med3_f32 v142, v142, s72, v197
	v_med3_f32 v143, v143, s72, v197
	v_med3_f32 v144, v144, s72, v197
	v_med3_f32 v145, v145, s72, v197
	v_med3_f32 v134, v134, s72, v197
	v_med3_f32 v135, v135, s72, v197
	v_med3_f32 v136, v136, s72, v197
	v_med3_f32 v137, v137, s72, v197
	v_med3_f32 v126, v126, s72, v197
	v_med3_f32 v127, v127, s72, v197
	v_med3_f32 v128, v128, s72, v197
	v_med3_f32 v129, v129, s72, v197
	v_med3_f32 v118, v118, s72, v197
	v_med3_f32 v119, v119, s72, v197
	v_med3_f32 v120, v120, s72, v197
	v_med3_f32 v121, v121, s72, v197
	v_cvt_pk_fp8_f32 v246, v142, v143
	v_cvt_pk_fp8_f32 v247, v134, v135
	v_cvt_pk_fp8_f32 v248, v126, v127
	v_cvt_pk_fp8_f32 v249, v118, v119
	v_add_u32_e32 v208, s57, v206
	v_cvt_pk_fp8_f32 v246, v144, v145 op_sel:[0,0,1]
	v_cvt_pk_fp8_f32 v247, v136, v137 op_sel:[0,0,1]
	v_cvt_pk_fp8_f32 v248, v128, v129 op_sel:[0,0,1]
	v_cvt_pk_fp8_f32 v249, v120, v121 op_sel:[0,0,1]
	s_nop 1
	global_store_dwordx2 v206, v[246:247], s[100:101]
	global_store_dwordx2 v208, v[248:249], s[100:101]
	s_waitcnt vmcnt(10)
	s_waitcnt lgkmcnt(0)
	s_barrier
	s_waitcnt lgkmcnt(0)
	v_mfma_f32_16x16x128_f8f6f4 v[94:97], v[2:9], v[164:171], v[94:97]
	v_pk_fma_f32 v[138:139], v[138:139], s[18:19], 0 op_sel_hi:[1,0,0]
	v_pk_fma_f32 v[140:141], v[140:141], s[18:19], 0 op_sel_hi:[1,0,0]
	v_pk_fma_f32 v[130:131], v[130:131], s[18:19], 0 op_sel_hi:[1,0,0]
	v_pk_fma_f32 v[132:133], v[132:133], s[18:19], 0 op_sel_hi:[1,0,0]
	v_pk_fma_f32 v[110:111], v[110:111], s[20:21], 0 op_sel_hi:[1,0,0]
	v_pk_fma_f32 v[112:113], v[112:113], s[20:21], 0 op_sel_hi:[1,0,0]
	v_pk_fma_f32 v[106:107], v[106:107], s[20:21], 0 op_sel_hi:[1,0,0]
	v_mfma_f32_16x16x128_f8f6f4 v[90:93], v[10:17], v[164:171], v[90:93]
	v_pk_fma_f32 v[108:109], v[108:109], s[20:21], 0 op_sel_hi:[1,0,0]
	v_pk_fma_f32 v[122:123], v[122:123], s[18:19], 0 op_sel_hi:[1,0,0]
	v_pk_fma_f32 v[124:125], v[124:125], s[18:19], 0 op_sel_hi:[1,0,0]
	v_pk_fma_f32 v[114:115], v[114:115], s[18:19], 0 op_sel_hi:[1,0,0]
	v_pk_fma_f32 v[116:117], v[116:117], s[18:19], 0 op_sel_hi:[1,0,0]
	v_pk_fma_f32 v[102:103], v[102:103], s[20:21], 0 op_sel_hi:[1,0,0]
	v_pk_fma_f32 v[104:105], v[104:105], s[20:21], 0 op_sel_hi:[1,0,0]
	v_mfma_f32_16x16x128_f8f6f4 v[86:89], v[2:9], v[198:205], v[86:89]
	v_pk_fma_f32 v[98:99], v[98:99], s[20:21], 0 op_sel_hi:[1,0,0]
	v_pk_fma_f32 v[100:101], v[100:101], s[20:21], 0 op_sel_hi:[1,0,0]
	v_pk_mul_f32 v[230:231], v[138:139], s[98:99] op_sel_hi:[1,0]
	v_pk_mul_f32 v[232:233], v[140:141], s[98:99] op_sel_hi:[1,0]
	v_pk_mul_f32 v[234:235], v[130:131], s[98:99] op_sel_hi:[1,0]
	v_pk_mul_f32 v[236:237], v[132:133], s[98:99] op_sel_hi:[1,0]
	v_pk_mul_f32 v[238:239], v[122:123], s[98:99] op_sel_hi:[1,0]
	v_mfma_f32_16x16x128_f8f6f4 v[82:85], v[10:17], v[198:205], v[82:85]
	v_pk_mul_f32 v[240:241], v[124:125], s[98:99] op_sel_hi:[1,0]
	v_pk_mul_f32 v[242:243], v[114:115], s[98:99] op_sel_hi:[1,0]
	v_pk_mul_f32 v[244:245], v[116:117], s[98:99] op_sel_hi:[1,0]
	v_exp_f32_e32 v230, v230
	v_exp_f32_e32 v231, v231
	v_exp_f32_e32 v232, v232
	v_exp_f32_e32 v233, v233
	v_mfma_f32_16x16x128_f8f6f4 v[74:77], v[2:9], v[214:221], v[74:77]
	v_exp_f32_e32 v234, v234
	v_exp_f32_e32 v235, v235
	v_exp_f32_e32 v236, v236
	v_exp_f32_e32 v237, v237
	v_exp_f32_e32 v238, v238
	v_exp_f32_e32 v239, v239
	v_exp_f32_e32 v240, v240
	v_mfma_f32_16x16x128_f8f6f4 v[66:69], v[10:17], v[214:221], v[66:69]
	v_exp_f32_e32 v241, v241
	v_exp_f32_e32 v242, v242
	v_exp_f32_e32 v243, v243
	v_exp_f32_e32 v244, v244
	v_exp_f32_e32 v245, v245
	v_pk_add_f32 v[230:231], v[230:231], 1.0 op_sel_hi:[1,0]
	v_pk_add_f32 v[232:233], v[232:233], 1.0 op_sel_hi:[1,0]
	v_mfma_f32_16x16x128_f8f6f4 v[58:61], v[2:9], v[222:229], v[58:61]
	v_pk_add_f32 v[234:235], v[234:235], 1.0 op_sel_hi:[1,0]
	v_pk_add_f32 v[236:237], v[236:237], 1.0 op_sel_hi:[1,0]
	v_pk_add_f32 v[238:239], v[238:239], 1.0 op_sel_hi:[1,0]
	v_pk_add_f32 v[240:241], v[240:241], 1.0 op_sel_hi:[1,0]
	v_pk_add_f32 v[242:243], v[242:243], 1.0 op_sel_hi:[1,0]
	v_pk_add_f32 v[244:245], v[244:245], 1.0 op_sel_hi:[1,0]
	v_rcp_f32_e32 v230, v230
	v_mfma_f32_16x16x128_f8f6f4 v[50:53], v[10:17], v[222:229], v[50:53]
	v_rcp_f32_e32 v231, v231
	v_rcp_f32_e32 v232, v232
	v_rcp_f32_e32 v233, v233
	v_rcp_f32_e32 v234, v234
	v_rcp_f32_e32 v235, v235
	v_rcp_f32_e32 v236, v236
	v_rcp_f32_e32 v237, v237
	v_mfma_f32_16x16x128_f8f6f4 v[78:81], v[18:25], v[164:171], v[78:81]
	v_rcp_f32_e32 v238, v238
	v_rcp_f32_e32 v239, v239
	v_rcp_f32_e32 v240, v240
	v_rcp_f32_e32 v241, v241
	v_rcp_f32_e32 v242, v242
	v_rcp_f32_e32 v243, v243
	v_rcp_f32_e32 v244, v244
	v_mfma_f32_16x16x128_f8f6f4 v[70:73], v[26:33], v[164:171], v[70:73]
	v_rcp_f32_e32 v245, v245
	v_pk_mul_f32 v[230:231], v[138:139], v[230:231]
	v_pk_mul_f32 v[232:233], v[140:141], v[232:233]
	v_pk_mul_f32 v[234:235], v[130:131], v[234:235]
	v_pk_mul_f32 v[236:237], v[132:133], v[236:237]
	v_pk_mul_f32 v[238:239], v[122:123], v[238:239]
	v_pk_mul_f32 v[240:241], v[124:125], v[240:241]
	v_mfma_f32_16x16x128_f8f6f4 v[62:65], v[18:25], v[198:205], v[62:65]
	v_pk_mul_f32 v[242:243], v[114:115], v[242:243]
	v_pk_mul_f32 v[244:245], v[116:117], v[244:245]
	v_pk_mul_f32 v[110:111], v[110:111], v[230:231]
	v_pk_mul_f32 v[112:113], v[112:113], v[232:233]
	v_pk_mul_f32 v[106:107], v[106:107], v[234:235]
	v_pk_mul_f32 v[108:109], v[108:109], v[236:237]
	v_pk_mul_f32 v[102:103], v[102:103], v[238:239]
	v_mfma_f32_16x16x128_f8f6f4 v[54:57], v[26:33], v[198:205], v[54:57]
	v_pk_mul_f32 v[104:105], v[104:105], v[240:241]
	v_pk_mul_f32 v[98:99], v[98:99], v[242:243]
	v_pk_mul_f32 v[100:101], v[100:101], v[244:245]
	v_med3_f32 v110, v110, s72, v197
	v_med3_f32 v111, v111, s72, v197
	v_med3_f32 v112, v112, s72, v197
	v_med3_f32 v113, v113, s72, v197
	v_mfma_f32_16x16x128_f8f6f4 v[46:49], v[18:25], v[214:221], v[46:49]
	v_med3_f32 v106, v106, s72, v197
	v_med3_f32 v107, v107, s72, v197
	v_med3_f32 v108, v108, s72, v197
	v_med3_f32 v109, v109, s72, v197
	v_med3_f32 v102, v102, s72, v197
	v_med3_f32 v103, v103, s72, v197
	v_med3_f32 v104, v104, s72, v197
	v_mfma_f32_16x16x128_f8f6f4 v[42:45], v[26:33], v[214:221], v[42:45]
	v_med3_f32 v105, v105, s72, v197
	v_med3_f32 v98, v98, s72, v197
	v_med3_f32 v99, v99, s72, v197
	v_med3_f32 v100, v100, s72, v197
	v_med3_f32 v101, v101, s72, v197
	v_cvt_pk_fp8_f32 v246, v110, v111
	v_cvt_pk_fp8_f32 v247, v106, v107
	v_mfma_f32_16x16x128_f8f6f4 v[38:41], v[18:25], v[222:229], v[38:41]
	v_cvt_pk_fp8_f32 v248, v102, v103
	v_cvt_pk_fp8_f32 v249, v98, v99
	v_add_u32_e32 v207, s73, v206
	v_add_u32_e32 v208, s74, v206
	v_cvt_pk_fp8_f32 v246, v112, v113 op_sel:[0,0,1]
	v_cvt_pk_fp8_f32 v247, v108, v109 op_sel:[0,0,1]
	v_cvt_pk_fp8_f32 v248, v104, v105 op_sel:[0,0,1]
	v_mfma_f32_16x16x128_f8f6f4 v[34:37], v[26:33], v[222:229], v[34:37]
	v_cvt_pk_fp8_f32 v249, v100, v101 op_sel:[0,0,1]
	s_nop 1
	global_store_dwordx2 v207, v[246:247], s[100:101]
	global_store_dwordx2 v208, v[248:249], s[100:101]
	s_barrier
	s_and_b64 vcc, exec, s[16:17]
	s_cbranch_vccz .Lh23_nb
	s_barrier

.LBB0_2945:
	s_setprio 0
	s_cmp_lt_i32 s41, 25
	s_cbranch_scc1 .LBB0_2995
	s_waitcnt vmcnt(0)
	v_cmp_eq_u32_e32 vcc, 0, v0
	s_waitcnt vmcnt(0) lgkmcnt(0)
	s_barrier
	s_and_saveexec_b64 s[2:3], vcc
	s_cbranch_execz .LBB0_2994
	v_mov_b32_e32 v1, s92
	s_waitcnt vmcnt(0) expcnt(0) lgkmcnt(0)
	ds_read_b32 v3, v1
	ds_read_b32 v1, v1 offset:4
	s_waitcnt lgkmcnt(1)
	v_cmp_ne_u32_e32 vcc, 0, v3
	s_cbranch_vccnz .LBB0_2962
	v_readlane_b32 s4, v254, 1
	v_readlane_b32 s5, v254, 2
	s_load_dwordx2 s[8:9], s[4:5], 0x4
	s_add_u32 s4, s42, 0x1000
	s_addc_u32 s5, s43, 0
	s_add_u32 s6, s42, 0x1100
	s_addc_u32 s7, s43, 0
	s_waitcnt lgkmcnt(0)
	s_mul_i32 s18, s8, s34
	s_add_u32 s8, s42, 0x1200
	s_mul_i32 s18, s18, s9
	s_addc_u32 s9, s43, 0
	s_add_u32 s10, s42, 0x1300
	s_addc_u32 s11, s43, 0
	s_mov_b32 s19, 1
	v_mov_b32_e32 v17, 0
	s_branch .LBB0_2950

.LBB0_2995:
.LBB0_2996:
	s_cmp_gt_i32 s40, 24
	s_cselect_b64 s[2:3], -1, 0
	s_cmp_lt_i32 s41, 25
	s_cselect_b64 s[4:5], -1, 0
	s_or_b64 s[2:3], s[2:3], s[4:5]
	s_and_b64 vcc, exec, s[2:3]
	s_cbranch_vccnz .LBB0_3066
	s_cmp_ge_u32 s27, 4
	s_cbranch_scc0 .Lsp_24
	s_setprio 1
.Lsp_24:
	v_mov_b32_e32 v1, 0x6c2000
	global_load_dword v1, v1, s[38:39] offset:2048
	v_mov_b32_e32 v2, v0
	s_movk_i32 s3, 0xb00
	s_movk_i32 s66, 0xb00
	s_movk_i32 s14, 0xb00
	s_waitcnt vmcnt(0)
	v_lshlrev_b32_e32 v162, 3, v1
	v_cmp_ge_i32_e32 vcc, s26, v162
	v_readfirstlane_b32 s2, v2
	v_readfirstlane_b32 s17, v1
	s_cbranch_vccnz .LBB0_3015
	s_add_u32 s4, s38, 0x4b400000
	s_addc_u32 s5, s39, 0
	s_add_u32 s6, s38, 0x1df00000
	s_addc_u32 s7, s39, 0
	s_add_u32 s22, s38, 0x6c2000
	s_addc_u32 s23, s39, 0
	s_ashr_i32 s28, s26, 31
	s_lshr_b32 s8, s28, 29
	s_add_i32 s8, s26, s8
	s_waitcnt lgkmcnt(0)
	s_ashr_i32 s12, s2, 6
	s_ashr_i32 s9, s8, 3
	s_and_b32 s8, s8, -8
	s_ashr_i32 s13, s2, 8
	s_lshl_b32 s24, s66, 7
	s_lshl_b32 s25, s14, 7
	s_lshl_b32 s15, s12, 10
	s_sub_i32 s8, s26, s8
	s_add_i32 s29, s17, 1
	s_cmp_lt_i32 s8, 0
	s_cselect_b32 s10, s29, s17
	s_mul_i32 s8, s10, s8
	s_add_i32 s8, s8, s9
	s_ashr_i32 s9, s8, 31
	s_lshr_b32 s9, s9, 26
	s_add_i32 s9, s8, s9
	s_ashr_i32 s10, s9, 6
	s_lshl_b32 s10, s10, 3
	s_sub_i32 s11, s17, s10
	s_min_i32 s11, s11, 8
	s_abs_i32 s16, s11
	v_cvt_f32_u32_e32 v1, s16
	s_sub_i32 s19, 0, s16
	s_andn2_b32 s9, s9, 63
	s_sub_i32 s8, s8, s9
	v_rcp_iflag_f32_e32 v1, v1
	s_abs_i32 s18, s8
	s_xor_b32 s9, s8, s11
	s_ashr_i32 s9, s9, 31
	v_mul_f32_e32 v1, 0x4f7ffffe, v1
	v_cvt_u32_f32_e32 v1, v1
	v_bfe_i32 v6, v2, 27, 1
	v_lshlrev_b32_e32 v4, 4, v2
	v_lshrrev_b32_e32 v6, 22, v6
	v_readfirstlane_b32 s20, v1
	s_mul_i32 s19, s19, s20
	s_mul_hi_u32 s19, s20, s19
	s_add_i32 s20, s20, s19
	s_mul_hi_u32 s19, s18, s20
	s_mul_i32 s20, s19, s16
	s_sub_i32 s18, s18, s20
	s_add_i32 s20, s19, 1
	s_sub_i32 s21, s18, s16
	s_cmp_ge_u32 s18, s16
	s_cselect_b32 s19, s20, s19
	s_cselect_b32 s18, s21, s18
	s_add_i32 s20, s19, 1
	s_cmp_ge_u32 s18, s16
	s_cselect_b32 s16, s20, s19
	s_xor_b32 s16, s16, s9
	s_sub_i32 s56, s16, s9
	s_mul_i32 s9, s56, s11
	s_sub_i32 s8, s8, s9
	s_add_i32 s10, s10, s8
	s_ashr_i32 s11, s10, 31
	s_lshl_b64 s[8:9], s[10:11], 2
	s_add_u32 s8, s22, s8
	s_addc_u32 s9, s23, s9
	v_mov_b32_e32 v1, 0
	global_load_dword v3, v1, s[8:9]
	v_add_u32_e32 v6, v4, v6
	v_and_b32_e32 v6, 0xfffffc00, v6
	v_sub_u32_e32 v4, v4, v6
	v_ashrrev_i32_e32 v5, 31, v2
	v_lshrrev_b32_e32 v8, 4, v4
	v_lshrrev_b32_e32 v5, 26, v5
	v_bitop3_b32 v4, v8, v4, 32 bitop3:0x6c
	v_add_u32_e32 v5, v2, v5
	v_ashrrev_i32_e32 v8, 31, v4
	v_ashrrev_i32_e32 v5, 6, v5
	v_lshrrev_b32_e32 v8, 26, v8
	v_lshlrev_b32_e32 v6, 3, v5
	v_add_u32_e32 v8, v4, v8
	v_and_b32_e32 v6, -16, v6
	v_ashrrev_i32_e32 v9, 6, v8
	v_and_b32_e32 v8, 0xc0, v8
	v_mov_b32_e32 v7, 1
	v_lshlrev_b32_e32 v5, 5, v5
	v_add_u32_e32 v6, v9, v6
	v_sub_u32_e32 v4, v4, v8
	s_mov_b32 s8, 0x7fffffe0
	v_and_b32_e32 v5, 32, v5
	v_and_b32_e32 v8, 3, v9
	v_ashrrev_i16_sdwa v4, v7, sext(v4) dst_sel:DWORD dst_unused:UNUSED_PAD src0_sel:DWORD src1_sel:BYTE_0
	v_lshlrev_b32_e32 v7, 1, v6
	v_lshrrev_b32_e32 v9, 2, v6
	v_and_or_b32 v8, v6, s8, v8
	v_add_u32_sdwa v4, v5, sext(v4) dst_sel:DWORD dst_unused:UNUSED_PAD src0_sel:DWORD src1_sel:WORD_0
	v_and_b32_e32 v5, 24, v7
	v_and_b32_e32 v7, 4, v9
	v_or3_b32 v5, v8, v7, v5
	v_mul_lo_u32 v5, v5, s14
	v_mul_lo_u32 v6, v6, s66
	v_add_lshl_u32 v165, v5, v4, 1
	s_add_i32 s30, s15, 0
	v_add_lshl_u32 v164, v4, v6, 1
	v_mov_b32_e32 v4, v165
	s_add_i32 s31, s30, 0x10000
	v_mov_b32_e32 v5, v165
	s_add_i32 s35, s30, 0x12000
	s_mov_b32 m0, s31
	v_mov_b32_e32 v8, v165
	s_add_i32 s44, s30, 0x14000
	v_mov_b32_e32 v9, v165
	s_add_i32 s45, s30, 0x16000
	v_mov_b32_e32 v6, v164
	s_mul_i32 s74, s10, 0x160000
	v_mov_b32_e32 v7, v164
	s_add_i32 s8, s74, s24
	s_add_i32 s46, s30, 0x2000
	s_add_i32 s47, s30, 0x4000
	s_add_i32 s48, s30, 0x6000
	s_mov_b32 s49, 0
	s_mov_b32 s50, 0x10000
	s_waitcnt vmcnt(0)
	v_readfirstlane_b32 s9, v3
	s_lshl_b32 s9, s9, 3
	s_add_i32 s9, s9, s56
	s_mul_i32 s75, s9, 0x160000
	v_add_u32_e32 v3, s75, v4
	s_add_i32 s9, s75, s25
	global_load_lds_dwordx4 v3, s[6:7]
	s_add_i32 s11, s9, s25
	v_add_u32_e32 v3, s9, v5
	s_mov_b32 m0, s35
	s_add_i32 s9, s11, s25
	global_load_lds_dwordx4 v3, s[6:7]
	s_mov_b32 m0, s44
	v_add_u32_e32 v3, s11, v8
	global_load_lds_dwordx4 v3, s[6:7]
	s_mov_b32 m0, s45
	v_add_u32_e32 v3, s9, v9
	global_load_lds_dwordx4 v3, s[6:7]
	s_mov_b32 m0, s30
	v_add_u32_e32 v3, s74, v6
	global_load_lds_dwordx4 v3, s[4:5]
	s_mov_b32 m0, s46
	v_add_u32_e32 v3, s8, v7
	global_load_lds_dwordx4 v3, s[4:5]
	v_mov_b32_e32 v3, v164
	s_add_i32 s8, s8, s24
	s_mov_b32 m0, s47
	v_add_u32_e32 v3, s8, v3
	global_load_lds_dwordx4 v3, s[4:5]
	v_mov_b32_e32 v3, v164
	s_add_i32 s8, s8, s24
	v_add_u32_e32 v3, s8, v3
	s_mov_b32 m0, s48
	s_cmp_eq_u32 s13, 1
	global_load_lds_dwordx4 v3, s[4:5]
	s_cselect_b64 s[8:9], -1, 0
	s_cmp_lg_u32 s13, 1
	s_cbranch_scc1 .LBB0_3000
	s_barrier

.LBB0_3005:
	s_andn2_b64 vcc, exec, s[12:13]
	v_mov_b64_e32 v[2:3], 0
	v_mov_b64_e32 v[4:5], 0
	v_mov_b64_e32 v[6:7], 0
	v_mov_b64_e32 v[8:9], 0
	v_mov_b64_e32 v[10:11], 0
	v_mov_b64_e32 v[12:13], 0
	v_mov_b64_e32 v[14:15], 0
	v_mov_b64_e32 v[16:17], 0
	v_mov_b64_e32 v[18:19], 0
	v_mov_b64_e32 v[20:21], 0
	v_mov_b64_e32 v[22:23], 0
	v_mov_b64_e32 v[24:25], 0
	v_mov_b64_e32 v[26:27], 0
	v_mov_b64_e32 v[28:29], 0
	v_mov_b64_e32 v[30:31], 0
	v_mov_b64_e32 v[32:33], 0
	s_cbranch_vccnz .Lzs_13
	s_add_i32 s20, s74, 0x80
	s_add_i32 s74, s75, 0x100
	s_mov_b32 s75, 0
	ds_read_b128 v[18:21], v168
	ds_read_b128 v[22:25], v169
	ds_read_b128 v[26:29], v176
	ds_read_b128 v[30:33], v177
	ds_read_b128 v[2:5], v170
	ds_read_b128 v[6:9], v171
	ds_read_b128 v[10:13], v178
	ds_read_b128 v[14:17], v179
	s_add_i32 s76, s20, 0x80
	s_cmp_eq_u32 s61, s75
	s_cselect_b32 s78, s11, s76
	s_cselect_b32 s77, s21, s74
	s_add_i32 s76, s78, 0x80
	v_mov_b32_e32 v185, v164
	ds_read_b128 v[186:189], v184
	ds_read_b128 v[190:193], v184 offset:1024
	ds_read_b128 v[194:197], v184 offset:2048
	ds_read_b128 v[198:201], v184 offset:3072
	ds_read_b128 v[202:205], v184 offset:4096
	ds_read_b128 v[206:209], v184 offset:5120
	ds_read_b128 v[214:217], v184 offset:6144
	ds_read_b128 v[218:221], v184 offset:7168
	s_add_i32 s79, s20, s59
	v_add_u32_e32 v185, s79, v185
	s_add_i32 m0, s30, 0xc000
	s_add_i32 s79, s20, s66
	global_load_lds_dwordx4 v185, s[4:5]
	v_mov_b32_e32 v185, v164
	s_add_i32 m0, s30, 0xe000
	v_add_u32_e32 v185, s79, v185
	global_load_lds_dwordx4 v185, s[4:5]
	s_waitcnt vmcnt(8)
	s_waitcnt lgkmcnt(0)
	s_barrier
	s_waitcnt lgkmcnt(0)
	v_mfma_f32_16x16x128_f8f6f4 v[158:161], v[18:25], v[186:193], 0
	v_mfma_f32_16x16x128_f8f6f4 v[154:157], v[26:33], v[186:193], 0
	v_mfma_f32_16x16x128_f8f6f4 v[150:153], v[18:25], v[194:201], 0
	v_mfma_f32_16x16x128_f8f6f4 v[146:149], v[26:33], v[194:201], 0
	v_mfma_f32_16x16x128_f8f6f4 v[138:141], v[18:25], v[202:209], 0
	v_mfma_f32_16x16x128_f8f6f4 v[130:133], v[26:33], v[202:209], 0
	v_mfma_f32_16x16x128_f8f6f4 v[122:125], v[18:25], v[214:221], 0
	v_mfma_f32_16x16x128_f8f6f4 v[114:117], v[26:33], v[214:221], 0
	v_mfma_f32_16x16x128_f8f6f4 v[142:145], v[2:9], v[186:193], 0
	v_mfma_f32_16x16x128_f8f6f4 v[134:137], v[10:17], v[186:193], 0
	v_mfma_f32_16x16x128_f8f6f4 v[126:129], v[2:9], v[194:201], 0
	v_mfma_f32_16x16x128_f8f6f4 v[118:121], v[10:17], v[194:201], 0
	v_mfma_f32_16x16x128_f8f6f4 v[110:113], v[2:9], v[202:209], 0
	v_mfma_f32_16x16x128_f8f6f4 v[106:109], v[10:17], v[202:209], 0
	v_mfma_f32_16x16x128_f8f6f4 v[102:105], v[2:9], v[214:221], 0
	v_mfma_f32_16x16x128_f8f6f4 v[98:101], v[10:17], v[214:221], 0
	s_barrier
	v_mov_b32_e32 v185, v165
	ds_read_b128 v[186:189], v184 offset:16384
	ds_read_b128 v[190:193], v184 offset:17408
	ds_read_b128 v[194:197], v184 offset:18432
	ds_read_b128 v[198:201], v184 offset:19456
	ds_read_b128 v[202:205], v184 offset:20480
	ds_read_b128 v[206:209], v184 offset:21504
	ds_read_b128 v[214:217], v184 offset:22528
	ds_read_b128 v[218:221], v184 offset:23552
	s_mov_b32 m0, s31
	v_add_u32_e32 v185, s77, v185
	global_load_lds_dwordx4 v185, s[6:7]
	v_mov_b32_e32 v185, v165
	s_add_i32 s79, s77, s25
	v_add_u32_e32 v185, s79, v185
	s_mov_b32 m0, s35
	s_add_i32 s79, s79, s25
	global_load_lds_dwordx4 v185, s[6:7]
	v_mov_b32_e32 v185, v165
	s_mov_b32 m0, s44
	v_add_u32_e32 v185, s79, v185
	global_load_lds_dwordx4 v185, s[6:7]
	v_mov_b32_e32 v185, v165
	s_add_i32 s79, s79, s25
	v_add_u32_e32 v185, s79, v185
	s_mov_b32 m0, s45
	s_nop 0
	global_load_lds_dwordx4 v185, s[6:7]
	v_mov_b32_e32 v185, v164
	s_mov_b32 m0, s30
	v_add_u32_e32 v185, s78, v185
	global_load_lds_dwordx4 v185, s[4:5]
	v_mov_b32_e32 v185, v164
	s_add_i32 s78, s78, s24
	v_add_u32_e32 v185, s78, v185
	s_mov_b32 m0, s46
	s_nop 0
	global_load_lds_dwordx4 v185, s[4:5]
	s_waitcnt vmcnt(8)
	s_waitcnt lgkmcnt(0)
	s_barrier
	s_waitcnt lgkmcnt(0)
	v_mfma_f32_16x16x128_f8f6f4 v[94:97], v[18:25], v[186:193], 0
	v_mfma_f32_16x16x128_f8f6f4 v[90:93], v[26:33], v[186:193], 0
	v_mfma_f32_16x16x128_f8f6f4 v[86:89], v[18:25], v[194:201], 0
	v_mfma_f32_16x16x128_f8f6f4 v[82:85], v[26:33], v[194:201], 0
	v_mfma_f32_16x16x128_f8f6f4 v[74:77], v[18:25], v[202:209], 0
	v_mfma_f32_16x16x128_f8f6f4 v[66:69], v[26:33], v[202:209], 0
	v_mfma_f32_16x16x128_f8f6f4 v[58:61], v[18:25], v[214:221], 0
	v_mfma_f32_16x16x128_f8f6f4 v[50:53], v[26:33], v[214:221], 0
	v_mfma_f32_16x16x128_f8f6f4 v[78:81], v[2:9], v[186:193], 0
	v_mfma_f32_16x16x128_f8f6f4 v[70:73], v[10:17], v[186:193], 0
	v_mfma_f32_16x16x128_f8f6f4 v[62:65], v[2:9], v[194:201], 0
	v_mfma_f32_16x16x128_f8f6f4 v[54:57], v[10:17], v[194:201], 0
	v_mfma_f32_16x16x128_f8f6f4 v[46:49], v[2:9], v[202:209], 0
	v_mfma_f32_16x16x128_f8f6f4 v[42:45], v[10:17], v[202:209], 0
	v_mfma_f32_16x16x128_f8f6f4 v[38:41], v[2:9], v[214:221], 0
	v_mfma_f32_16x16x128_f8f6f4 v[34:37], v[10:17], v[214:221], 0
	s_barrier
	s_branch .Lmid_11
.LBB0_3007:
	ds_read_b128 v[18:21], v168
	ds_read_b128 v[22:25], v169
	ds_read_b128 v[26:29], v176
	ds_read_b128 v[30:33], v177
	ds_read_b128 v[2:5], v170
	ds_read_b128 v[6:9], v171
	ds_read_b128 v[10:13], v178
	ds_read_b128 v[14:17], v179
	s_add_i32 s76, s20, 0x80
	s_cmp_eq_u32 s61, s75
	s_cselect_b32 s78, s11, s76
	s_cselect_b32 s77, s21, s74
	s_add_i32 s76, s78, 0x80
	v_mov_b32_e32 v185, v164
	ds_read_b128 v[186:189], v184
	ds_read_b128 v[190:193], v184 offset:1024
	ds_read_b128 v[194:197], v184 offset:2048
	ds_read_b128 v[198:201], v184 offset:3072
	ds_read_b128 v[202:205], v184 offset:4096
	ds_read_b128 v[206:209], v184 offset:5120
	ds_read_b128 v[214:217], v184 offset:6144
	ds_read_b128 v[218:221], v184 offset:7168
	s_add_i32 s79, s20, s59
	v_add_u32_e32 v185, s79, v185
	s_add_i32 m0, s30, 0xc000
	s_add_i32 s79, s20, s66
	global_load_lds_dwordx4 v185, s[4:5]
	v_mov_b32_e32 v185, v164
	s_add_i32 m0, s30, 0xe000
	v_add_u32_e32 v185, s79, v185
	global_load_lds_dwordx4 v185, s[4:5]
	s_waitcnt vmcnt(8)
	s_waitcnt lgkmcnt(0)
	s_barrier
	s_waitcnt lgkmcnt(0)
	v_mfma_f32_16x16x128_f8f6f4 v[158:161], v[18:25], v[186:193], v[158:161]
	v_mfma_f32_16x16x128_f8f6f4 v[154:157], v[26:33], v[186:193], v[154:157]
	v_mfma_f32_16x16x128_f8f6f4 v[150:153], v[18:25], v[194:201], v[150:153]
	v_mfma_f32_16x16x128_f8f6f4 v[146:149], v[26:33], v[194:201], v[146:149]
	v_mfma_f32_16x16x128_f8f6f4 v[138:141], v[18:25], v[202:209], v[138:141]
	v_mfma_f32_16x16x128_f8f6f4 v[130:133], v[26:33], v[202:209], v[130:133]
	v_mfma_f32_16x16x128_f8f6f4 v[122:125], v[18:25], v[214:221], v[122:125]
	v_mfma_f32_16x16x128_f8f6f4 v[114:117], v[26:33], v[214:221], v[114:117]
	v_mfma_f32_16x16x128_f8f6f4 v[142:145], v[2:9], v[186:193], v[142:145]
	v_mfma_f32_16x16x128_f8f6f4 v[134:137], v[10:17], v[186:193], v[134:137]
	v_mfma_f32_16x16x128_f8f6f4 v[126:129], v[2:9], v[194:201], v[126:129]
	v_mfma_f32_16x16x128_f8f6f4 v[118:121], v[10:17], v[194:201], v[118:121]
	v_mfma_f32_16x16x128_f8f6f4 v[110:113], v[2:9], v[202:209], v[110:113]
	v_mfma_f32_16x16x128_f8f6f4 v[106:109], v[10:17], v[202:209], v[106:109]
	v_mfma_f32_16x16x128_f8f6f4 v[102:105], v[2:9], v[214:221], v[102:105]
	v_mfma_f32_16x16x128_f8f6f4 v[98:101], v[10:17], v[214:221], v[98:101]
	s_barrier
	v_mov_b32_e32 v185, v165
	ds_read_b128 v[186:189], v184 offset:16384
	ds_read_b128 v[190:193], v184 offset:17408
	ds_read_b128 v[194:197], v184 offset:18432
	ds_read_b128 v[198:201], v184 offset:19456
	ds_read_b128 v[202:205], v184 offset:20480
	ds_read_b128 v[206:209], v184 offset:21504
	ds_read_b128 v[214:217], v184 offset:22528
	ds_read_b128 v[218:221], v184 offset:23552
	s_mov_b32 m0, s31
	v_add_u32_e32 v185, s77, v185
	global_load_lds_dwordx4 v185, s[6:7]
	v_mov_b32_e32 v185, v165
	s_add_i32 s79, s77, s25
	v_add_u32_e32 v185, s79, v185
	s_mov_b32 m0, s35
	s_add_i32 s79, s79, s25
	global_load_lds_dwordx4 v185, s[6:7]
	v_mov_b32_e32 v185, v165
	s_mov_b32 m0, s44
	v_add_u32_e32 v185, s79, v185
	global_load_lds_dwordx4 v185, s[6:7]
	v_mov_b32_e32 v185, v165
	s_add_i32 s79, s79, s25
	v_add_u32_e32 v185, s79, v185
	s_mov_b32 m0, s45
	s_nop 0
	global_load_lds_dwordx4 v185, s[6:7]
	v_mov_b32_e32 v185, v164
	s_mov_b32 m0, s30
	v_add_u32_e32 v185, s78, v185
	global_load_lds_dwordx4 v185, s[4:5]
	v_mov_b32_e32 v185, v164
	s_add_i32 s78, s78, s24
	v_add_u32_e32 v185, s78, v185
	s_mov_b32 m0, s46
	s_nop 0
	global_load_lds_dwordx4 v185, s[4:5]
	s_waitcnt vmcnt(8)
	s_waitcnt lgkmcnt(0)
	s_barrier
	s_waitcnt lgkmcnt(0)
	v_mfma_f32_16x16x128_f8f6f4 v[94:97], v[18:25], v[186:193], v[94:97]
	v_mfma_f32_16x16x128_f8f6f4 v[90:93], v[26:33], v[186:193], v[90:93]
	v_mfma_f32_16x16x128_f8f6f4 v[86:89], v[18:25], v[194:201], v[86:89]
	v_mfma_f32_16x16x128_f8f6f4 v[82:85], v[26:33], v[194:201], v[82:85]
	v_mfma_f32_16x16x128_f8f6f4 v[74:77], v[18:25], v[202:209], v[74:77]
	v_mfma_f32_16x16x128_f8f6f4 v[66:69], v[26:33], v[202:209], v[66:69]
	v_mfma_f32_16x16x128_f8f6f4 v[58:61], v[18:25], v[214:221], v[58:61]
	v_mfma_f32_16x16x128_f8f6f4 v[50:53], v[26:33], v[214:221], v[50:53]
	v_mfma_f32_16x16x128_f8f6f4 v[78:81], v[2:9], v[186:193], v[78:81]
	v_mfma_f32_16x16x128_f8f6f4 v[70:73], v[10:17], v[186:193], v[70:73]
	v_mfma_f32_16x16x128_f8f6f4 v[62:65], v[2:9], v[194:201], v[62:65]
	v_mfma_f32_16x16x128_f8f6f4 v[54:57], v[10:17], v[194:201], v[54:57]
	v_mfma_f32_16x16x128_f8f6f4 v[46:49], v[2:9], v[202:209], v[46:49]
	v_mfma_f32_16x16x128_f8f6f4 v[42:45], v[10:17], v[202:209], v[42:45]
	v_mfma_f32_16x16x128_f8f6f4 v[38:41], v[2:9], v[214:221], v[38:41]
	v_mfma_f32_16x16x128_f8f6f4 v[34:37], v[10:17], v[214:221], v[34:37]
	s_barrier

.Ltx24_skip:
	ds_read_b128 v[2:5], v172
	ds_read_b128 v[6:9], v173
	ds_read_b128 v[10:13], v180
	ds_read_b128 v[14:17], v181
	ds_read_b128 v[18:21], v174
	ds_read_b128 v[22:25], v175
	ds_read_b128 v[26:29], v182
	ds_read_b128 v[30:33], v183
	v_mov_b32_e32 v185, v164
	ds_read_b128 v[186:189], v184 offset:32768
	ds_read_b128 v[190:193], v184 offset:33792
	ds_read_b128 v[194:197], v184 offset:34816
	ds_read_b128 v[198:201], v184 offset:35840
	ds_read_b128 v[202:205], v184 offset:36864
	ds_read_b128 v[206:209], v184 offset:37888
	ds_read_b128 v[214:217], v184 offset:38912
	ds_read_b128 v[218:221], v184 offset:39936
	s_add_i32 s78, s78, s24
	s_mov_b32 m0, s47
	v_add_u32_e32 v185, s78, v185
	global_load_lds_dwordx4 v185, s[4:5]
	v_mov_b32_e32 v185, v164
	s_add_i32 s78, s78, s24
	v_add_u32_e32 v185, s78, v185
	s_mov_b32 m0, s48
	s_nop 0
	global_load_lds_dwordx4 v185, s[4:5]
	s_waitcnt vmcnt(8)
	s_waitcnt lgkmcnt(0)
	s_barrier
	s_waitcnt lgkmcnt(0)
	v_mfma_f32_16x16x128_f8f6f4 v[158:161], v[2:9], v[186:193], v[158:161]
	v_mfma_f32_16x16x128_f8f6f4 v[154:157], v[10:17], v[186:193], v[154:157]
	v_mfma_f32_16x16x128_f8f6f4 v[150:153], v[2:9], v[194:201], v[150:153]
	v_mfma_f32_16x16x128_f8f6f4 v[146:149], v[10:17], v[194:201], v[146:149]
	v_mfma_f32_16x16x128_f8f6f4 v[138:141], v[2:9], v[202:209], v[138:141]
	v_mfma_f32_16x16x128_f8f6f4 v[130:133], v[10:17], v[202:209], v[130:133]
	v_mfma_f32_16x16x128_f8f6f4 v[122:125], v[2:9], v[214:221], v[122:125]
	v_mfma_f32_16x16x128_f8f6f4 v[114:117], v[10:17], v[214:221], v[114:117]
	v_mfma_f32_16x16x128_f8f6f4 v[142:145], v[18:25], v[186:193], v[142:145]
	v_mfma_f32_16x16x128_f8f6f4 v[134:137], v[26:33], v[186:193], v[134:137]
	v_mfma_f32_16x16x128_f8f6f4 v[126:129], v[18:25], v[194:201], v[126:129]
	v_mfma_f32_16x16x128_f8f6f4 v[118:121], v[26:33], v[194:201], v[118:121]
	v_mfma_f32_16x16x128_f8f6f4 v[110:113], v[18:25], v[202:209], v[110:113]
	v_mfma_f32_16x16x128_f8f6f4 v[106:109], v[26:33], v[202:209], v[106:109]
	v_mfma_f32_16x16x128_f8f6f4 v[102:105], v[18:25], v[214:221], v[102:105]
	v_mfma_f32_16x16x128_f8f6f4 v[98:101], v[26:33], v[214:221], v[98:101]
	s_barrier
	v_mov_b32_e32 v185, v165
	ds_read_b128 v[186:189], v184 offset:49152
	ds_read_b128 v[190:193], v184 offset:50176
	ds_read_b128 v[194:197], v184 offset:51200
	ds_read_b128 v[198:201], v184 offset:52224
	ds_read_b128 v[202:205], v184 offset:53248
	ds_read_b128 v[206:209], v184 offset:54272
	ds_read_b128 v[214:217], v184 offset:55296
	ds_read_b128 v[218:221], v184 offset:56320
	s_addk_i32 s77, 0x80
	s_mov_b32 m0, s51
	v_add_u32_e32 v185, s77, v185
	global_load_lds_dwordx4 v185, s[6:7]
	v_mov_b32_e32 v185, v165
	s_add_i32 s77, s77, s25
	v_add_u32_e32 v185, s77, v185
	s_mov_b32 m0, s52
	s_add_i32 s77, s77, s25
	global_load_lds_dwordx4 v185, s[6:7]
	v_mov_b32_e32 v185, v165
	s_mov_b32 m0, s55
	v_add_u32_e32 v185, s77, v185
	global_load_lds_dwordx4 v185, s[6:7]
	v_mov_b32_e32 v185, v165
	s_add_i32 s77, s77, s25
	v_add_u32_e32 v185, s77, v185
	s_mov_b32 m0, s57
	s_nop 0
	global_load_lds_dwordx4 v185, s[6:7]
	v_mov_b32_e32 v185, v164
	s_mov_b32 m0, s53
	v_add_u32_e32 v185, s76, v185
	global_load_lds_dwordx4 v185, s[4:5]
	v_mov_b32_e32 v185, v164
	s_add_i32 s76, s76, s24
	v_add_u32_e32 v185, s76, v185
	s_mov_b32 m0, s54
	s_nop 0
	global_load_lds_dwordx4 v185, s[4:5]
	s_waitcnt vmcnt(8)
	s_waitcnt lgkmcnt(0)
	s_barrier
	s_waitcnt lgkmcnt(0)
	v_mfma_f32_16x16x128_f8f6f4 v[94:97], v[2:9], v[186:193], v[94:97]
	v_mfma_f32_16x16x128_f8f6f4 v[90:93], v[10:17], v[186:193], v[90:93]
	v_mfma_f32_16x16x128_f8f6f4 v[86:89], v[2:9], v[194:201], v[86:89]
	v_mfma_f32_16x16x128_f8f6f4 v[82:85], v[10:17], v[194:201], v[82:85]
	v_mfma_f32_16x16x128_f8f6f4 v[74:77], v[2:9], v[202:209], v[74:77]
	v_mfma_f32_16x16x128_f8f6f4 v[66:69], v[10:17], v[202:209], v[66:69]
	v_mfma_f32_16x16x128_f8f6f4 v[58:61], v[2:9], v[214:221], v[58:61]
	v_mfma_f32_16x16x128_f8f6f4 v[50:53], v[10:17], v[214:221], v[50:53]
	v_mfma_f32_16x16x128_f8f6f4 v[78:81], v[18:25], v[186:193], v[78:81]
	v_mfma_f32_16x16x128_f8f6f4 v[70:73], v[26:33], v[186:193], v[70:73]
	v_mfma_f32_16x16x128_f8f6f4 v[62:65], v[18:25], v[194:201], v[62:65]
	v_mfma_f32_16x16x128_f8f6f4 v[54:57], v[26:33], v[194:201], v[54:57]
	v_mfma_f32_16x16x128_f8f6f4 v[46:49], v[18:25], v[202:209], v[46:49]
	v_mfma_f32_16x16x128_f8f6f4 v[42:45], v[26:33], v[202:209], v[42:45]
	v_mfma_f32_16x16x128_f8f6f4 v[38:41], v[18:25], v[214:221], v[38:41]
	v_mfma_f32_16x16x128_f8f6f4 v[34:37], v[26:33], v[214:221], v[34:37]
	s_barrier
	s_add_i32 s75, s75, 2
	s_addk_i32 s20, 0x100
	s_addk_i32 s74, 0x100
	s_cmp_ge_i32 s75, s58
	s_cbranch_scc0 .LBB0_3007
	v_pk_mul_f32 v[2:3], v[160:161], s[16:17] op_sel_hi:[1,0]
	v_pk_mul_f32 v[4:5], v[158:159], s[16:17] op_sel_hi:[1,0]
	v_pk_mul_f32 v[6:7], v[156:157], s[16:17] op_sel_hi:[1,0]
	v_pk_mul_f32 v[12:13], v[154:155], s[16:17] op_sel_hi:[1,0]
	v_pk_mul_f32 v[144:145], v[144:145], s[16:17] op_sel_hi:[1,0]
	v_pk_mul_f32 v[142:143], v[142:143], s[16:17] op_sel_hi:[1,0]
	v_pk_mul_f32 v[136:137], v[136:137], s[16:17] op_sel_hi:[1,0]
	v_pk_mul_f32 v[134:135], v[134:135], s[16:17] op_sel_hi:[1,0]
	v_pk_mul_f32 v[8:9], v[152:153], s[16:17] op_sel_hi:[1,0]
	v_pk_mul_f32 v[14:15], v[150:151], s[16:17] op_sel_hi:[1,0]
	v_pk_mul_f32 v[18:19], v[148:149], s[16:17] op_sel_hi:[1,0]
	v_pk_mul_f32 v[26:27], v[146:147], s[16:17] op_sel_hi:[1,0]
	v_pk_mul_f32 v[128:129], v[128:129], s[16:17] op_sel_hi:[1,0]
	v_pk_mul_f32 v[126:127], v[126:127], s[16:17] op_sel_hi:[1,0]
	v_pk_mul_f32 v[120:121], v[120:121], s[16:17] op_sel_hi:[1,0]
	v_pk_mul_f32 v[118:119], v[118:119], s[16:17] op_sel_hi:[1,0]
	v_pk_mul_f32 v[10:11], v[140:141], s[16:17] op_sel_hi:[1,0]
	v_pk_mul_f32 v[20:21], v[138:139], s[16:17] op_sel_hi:[1,0]
	v_pk_mul_f32 v[22:23], v[132:133], s[16:17] op_sel_hi:[1,0]
	v_pk_mul_f32 v[30:31], v[130:131], s[16:17] op_sel_hi:[1,0]
	v_pk_mul_f32 v[112:113], v[112:113], s[16:17] op_sel_hi:[1,0]
	v_pk_mul_f32 v[110:111], v[110:111], s[16:17] op_sel_hi:[1,0]
	v_pk_mul_f32 v[108:109], v[108:109], s[16:17] op_sel_hi:[1,0]
	v_pk_mul_f32 v[106:107], v[106:107], s[16:17] op_sel_hi:[1,0]
	v_pk_mul_f32 v[16:17], v[124:125], s[16:17] op_sel_hi:[1,0]
	v_pk_mul_f32 v[24:25], v[122:123], s[16:17] op_sel_hi:[1,0]
	v_pk_mul_f32 v[28:29], v[116:117], s[16:17] op_sel_hi:[1,0]
	v_pk_mul_f32 v[32:33], v[114:115], s[16:17] op_sel_hi:[1,0]
	v_pk_mul_f32 v[104:105], v[104:105], s[16:17] op_sel_hi:[1,0]
	v_pk_mul_f32 v[102:103], v[102:103], s[16:17] op_sel_hi:[1,0]
	v_pk_mul_f32 v[100:101], v[100:101], s[16:17] op_sel_hi:[1,0]
	v_pk_mul_f32 v[98:99], v[98:99], s[16:17] op_sel_hi:[1,0]
	v_pk_mul_f32 v[96:97], v[96:97], s[16:17] op_sel_hi:[1,0]
	v_pk_mul_f32 v[94:95], v[94:95], s[16:17] op_sel_hi:[1,0]
	v_pk_mul_f32 v[92:93], v[92:93], s[16:17] op_sel_hi:[1,0]
	v_pk_mul_f32 v[90:91], v[90:91], s[16:17] op_sel_hi:[1,0]
	v_pk_mul_f32 v[114:115], v[80:81], s[16:17] op_sel_hi:[1,0]
	v_pk_mul_f32 v[116:117], v[78:79], s[16:17] op_sel_hi:[1,0]
	v_pk_mul_f32 v[122:123], v[72:73], s[16:17] op_sel_hi:[1,0]
	v_pk_mul_f32 v[124:125], v[70:71], s[16:17] op_sel_hi:[1,0]
	v_pk_mul_f32 v[70:71], v[88:89], s[16:17] op_sel_hi:[1,0]
	v_pk_mul_f32 v[72:73], v[86:87], s[16:17] op_sel_hi:[1,0]
	v_pk_mul_f32 v[78:79], v[84:85], s[16:17] op_sel_hi:[1,0]
	v_pk_mul_f32 v[80:81], v[82:83], s[16:17] op_sel_hi:[1,0]
	v_pk_mul_f32 v[82:83], v[64:65], s[16:17] op_sel_hi:[1,0]
	v_pk_mul_f32 v[84:85], v[62:63], s[16:17] op_sel_hi:[1,0]
	v_pk_mul_f32 v[86:87], v[56:57], s[16:17] op_sel_hi:[1,0]
	v_pk_mul_f32 v[88:89], v[54:55], s[16:17] op_sel_hi:[1,0]
	v_pk_mul_f32 v[54:55], v[76:77], s[16:17] op_sel_hi:[1,0]
	v_pk_mul_f32 v[56:57], v[74:75], s[16:17] op_sel_hi:[1,0]
	v_pk_mul_f32 v[62:63], v[68:69], s[16:17] op_sel_hi:[1,0]
	v_pk_mul_f32 v[64:65], v[66:67], s[16:17] op_sel_hi:[1,0]
	v_pk_mul_f32 v[66:67], v[48:49], s[16:17] op_sel_hi:[1,0]
	v_pk_mul_f32 v[68:69], v[46:47], s[16:17] op_sel_hi:[1,0]
	v_pk_mul_f32 v[74:75], v[44:45], s[16:17] op_sel_hi:[1,0]
	v_pk_mul_f32 v[76:77], v[42:43], s[16:17] op_sel_hi:[1,0]
	v_pk_mul_f32 v[42:43], v[60:61], s[16:17] op_sel_hi:[1,0]
	v_pk_mul_f32 v[44:45], v[58:59], s[16:17] op_sel_hi:[1,0]
	v_pk_mul_f32 v[46:47], v[52:53], s[16:17] op_sel_hi:[1,0]
	v_pk_mul_f32 v[48:49], v[50:51], s[16:17] op_sel_hi:[1,0]
	v_pk_mul_f32 v[40:41], v[40:41], s[16:17] op_sel_hi:[1,0]
	v_pk_mul_f32 v[38:39], v[38:39], s[16:17] op_sel_hi:[1,0]
	v_pk_mul_f32 v[36:37], v[36:37], s[16:17] op_sel_hi:[1,0]
	v_pk_mul_f32 v[34:35], v[34:35], s[16:17] op_sel_hi:[1,0]

.LBB0_3015:
	s_setprio 0
	s_cmp_lt_i32 s41, 26
	s_cbranch_scc1 .LBB0_3065
	s_waitcnt vmcnt(0)
	v_cmp_eq_u32_e32 vcc, 0, v0
	s_waitcnt vmcnt(0) lgkmcnt(0)
	s_barrier
	s_and_saveexec_b64 s[2:3], vcc
	s_cbranch_execz .LBB0_3064
	v_mov_b32_e32 v0, s92
	s_waitcnt vmcnt(0) expcnt(0) lgkmcnt(0)
	ds_read_b32 v2, v0
	ds_read_b32 v0, v0 offset:4
	s_waitcnt lgkmcnt(1)
	v_cmp_ne_u32_e32 vcc, 0, v2
	s_cbranch_vccnz .LBB0_3032
	v_readlane_b32 s4, v254, 1
	v_readlane_b32 s5, v254, 2
	s_load_dwordx2 s[8:9], s[4:5], 0x4
	s_add_u32 s4, s42, 0x1000
	s_addc_u32 s5, s43, 0
	s_add_u32 s6, s42, 0x1100
	s_addc_u32 s7, s43, 0
	s_waitcnt lgkmcnt(0)
	s_mul_i32 s18, s8, s34
	s_add_u32 s8, s42, 0x1200
	s_mul_i32 s18, s18, s9
	s_addc_u32 s9, s43, 0
	s_add_u32 s10, s42, 0x1300
	s_addc_u32 s11, s43, 0
	s_mov_b32 s19, 1
	v_mov_b32_e32 v16, 0
	s_branch .LBB0_3020
